# fp8 MFMA: v_mfma_scale_f32_16x16x128_f8f6f4 with both E8M0 scales = 1.0 replaced by the unscaled v_mfma_f32_16x16x128_f8f6f4 (same e4m3 operands, f32 accumulate; drops the ld_scale half of each 16-byt
# speedup vs baseline: 1.0042x; 1.0042x over previous
.LBB0_374:
	v_mov_b64_e32 v[2:3], 0x800
	s_ashr_i32 s45, s44, 31
	v_cmp_lt_i64_e32 vcc, s[10:11], v[2:3]
	s_lshl_b64 s[10:11], s[44:45], 18
	s_add_u32 s48, s27, s10
	s_addc_u32 s49, s60, s11
	s_and_b64 s[10:11], vcc, exec
	ds_read_b128 v[2:5], v165
	ds_read_b128 v[6:9], v166
	ds_read_b128 v[10:13], v167
	ds_read_b128 v[14:17], v168
	s_cselect_b32 s12, s49, s9
	s_cselect_b32 s13, s48, s8
	s_ashr_i32 s43, s42, 31
	s_lshl_b64 s[10:11], s[42:43], 18
	s_add_u32 s50, s62, s10
	s_addc_u32 s51, s63, s11
	s_and_b64 s[10:11], vcc, exec
	s_cselect_b32 s28, s51, s7
	s_cselect_b32 s43, s50, s6
	s_add_u32 s10, s8, 0x20080
	s_addc_u32 s11, s9, 0
	s_add_i32 s45, s64, 0xc000
	v_add_u32_e32 v181, s72, v164
	v_lshl_add_u64 v[50:51], s[10:11], 0, v[150:151]
	s_mov_b32 m0, s45
	s_add_i32 s47, s64, 0xe000
	ds_read_b128 v[18:21], v181
	ds_read_b128 v[22:25], v181 offset:1024
	ds_read_b128 v[26:29], v181 offset:2048
	ds_read_b128 v[30:33], v181 offset:3072
	ds_read_b128 v[34:37], v181 offset:4096
	ds_read_b128 v[38:41], v181 offset:5120
	ds_read_b128 v[42:45], v181 offset:6144
	ds_read_b128 v[46:49], v181 offset:7168
	global_load_lds_dwordx4 v[50:51], off
	v_lshl_add_u64 v[50:51], s[10:11], 0, v[148:149]
	s_mov_b32 m0, s47
	s_nop 0
	global_load_lds_dwordx4 v[50:51], off
	s_waitcnt lgkmcnt(8)
	s_barrier
	s_waitcnt lgkmcnt(0)
	s_setprio 1
	s_waitcnt lgkmcnt(0)
	v_mfma_f32_16x16x128_f8f6f4 v[142:145], v[2:9], v[18:25], 0
	v_mfma_f32_16x16x128_f8f6f4 v[138:141], v[10:17], v[18:25], 0
	v_mfma_f32_16x16x128_f8f6f4 v[126:129], v[2:9], v[26:33], 0
	v_mfma_f32_16x16x128_f8f6f4 v[122:125], v[10:17], v[26:33], 0
	v_mfma_f32_16x16x128_f8f6f4 v[110:113], v[2:9], v[34:41], 0
	v_mfma_f32_16x16x128_f8f6f4 v[106:109], v[10:17], v[34:41], 0
	v_mfma_f32_16x16x128_f8f6f4 v[94:97], v[2:9], v[42:49], 0
	v_mfma_f32_16x16x128_f8f6f4 v[90:93], v[10:17], v[42:49], 0
	s_setprio 0
	s_barrier
	v_lshl_add_u64 v[160:161], s[6:7], 0, v[0:1]
	s_mov_b64 s[10:11], 0x100
	s_mov_b32 m0, s65
	v_lshl_add_u64 v[50:51], v[160:161], 0, s[10:11]
	v_lshl_add_u64 v[162:163], s[6:7], 0, v[146:147]
	ds_read_b128 v[188:191], v169
	ds_read_b128 v[192:195], v170
	ds_read_b128 v[196:199], v171
	ds_read_b128 v[200:203], v172
	global_load_lds_dwordx4 v[50:51], off
	v_lshl_add_u64 v[50:51], v[162:163], 0, s[10:11]
	s_mov_b32 m0, s66
	s_nop 0
	global_load_lds_dwordx4 v[50:51], off
	s_barrier
	s_waitcnt lgkmcnt(0)
	s_setprio 1
	s_waitcnt lgkmcnt(0)
	v_mfma_f32_16x16x128_f8f6f4 v[134:137], v[188:195], v[18:25], 0
	v_mfma_f32_16x16x128_f8f6f4 v[130:133], v[196:203], v[18:25], 0
	v_mfma_f32_16x16x128_f8f6f4 v[118:121], v[188:195], v[26:33], 0
	v_mfma_f32_16x16x128_f8f6f4 v[114:117], v[196:203], v[26:33], 0
	v_mfma_f32_16x16x128_f8f6f4 v[102:105], v[188:195], v[34:41], 0
	v_mfma_f32_16x16x128_f8f6f4 v[98:101], v[196:203], v[34:41], 0
	v_mfma_f32_16x16x128_f8f6f4 v[86:89], v[188:195], v[42:49], 0
	v_mfma_f32_16x16x128_f8f6f4 v[82:85], v[196:203], v[42:49], 0
	s_setprio 0
	v_lshl_add_u64 v[156:157], s[8:9], 0, v[150:151]
	s_mov_b32 m0, s64
	v_lshl_add_u64 v[26:27], v[156:157], 0, s[10:11]
	v_lshl_add_u64 v[158:159], s[8:9], 0, v[148:149]
	s_barrier
	ds_read_b128 v[18:21], v181 offset:16384
	ds_read_b128 v[22:25], v181 offset:17408
	ds_read_b128 v[34:37], v181 offset:18432
	ds_read_b128 v[38:41], v181 offset:19456
	ds_read_b128 v[204:207], v181 offset:20480
	ds_read_b128 v[208:211], v181 offset:21504
	ds_read_b128 v[212:215], v181 offset:22528
	ds_read_b128 v[216:219], v181 offset:23552
	global_load_lds_dwordx4 v[26:27], off
	v_lshl_add_u64 v[26:27], v[158:159], 0, s[10:11]
	s_mov_b32 m0, s67
	s_nop 0
	global_load_lds_dwordx4 v[26:27], off
	s_barrier
	s_waitcnt lgkmcnt(0)
	s_setprio 1
	s_waitcnt lgkmcnt(0)
	v_mfma_f32_16x16x128_f8f6f4 v[78:81], v[2:9], v[18:25], 0
	v_mfma_f32_16x16x128_f8f6f4 v[74:77], v[10:17], v[18:25], 0
	v_mfma_f32_16x16x128_f8f6f4 v[62:65], v[2:9], v[34:41], 0
	v_mfma_f32_16x16x128_f8f6f4 v[58:61], v[10:17], v[34:41], 0
	v_mfma_f32_16x16x128_f8f6f4 v[46:49], v[2:9], v[204:211], 0
	v_mfma_f32_16x16x128_f8f6f4 v[42:45], v[10:17], v[204:211], 0
	v_mfma_f32_16x16x128_f8f6f4 v[30:33], v[2:9], v[212:219], 0
	v_mfma_f32_16x16x128_f8f6f4 v[26:29], v[10:17], v[212:219], 0
	s_setprio 0
	s_barrier
	s_add_u32 s10, s6, 0x20100
	s_addc_u32 s11, s7, 0
	s_mov_b32 m0, s68
	v_lshl_add_u64 v[2:3], s[10:11], 0, v[0:1]
	global_load_lds_dwordx4 v[2:3], off
	v_lshl_add_u64 v[2:3], s[10:11], 0, v[146:147]
	s_mov_b32 m0, s69
	s_nop 0
	global_load_lds_dwordx4 v[2:3], off
	s_waitcnt vmcnt(6)
	s_barrier
	s_setprio 1
	v_mfma_f32_16x16x128_f8f6f4 v[70:73], v[188:195], v[18:25], 0
	v_mfma_f32_16x16x128_f8f6f4 v[66:69], v[196:203], v[18:25], 0
	v_mfma_f32_16x16x128_f8f6f4 v[54:57], v[188:195], v[34:41], 0
	v_mfma_f32_16x16x128_f8f6f4 v[50:53], v[196:203], v[34:41], 0
	v_mfma_f32_16x16x128_f8f6f4 v[38:41], v[188:195], v[204:211], 0
	v_mfma_f32_16x16x128_f8f6f4 v[34:37], v[196:203], v[204:211], 0
	v_mfma_f32_16x16x128_f8f6f4 v[22:25], v[188:195], v[212:219], 0
	v_mfma_f32_16x16x128_f8f6f4 v[18:21], v[196:203], v[212:219], 0
	s_setprio 0
	s_barrier
	ds_read_b128 v[2:5], v173
	ds_read_b128 v[6:9], v174
	ds_read_b128 v[10:13], v175
	ds_read_b128 v[14:17], v176
	s_add_u32 s10, s8, 0x20100
	s_addc_u32 s11, s9, 0
	s_mov_b32 m0, s70
	v_lshl_add_u64 v[182:183], s[10:11], 0, v[150:151]
	ds_read_b128 v[188:191], v181 offset:32768
	ds_read_b128 v[192:195], v181 offset:33792
	ds_read_b128 v[196:199], v181 offset:34816
	ds_read_b128 v[200:203], v181 offset:35840
	ds_read_b128 v[204:207], v181 offset:36864
	ds_read_b128 v[208:211], v181 offset:37888
	ds_read_b128 v[212:215], v181 offset:38912
	ds_read_b128 v[216:219], v181 offset:39936
	global_load_lds_dwordx4 v[182:183], off
	v_lshl_add_u64 v[182:183], s[10:11], 0, v[148:149]
	s_mov_b32 m0, s71
	s_nop 0
	global_load_lds_dwordx4 v[182:183], off
	s_waitcnt lgkmcnt(8)
	s_barrier
	s_waitcnt lgkmcnt(0)
	s_setprio 1
	s_waitcnt lgkmcnt(0)
	v_mfma_f32_16x16x128_f8f6f4 v[142:145], v[2:9], v[188:195], v[142:145]
	v_mfma_f32_16x16x128_f8f6f4 v[138:141], v[10:17], v[188:195], v[138:141]
	v_mfma_f32_16x16x128_f8f6f4 v[126:129], v[2:9], v[196:203], v[126:129]
	v_mfma_f32_16x16x128_f8f6f4 v[122:125], v[10:17], v[196:203], v[122:125]
	v_mfma_f32_16x16x128_f8f6f4 v[110:113], v[2:9], v[204:211], v[110:113]
	v_mfma_f32_16x16x128_f8f6f4 v[106:109], v[10:17], v[204:211], v[106:109]
	v_mfma_f32_16x16x128_f8f6f4 v[94:97], v[2:9], v[212:219], v[94:97]
	v_mfma_f32_16x16x128_f8f6f4 v[90:93], v[10:17], v[212:219], v[90:93]
	s_setprio 0
	s_barrier
	s_mov_b64 s[10:11], 0x180
	s_mov_b32 m0, s73
	v_lshl_add_u64 v[160:161], v[160:161], 0, s[10:11]
	ds_read_b128 v[232:235], v177
	ds_read_b128 v[236:239], v178
	ds_read_b128 v[240:243], v179
	ds_read_b128 v[244:247], v180
	global_load_lds_dwordx4 v[160:161], off
	v_lshl_add_u64 v[160:161], v[162:163], 0, s[10:11]
	s_mov_b32 m0, s74
	s_nop 0
	global_load_lds_dwordx4 v[160:161], off
	s_barrier
	s_waitcnt lgkmcnt(0)
	s_setprio 1
	s_waitcnt lgkmcnt(0)
	v_mfma_f32_16x16x128_f8f6f4 v[134:137], v[232:239], v[188:195], v[134:137]
	v_mfma_f32_16x16x128_f8f6f4 v[130:133], v[240:247], v[188:195], v[130:133]
	v_mfma_f32_16x16x128_f8f6f4 v[118:121], v[232:239], v[196:203], v[118:121]
	v_mfma_f32_16x16x128_f8f6f4 v[114:117], v[240:247], v[196:203], v[114:117]
	v_mfma_f32_16x16x128_f8f6f4 v[102:105], v[232:239], v[204:211], v[102:105]
	v_mfma_f32_16x16x128_f8f6f4 v[98:101], v[240:247], v[204:211], v[98:101]
	v_mfma_f32_16x16x128_f8f6f4 v[86:89], v[232:239], v[212:219], v[86:89]
	v_mfma_f32_16x16x128_f8f6f4 v[82:85], v[240:247], v[212:219], v[82:85]
	s_setprio 0
	s_mov_b32 m0, s75
	v_lshl_add_u64 v[156:157], v[156:157], 0, s[10:11]
	s_barrier
	ds_read_b128 v[188:191], v181 offset:49152
	ds_read_b128 v[192:195], v181 offset:50176
	ds_read_b128 v[196:199], v181 offset:51200
	ds_read_b128 v[200:203], v181 offset:52224
	ds_read_b128 v[204:207], v181 offset:53248
	ds_read_b128 v[208:211], v181 offset:54272
	ds_read_b128 v[212:215], v181 offset:55296
	ds_read_b128 v[216:219], v181 offset:56320
	global_load_lds_dwordx4 v[156:157], off
	v_lshl_add_u64 v[156:157], v[158:159], 0, s[10:11]
	s_mov_b32 m0, s76
	s_nop 0
	global_load_lds_dwordx4 v[156:157], off
	s_barrier
	s_waitcnt lgkmcnt(0)
	s_setprio 1
	s_waitcnt lgkmcnt(0)
	v_mfma_f32_16x16x128_f8f6f4 v[78:81], v[2:9], v[188:195], v[78:81]
	v_mfma_f32_16x16x128_f8f6f4 v[74:77], v[10:17], v[188:195], v[74:77]
	v_mfma_f32_16x16x128_f8f6f4 v[62:65], v[2:9], v[196:203], v[62:65]
	v_mfma_f32_16x16x128_f8f6f4 v[58:61], v[10:17], v[196:203], v[58:61]
	v_mfma_f32_16x16x128_f8f6f4 v[46:49], v[2:9], v[204:211], v[46:49]
	v_mfma_f32_16x16x128_f8f6f4 v[42:45], v[10:17], v[204:211], v[42:45]
	v_mfma_f32_16x16x128_f8f6f4 v[30:33], v[2:9], v[212:219], v[30:33]
	v_mfma_f32_16x16x128_f8f6f4 v[26:29], v[10:17], v[212:219], v[26:29]
	s_setprio 0
	s_barrier
	s_add_u32 s10, s6, 0x20180
	s_addc_u32 s11, s7, 0
	s_mov_b32 m0, s77
	v_lshl_add_u64 v[2:3], s[10:11], 0, v[0:1]
	global_load_lds_dwordx4 v[2:3], off
	v_lshl_add_u64 v[2:3], s[10:11], 0, v[146:147]
	s_mov_b32 m0, s78
	s_nop 0
	global_load_lds_dwordx4 v[2:3], off
	s_waitcnt vmcnt(6)
	s_barrier
	s_setprio 1
	v_mfma_f32_16x16x128_f8f6f4 v[70:73], v[232:239], v[188:195], v[70:73]
	v_mfma_f32_16x16x128_f8f6f4 v[66:69], v[240:247], v[188:195], v[66:69]
	v_mfma_f32_16x16x128_f8f6f4 v[54:57], v[232:239], v[196:203], v[54:57]
	v_mfma_f32_16x16x128_f8f6f4 v[50:53], v[240:247], v[196:203], v[50:53]
	v_mfma_f32_16x16x128_f8f6f4 v[38:41], v[232:239], v[204:211], v[38:41]
	v_mfma_f32_16x16x128_f8f6f4 v[34:37], v[240:247], v[204:211], v[34:37]
	v_mfma_f32_16x16x128_f8f6f4 v[22:25], v[232:239], v[212:219], v[22:25]
	v_mfma_f32_16x16x128_f8f6f4 v[18:21], v[240:247], v[212:219], v[18:21]
	s_setprio 0
	s_add_u32 s8, s8, 0x20180
	s_addc_u32 s9, s9, 0
	s_add_u32 s52, s6, 0x200
	s_addc_u32 s53, s7, 0
	s_mov_b32 s54, 0
	s_barrier
.LBB0_375:
	ds_read_b128 v[10:13], v165
	ds_read_b128 v[14:17], v166
	ds_read_b128 v[156:159], v167
	ds_read_b128 v[160:163], v168
	s_add_u32 s6, s8, 0xfffe0080
	s_addc_u32 s7, s9, -1
	s_cmp_eq_u32 s54, 4
	s_cselect_b32 s11, s12, s7
	s_cselect_b32 s10, s13, s6
	s_cselect_b32 s7, s28, s53
	s_cselect_b32 s6, s43, s52
	s_mov_b32 m0, s45
	v_lshl_add_u64 v[2:3], s[8:9], 0, v[152:153]
	ds_read_b128 v[188:191], v181
	ds_read_b128 v[192:195], v181 offset:1024
	ds_read_b128 v[196:199], v181 offset:2048
	ds_read_b128 v[200:203], v181 offset:3072
	ds_read_b128 v[204:207], v181 offset:4096
	ds_read_b128 v[208:211], v181 offset:5120
	ds_read_b128 v[212:215], v181 offset:6144
	ds_read_b128 v[216:219], v181 offset:7168
	global_load_lds_dwordx4 v[2:3], off
	v_lshl_add_u64 v[2:3], s[8:9], 0, v[154:155]
	s_mov_b32 m0, s47
	s_nop 0
	global_load_lds_dwordx4 v[2:3], off
	s_waitcnt lgkmcnt(8)
	s_barrier
	s_waitcnt lgkmcnt(0)
	s_setprio 1
	s_waitcnt lgkmcnt(0)
	v_mfma_f32_16x16x128_f8f6f4 v[142:145], v[10:17], v[188:195], v[142:145]
	v_mfma_f32_16x16x128_f8f6f4 v[138:141], v[156:163], v[188:195], v[138:141]
	v_mfma_f32_16x16x128_f8f6f4 v[126:129], v[10:17], v[196:203], v[126:129]
	v_mfma_f32_16x16x128_f8f6f4 v[122:125], v[156:163], v[196:203], v[122:125]
	v_mfma_f32_16x16x128_f8f6f4 v[110:113], v[10:17], v[204:211], v[110:113]
	v_mfma_f32_16x16x128_f8f6f4 v[106:109], v[156:163], v[204:211], v[106:109]
	v_mfma_f32_16x16x128_f8f6f4 v[94:97], v[10:17], v[212:219], v[94:97]
	v_mfma_f32_16x16x128_f8f6f4 v[90:93], v[156:163], v[212:219], v[90:93]
	s_setprio 0
	s_barrier
	s_mov_b32 m0, s65
	v_lshl_add_u64 v[6:7], s[6:7], 0, v[0:1]
	ds_read_b128 v[232:235], v169
	ds_read_b128 v[236:239], v170
	ds_read_b128 v[240:243], v171
	ds_read_b128 v[244:247], v172
	global_load_lds_dwordx4 v[6:7], off
	v_lshl_add_u64 v[8:9], s[6:7], 0, v[146:147]
	s_mov_b32 m0, s66
	s_nop 0
	global_load_lds_dwordx4 v[8:9], off
	s_barrier
	s_waitcnt lgkmcnt(0)
	s_setprio 1
	s_waitcnt lgkmcnt(0)
	v_mfma_f32_16x16x128_f8f6f4 v[134:137], v[232:239], v[188:195], v[134:137]
	v_mfma_f32_16x16x128_f8f6f4 v[130:133], v[240:247], v[188:195], v[130:133]
	v_mfma_f32_16x16x128_f8f6f4 v[118:121], v[232:239], v[196:203], v[118:121]
	v_mfma_f32_16x16x128_f8f6f4 v[114:117], v[240:247], v[196:203], v[114:117]
	v_mfma_f32_16x16x128_f8f6f4 v[102:105], v[232:239], v[204:211], v[102:105]
	v_mfma_f32_16x16x128_f8f6f4 v[98:101], v[240:247], v[204:211], v[98:101]
	v_mfma_f32_16x16x128_f8f6f4 v[86:89], v[232:239], v[212:219], v[86:89]
	v_mfma_f32_16x16x128_f8f6f4 v[82:85], v[240:247], v[212:219], v[82:85]
	s_setprio 0
	s_mov_b32 m0, s64
	v_lshl_add_u64 v[2:3], s[10:11], 0, v[150:151]
	s_barrier
	ds_read_b128 v[188:191], v181 offset:16384
	ds_read_b128 v[192:195], v181 offset:17408
	ds_read_b128 v[196:199], v181 offset:18432
	ds_read_b128 v[200:203], v181 offset:19456
	ds_read_b128 v[204:207], v181 offset:20480
	ds_read_b128 v[208:211], v181 offset:21504
	ds_read_b128 v[212:215], v181 offset:22528
	ds_read_b128 v[216:219], v181 offset:23552
	global_load_lds_dwordx4 v[2:3], off
	v_lshl_add_u64 v[4:5], s[10:11], 0, v[148:149]
	s_mov_b32 m0, s67
	s_nop 0
	global_load_lds_dwordx4 v[4:5], off
	s_barrier
	s_waitcnt lgkmcnt(0)
	s_setprio 1
	s_waitcnt lgkmcnt(0)
	v_mfma_f32_16x16x128_f8f6f4 v[78:81], v[10:17], v[188:195], v[78:81]
	v_mfma_f32_16x16x128_f8f6f4 v[74:77], v[156:163], v[188:195], v[74:77]
	v_mfma_f32_16x16x128_f8f6f4 v[62:65], v[10:17], v[196:203], v[62:65]
	v_mfma_f32_16x16x128_f8f6f4 v[58:61], v[156:163], v[196:203], v[58:61]
	v_mfma_f32_16x16x128_f8f6f4 v[46:49], v[10:17], v[204:211], v[46:49]
	v_mfma_f32_16x16x128_f8f6f4 v[42:45], v[156:163], v[204:211], v[42:45]
	v_mfma_f32_16x16x128_f8f6f4 v[30:33], v[10:17], v[212:219], v[30:33]
	v_mfma_f32_16x16x128_f8f6f4 v[26:29], v[156:163], v[212:219], v[26:29]
	s_setprio 0
	s_barrier
	s_add_u32 s56, s6, 0x20000
	s_addc_u32 s57, s7, 0
	s_mov_b32 m0, s68
	v_lshl_add_u64 v[10:11], s[56:57], 0, v[0:1]
	global_load_lds_dwordx4 v[10:11], off
	v_lshl_add_u64 v[10:11], s[56:57], 0, v[146:147]
	s_mov_b32 m0, s69
	s_nop 0
	global_load_lds_dwordx4 v[10:11], off
	s_waitcnt vmcnt(6)
	s_barrier
	s_setprio 1
	v_mfma_f32_16x16x128_f8f6f4 v[70:73], v[232:239], v[188:195], v[70:73]
	v_mfma_f32_16x16x128_f8f6f4 v[66:69], v[240:247], v[188:195], v[66:69]
	v_mfma_f32_16x16x128_f8f6f4 v[54:57], v[232:239], v[196:203], v[54:57]
	v_mfma_f32_16x16x128_f8f6f4 v[50:53], v[240:247], v[196:203], v[50:53]
	v_mfma_f32_16x16x128_f8f6f4 v[38:41], v[232:239], v[204:211], v[38:41]
	v_mfma_f32_16x16x128_f8f6f4 v[34:37], v[240:247], v[204:211], v[34:37]
	v_mfma_f32_16x16x128_f8f6f4 v[22:25], v[232:239], v[212:219], v[22:25]
	v_mfma_f32_16x16x128_f8f6f4 v[18:21], v[240:247], v[212:219], v[18:21]
	s_setprio 0
	s_barrier
	ds_read_b128 v[10:13], v173
	ds_read_b128 v[14:17], v174
	ds_read_b128 v[156:159], v175
	ds_read_b128 v[160:163], v176
	s_add_u32 s10, s10, 0x20000
	s_addc_u32 s11, s11, 0
	s_mov_b32 m0, s70
	v_lshl_add_u64 v[182:183], s[10:11], 0, v[150:151]
	ds_read_b128 v[188:191], v181 offset:32768
	ds_read_b128 v[192:195], v181 offset:33792
	ds_read_b128 v[196:199], v181 offset:34816
	ds_read_b128 v[200:203], v181 offset:35840
	ds_read_b128 v[204:207], v181 offset:36864
	ds_read_b128 v[208:211], v181 offset:37888
	ds_read_b128 v[212:215], v181 offset:38912
	ds_read_b128 v[216:219], v181 offset:39936
	global_load_lds_dwordx4 v[182:183], off
	v_lshl_add_u64 v[182:183], s[10:11], 0, v[148:149]
	s_mov_b32 m0, s71
	s_nop 0
	global_load_lds_dwordx4 v[182:183], off
	s_waitcnt lgkmcnt(8)
	s_barrier
	s_waitcnt lgkmcnt(0)
	s_setprio 1
	s_waitcnt lgkmcnt(0)
	v_mfma_f32_16x16x128_f8f6f4 v[142:145], v[10:17], v[188:195], v[142:145]
	v_mfma_f32_16x16x128_f8f6f4 v[138:141], v[156:163], v[188:195], v[138:141]
	v_mfma_f32_16x16x128_f8f6f4 v[126:129], v[10:17], v[196:203], v[126:129]
	v_mfma_f32_16x16x128_f8f6f4 v[122:125], v[156:163], v[196:203], v[122:125]
	v_mfma_f32_16x16x128_f8f6f4 v[110:113], v[10:17], v[204:211], v[110:113]
	v_mfma_f32_16x16x128_f8f6f4 v[106:109], v[156:163], v[204:211], v[106:109]
	v_mfma_f32_16x16x128_f8f6f4 v[94:97], v[10:17], v[212:219], v[94:97]
	v_mfma_f32_16x16x128_f8f6f4 v[90:93], v[156:163], v[212:219], v[90:93]
	s_setprio 0
	s_barrier
	s_mov_b32 m0, s73
	v_lshl_add_u64 v[6:7], v[6:7], 0, s[24:25]
	ds_read_b128 v[232:235], v177
	ds_read_b128 v[236:239], v178
	ds_read_b128 v[240:243], v179
	ds_read_b128 v[244:247], v180
	global_load_lds_dwordx4 v[6:7], off
	v_lshl_add_u64 v[6:7], v[8:9], 0, s[24:25]
	s_mov_b32 m0, s74
	s_nop 0
	global_load_lds_dwordx4 v[6:7], off
	s_barrier
	s_waitcnt lgkmcnt(0)
	s_setprio 1
	s_waitcnt lgkmcnt(0)
	v_mfma_f32_16x16x128_f8f6f4 v[134:137], v[232:239], v[188:195], v[134:137]
	v_mfma_f32_16x16x128_f8f6f4 v[130:133], v[240:247], v[188:195], v[130:133]
	v_mfma_f32_16x16x128_f8f6f4 v[118:121], v[232:239], v[196:203], v[118:121]
	v_mfma_f32_16x16x128_f8f6f4 v[114:117], v[240:247], v[196:203], v[114:117]
	v_mfma_f32_16x16x128_f8f6f4 v[102:105], v[232:239], v[204:211], v[102:105]
	v_mfma_f32_16x16x128_f8f6f4 v[98:101], v[240:247], v[204:211], v[98:101]
	v_mfma_f32_16x16x128_f8f6f4 v[86:89], v[232:239], v[212:219], v[86:89]
	v_mfma_f32_16x16x128_f8f6f4 v[82:85], v[240:247], v[212:219], v[82:85]
	s_setprio 0
	s_mov_b32 m0, s75
	v_lshl_add_u64 v[2:3], v[2:3], 0, s[24:25]
	s_barrier
	ds_read_b128 v[188:191], v181 offset:49152
	ds_read_b128 v[192:195], v181 offset:50176
	ds_read_b128 v[196:199], v181 offset:51200
	ds_read_b128 v[200:203], v181 offset:52224
	ds_read_b128 v[204:207], v181 offset:53248
	ds_read_b128 v[208:211], v181 offset:54272
	ds_read_b128 v[212:215], v181 offset:55296
	ds_read_b128 v[216:219], v181 offset:56320
	global_load_lds_dwordx4 v[2:3], off
	v_lshl_add_u64 v[2:3], v[4:5], 0, s[24:25]
	s_mov_b32 m0, s76
	s_nop 0
	global_load_lds_dwordx4 v[2:3], off
	s_barrier
	s_waitcnt lgkmcnt(0)
	s_setprio 1
	s_waitcnt lgkmcnt(0)
	v_mfma_f32_16x16x128_f8f6f4 v[78:81], v[10:17], v[188:195], v[78:81]
	v_mfma_f32_16x16x128_f8f6f4 v[74:77], v[156:163], v[188:195], v[74:77]
	v_mfma_f32_16x16x128_f8f6f4 v[62:65], v[10:17], v[196:203], v[62:65]
	v_mfma_f32_16x16x128_f8f6f4 v[58:61], v[156:163], v[196:203], v[58:61]
	v_mfma_f32_16x16x128_f8f6f4 v[46:49], v[10:17], v[204:211], v[46:49]
	v_mfma_f32_16x16x128_f8f6f4 v[42:45], v[156:163], v[204:211], v[42:45]
	v_mfma_f32_16x16x128_f8f6f4 v[30:33], v[10:17], v[212:219], v[30:33]
	v_mfma_f32_16x16x128_f8f6f4 v[26:29], v[156:163], v[212:219], v[26:29]
	s_setprio 0
	s_barrier
	s_add_u32 s6, s6, 0x20080
	s_addc_u32 s7, s7, 0
	s_mov_b32 m0, s77
	v_lshl_add_u64 v[2:3], s[6:7], 0, v[0:1]
	global_load_lds_dwordx4 v[2:3], off
	v_lshl_add_u64 v[2:3], s[6:7], 0, v[146:147]
	s_mov_b32 m0, s78
	s_nop 0
	global_load_lds_dwordx4 v[2:3], off
	s_waitcnt vmcnt(6)
	s_barrier
	s_setprio 1
	v_mfma_f32_16x16x128_f8f6f4 v[70:73], v[232:239], v[188:195], v[70:73]
	v_mfma_f32_16x16x128_f8f6f4 v[66:69], v[240:247], v[188:195], v[66:69]
	v_mfma_f32_16x16x128_f8f6f4 v[54:57], v[232:239], v[196:203], v[54:57]
	v_mfma_f32_16x16x128_f8f6f4 v[50:53], v[240:247], v[196:203], v[50:53]
	v_mfma_f32_16x16x128_f8f6f4 v[38:41], v[232:239], v[204:211], v[38:41]
	v_mfma_f32_16x16x128_f8f6f4 v[34:37], v[240:247], v[204:211], v[34:37]
	v_mfma_f32_16x16x128_f8f6f4 v[22:25], v[232:239], v[212:219], v[22:25]
	v_mfma_f32_16x16x128_f8f6f4 v[18:21], v[240:247], v[212:219], v[18:21]
	s_setprio 0
	s_add_i32 s54, s54, 2
	s_add_u32 s8, s8, 0x100
	s_addc_u32 s9, s9, 0
	s_add_u32 s52, s52, 0x100
	s_addc_u32 s53, s53, 0
	s_cmp_gt_u32 s54, 5
	s_barrier
	s_cbranch_scc0 .LBB0_375
	s_and_b32 s43, s82, 3
	s_cmp_lt_i32 s82, 4
	s_cselect_b64 s[6:7], -1, 0
	s_cmp_gt_i32 s82, 3
	s_nop 15
	s_nop 15
	v_mbcnt_lo_u32_b32 v2, -1, 0
	v_mbcnt_hi_u32_b32 v2, -1, v2
	s_cselect_b64 s[58:59], -1, 0
	s_cmp_lt_i32 s82, 8
	s_cselect_b64 s[8:9], -1, 0
	s_cmp_gt_i32 s82, 7
	v_readlane_b32 s47, v252, 51
	v_readlane_b32 s45, v252, 52
	s_cselect_b64 s[12:13], -1, 0
	s_mov_b64 s[10:11], -1
	s_and_b64 vcc, exec, s[58:59]
	s_cbranch_vccz .LBB0_382
	s_and_b64 vcc, exec, s[12:13]
	s_cbranch_vccz .LBB0_379
	s_lshl_b32 s10, s82, 8
	s_add_i32 s28, s10, 0xfffff800
	s_mov_b64 s[10:11], 0

.LBB0_525:
	s_ashr_i32 s9, s8, 31
	v_cmp_lt_i64_e32 vcc, s[10:11], v[248:249]
	s_lshl_b64 s[10:11], s[8:9], 18
	s_add_u32 s10, s44, s10
	s_addc_u32 s11, s45, s11
	s_and_b64 s[12:13], vcc, exec
	ds_read_b128 v[2:5], v165
	ds_read_b128 v[6:9], v166
	ds_read_b128 v[10:13], v167
	ds_read_b128 v[14:17], v168
	s_cselect_b32 s9, s11, s43
	s_cselect_b32 s67, s10, s42
	s_ashr_i32 s7, s6, 31
	s_lshl_b64 s[12:13], s[6:7], 18
	s_add_u32 s12, s27, s12
	s_addc_u32 s13, s60, s13
	s_and_b64 s[20:21], vcc, exec
	s_cselect_b32 s7, s13, s35
	s_cselect_b32 s68, s12, s34
	s_add_u32 s20, s42, 0x20080
	s_addc_u32 s21, s43, 0
	s_add_i32 s69, s46, 0xc000
	v_add_u32_e32 v181, s54, v164
	v_lshl_add_u64 v[42:43], s[20:21], 0, v[150:151]
	s_mov_b32 m0, s69
	s_add_i32 s70, s46, 0xe000
	ds_read_b128 v[18:21], v181
	ds_read_b128 v[22:25], v181 offset:1024
	ds_read_b128 v[26:29], v181 offset:2048
	ds_read_b128 v[30:33], v181 offset:3072
	ds_read_b128 v[34:37], v181 offset:4096
	ds_read_b128 v[38:41], v181 offset:5120
	ds_read_b128 v[50:53], v181 offset:6144
	ds_read_b128 v[54:57], v181 offset:7168
	global_load_lds_dwordx4 v[42:43], off
	v_lshl_add_u64 v[42:43], s[20:21], 0, v[148:149]
	s_mov_b32 m0, s70
	s_nop 0
	global_load_lds_dwordx4 v[42:43], off
	s_waitcnt lgkmcnt(8)
	s_barrier
	s_waitcnt lgkmcnt(0)
	s_setprio 1
	s_waitcnt lgkmcnt(0)
	v_mfma_f32_16x16x128_f8f6f4 v[130:133], v[2:9], v[18:25], 0
	v_mfma_f32_16x16x128_f8f6f4 v[122:125], v[10:17], v[18:25], 0
	v_mfma_f32_16x16x128_f8f6f4 v[114:117], v[2:9], v[26:33], 0
	v_mfma_f32_16x16x128_f8f6f4 v[106:109], v[10:17], v[26:33], 0
	v_mfma_f32_16x16x128_f8f6f4 v[98:101], v[2:9], v[34:41], 0
	v_mfma_f32_16x16x128_f8f6f4 v[90:93], v[10:17], v[34:41], 0
	v_mfma_f32_16x16x128_f8f6f4 v[86:89], v[2:9], v[50:57], 0
	v_mfma_f32_16x16x128_f8f6f4 v[82:85], v[10:17], v[50:57], 0
	s_setprio 0
	s_barrier
	v_lshl_add_u64 v[160:161], s[34:35], 0, v[0:1]
	s_mov_b64 s[20:21], 0x100
	s_mov_b32 m0, s47
	v_lshl_add_u64 v[42:43], v[160:161], 0, s[20:21]
	v_lshl_add_u64 v[162:163], s[34:35], 0, v[146:147]
	ds_read_b128 v[188:191], v169
	ds_read_b128 v[192:195], v170
	ds_read_b128 v[196:199], v171
	ds_read_b128 v[200:203], v172
	global_load_lds_dwordx4 v[42:43], off
	v_lshl_add_u64 v[42:43], v[162:163], 0, s[20:21]
	s_mov_b32 m0, s48
	s_nop 0
	global_load_lds_dwordx4 v[42:43], off
	s_barrier
	s_waitcnt lgkmcnt(0)
	s_setprio 1
	s_waitcnt lgkmcnt(0)
	v_mfma_f32_16x16x128_f8f6f4 v[62:65], v[188:195], v[18:25], 0
	v_mfma_f32_16x16x128_f8f6f4 v[58:61], v[196:203], v[18:25], 0
	v_mfma_f32_16x16x128_f8f6f4 v[46:49], v[188:195], v[26:33], 0
	v_mfma_f32_16x16x128_f8f6f4 v[42:45], v[196:203], v[26:33], 0
	v_mfma_f32_16x16x128_f8f6f4 v[30:33], v[188:195], v[34:41], 0
	v_mfma_f32_16x16x128_f8f6f4 v[26:29], v[196:203], v[34:41], 0
	v_mfma_f32_16x16x128_f8f6f4 v[22:25], v[188:195], v[50:57], 0
	v_mfma_f32_16x16x128_f8f6f4 v[18:21], v[196:203], v[50:57], 0
	s_setprio 0
	v_lshl_add_u64 v[156:157], s[42:43], 0, v[150:151]
	s_mov_b32 m0, s46
	v_lshl_add_u64 v[66:67], v[156:157], 0, s[20:21]
	v_lshl_add_u64 v[158:159], s[42:43], 0, v[148:149]
	s_barrier
	ds_read_b128 v[34:37], v181 offset:16384
	ds_read_b128 v[38:41], v181 offset:17408
	ds_read_b128 v[50:53], v181 offset:18432
	ds_read_b128 v[54:57], v181 offset:19456
	ds_read_b128 v[204:207], v181 offset:20480
	ds_read_b128 v[208:211], v181 offset:21504
	ds_read_b128 v[212:215], v181 offset:22528
	ds_read_b128 v[216:219], v181 offset:23552
	global_load_lds_dwordx4 v[66:67], off
	v_lshl_add_u64 v[66:67], v[158:159], 0, s[20:21]
	s_mov_b32 m0, s49
	s_nop 0
	global_load_lds_dwordx4 v[66:67], off
	s_barrier
	s_waitcnt lgkmcnt(0)
	s_setprio 1
	s_waitcnt lgkmcnt(0)
	v_mfma_f32_16x16x128_f8f6f4 v[142:145], v[2:9], v[34:41], 0
	v_mfma_f32_16x16x128_f8f6f4 v[138:141], v[10:17], v[34:41], 0
	v_mfma_f32_16x16x128_f8f6f4 v[134:137], v[2:9], v[50:57], 0
	v_mfma_f32_16x16x128_f8f6f4 v[126:129], v[10:17], v[50:57], 0
	v_mfma_f32_16x16x128_f8f6f4 v[118:121], v[2:9], v[204:211], 0
	v_mfma_f32_16x16x128_f8f6f4 v[110:113], v[10:17], v[204:211], 0
	v_mfma_f32_16x16x128_f8f6f4 v[102:105], v[2:9], v[212:219], 0
	v_mfma_f32_16x16x128_f8f6f4 v[94:97], v[10:17], v[212:219], 0
	s_setprio 0
	s_barrier
	s_add_u32 s20, s34, 0x20100
	s_addc_u32 s21, s35, 0
	s_mov_b32 m0, s50
	v_lshl_add_u64 v[2:3], s[20:21], 0, v[0:1]
	global_load_lds_dwordx4 v[2:3], off
	v_lshl_add_u64 v[2:3], s[20:21], 0, v[146:147]
	s_mov_b32 m0, s51
	s_nop 0
	global_load_lds_dwordx4 v[2:3], off
	s_waitcnt vmcnt(6)
	s_barrier
	s_setprio 1
	v_mfma_f32_16x16x128_f8f6f4 v[78:81], v[188:195], v[34:41], 0
	v_mfma_f32_16x16x128_f8f6f4 v[74:77], v[196:203], v[34:41], 0
	v_mfma_f32_16x16x128_f8f6f4 v[70:73], v[188:195], v[50:57], 0
	v_mfma_f32_16x16x128_f8f6f4 v[66:69], v[196:203], v[50:57], 0
	v_mfma_f32_16x16x128_f8f6f4 v[54:57], v[188:195], v[204:211], 0
	v_mfma_f32_16x16x128_f8f6f4 v[50:53], v[196:203], v[204:211], 0
	v_mfma_f32_16x16x128_f8f6f4 v[38:41], v[188:195], v[212:219], 0
	v_mfma_f32_16x16x128_f8f6f4 v[34:37], v[196:203], v[212:219], 0
	s_setprio 0
	s_barrier
	ds_read_b128 v[2:5], v173
	ds_read_b128 v[6:9], v174
	ds_read_b128 v[10:13], v175
	ds_read_b128 v[14:17], v176
	s_add_u32 s20, s42, 0x20100
	s_addc_u32 s21, s43, 0
	s_mov_b32 m0, s52
	v_lshl_add_u64 v[182:183], s[20:21], 0, v[150:151]
	ds_read_b128 v[188:191], v181 offset:32768
	ds_read_b128 v[192:195], v181 offset:33792
	ds_read_b128 v[196:199], v181 offset:34816
	ds_read_b128 v[200:203], v181 offset:35840
	ds_read_b128 v[204:207], v181 offset:36864
	ds_read_b128 v[208:211], v181 offset:37888
	ds_read_b128 v[212:215], v181 offset:38912
	ds_read_b128 v[216:219], v181 offset:39936
	global_load_lds_dwordx4 v[182:183], off
	v_lshl_add_u64 v[182:183], s[20:21], 0, v[148:149]
	s_mov_b32 m0, s53
	s_nop 0
	global_load_lds_dwordx4 v[182:183], off
	s_waitcnt lgkmcnt(8)
	s_barrier
	s_waitcnt lgkmcnt(0)
	s_setprio 1
	s_waitcnt lgkmcnt(0)
	v_mfma_f32_16x16x128_f8f6f4 v[130:133], v[2:9], v[188:195], v[130:133]
	v_mfma_f32_16x16x128_f8f6f4 v[122:125], v[10:17], v[188:195], v[122:125]
	v_mfma_f32_16x16x128_f8f6f4 v[114:117], v[2:9], v[196:203], v[114:117]
	v_mfma_f32_16x16x128_f8f6f4 v[106:109], v[10:17], v[196:203], v[106:109]
	v_mfma_f32_16x16x128_f8f6f4 v[98:101], v[2:9], v[204:211], v[98:101]
	v_mfma_f32_16x16x128_f8f6f4 v[90:93], v[10:17], v[204:211], v[90:93]
	v_mfma_f32_16x16x128_f8f6f4 v[86:89], v[2:9], v[212:219], v[86:89]
	v_mfma_f32_16x16x128_f8f6f4 v[82:85], v[10:17], v[212:219], v[82:85]
	s_setprio 0
	s_barrier
	s_mov_b64 s[20:21], 0x180
	s_mov_b32 m0, s55
	v_lshl_add_u64 v[160:161], v[160:161], 0, s[20:21]
	ds_read_b128 v[232:235], v177
	ds_read_b128 v[236:239], v178
	ds_read_b128 v[240:243], v179
	ds_read_b128 v[244:247], v180
	global_load_lds_dwordx4 v[160:161], off
	v_lshl_add_u64 v[160:161], v[162:163], 0, s[20:21]
	s_mov_b32 m0, s56
	s_nop 0
	global_load_lds_dwordx4 v[160:161], off
	s_barrier
	s_waitcnt lgkmcnt(0)
	s_setprio 1
	s_waitcnt lgkmcnt(0)
	v_mfma_f32_16x16x128_f8f6f4 v[62:65], v[232:239], v[188:195], v[62:65]
	v_mfma_f32_16x16x128_f8f6f4 v[58:61], v[240:247], v[188:195], v[58:61]
	v_mfma_f32_16x16x128_f8f6f4 v[46:49], v[232:239], v[196:203], v[46:49]
	v_mfma_f32_16x16x128_f8f6f4 v[42:45], v[240:247], v[196:203], v[42:45]
	v_mfma_f32_16x16x128_f8f6f4 v[30:33], v[232:239], v[204:211], v[30:33]
	v_mfma_f32_16x16x128_f8f6f4 v[26:29], v[240:247], v[204:211], v[26:29]
	v_mfma_f32_16x16x128_f8f6f4 v[22:25], v[232:239], v[212:219], v[22:25]
	v_mfma_f32_16x16x128_f8f6f4 v[18:21], v[240:247], v[212:219], v[18:21]
	s_setprio 0
	s_mov_b32 m0, s57
	v_lshl_add_u64 v[156:157], v[156:157], 0, s[20:21]
	s_barrier
	ds_read_b128 v[188:191], v181 offset:49152
	ds_read_b128 v[192:195], v181 offset:50176
	ds_read_b128 v[196:199], v181 offset:51200
	ds_read_b128 v[200:203], v181 offset:52224
	ds_read_b128 v[204:207], v181 offset:53248
	ds_read_b128 v[208:211], v181 offset:54272
	ds_read_b128 v[212:215], v181 offset:55296
	ds_read_b128 v[216:219], v181 offset:56320
	global_load_lds_dwordx4 v[156:157], off
	v_lshl_add_u64 v[156:157], v[158:159], 0, s[20:21]
	s_mov_b32 m0, s58
	s_nop 0
	global_load_lds_dwordx4 v[156:157], off
	s_barrier
	s_waitcnt lgkmcnt(0)
	s_setprio 1
	s_waitcnt lgkmcnt(0)
	v_mfma_f32_16x16x128_f8f6f4 v[142:145], v[2:9], v[188:195], v[142:145]
	v_mfma_f32_16x16x128_f8f6f4 v[138:141], v[10:17], v[188:195], v[138:141]
	v_mfma_f32_16x16x128_f8f6f4 v[134:137], v[2:9], v[196:203], v[134:137]
	v_mfma_f32_16x16x128_f8f6f4 v[126:129], v[10:17], v[196:203], v[126:129]
	v_mfma_f32_16x16x128_f8f6f4 v[118:121], v[2:9], v[204:211], v[118:121]
	v_mfma_f32_16x16x128_f8f6f4 v[110:113], v[10:17], v[204:211], v[110:113]
	v_mfma_f32_16x16x128_f8f6f4 v[102:105], v[2:9], v[212:219], v[102:105]
	v_mfma_f32_16x16x128_f8f6f4 v[94:97], v[10:17], v[212:219], v[94:97]
	s_setprio 0
	s_barrier
	s_add_u32 s20, s34, 0x20180
	s_addc_u32 s21, s35, 0
	s_mov_b32 m0, s59
	v_lshl_add_u64 v[2:3], s[20:21], 0, v[0:1]
	global_load_lds_dwordx4 v[2:3], off
	v_lshl_add_u64 v[2:3], s[20:21], 0, v[146:147]
	s_mov_b32 m0, s61
	s_nop 0
	global_load_lds_dwordx4 v[2:3], off
	s_waitcnt vmcnt(6)
	s_barrier
	s_setprio 1
	v_mfma_f32_16x16x128_f8f6f4 v[78:81], v[232:239], v[188:195], v[78:81]
	v_mfma_f32_16x16x128_f8f6f4 v[74:77], v[240:247], v[188:195], v[74:77]
	v_mfma_f32_16x16x128_f8f6f4 v[70:73], v[232:239], v[196:203], v[70:73]
	v_mfma_f32_16x16x128_f8f6f4 v[66:69], v[240:247], v[196:203], v[66:69]
	v_mfma_f32_16x16x128_f8f6f4 v[54:57], v[232:239], v[204:211], v[54:57]
	v_mfma_f32_16x16x128_f8f6f4 v[50:53], v[240:247], v[204:211], v[50:53]
	v_mfma_f32_16x16x128_f8f6f4 v[38:41], v[232:239], v[212:219], v[38:41]
	v_mfma_f32_16x16x128_f8f6f4 v[34:37], v[240:247], v[212:219], v[34:37]
	s_setprio 0
	s_add_u32 s20, s42, 0x20180
	s_addc_u32 s21, s43, 0
	s_add_u32 s71, s34, 0x200
	s_addc_u32 s72, s35, 0
	s_mov_b32 s73, 0
	s_barrier
.LBB0_526:
	ds_read_b128 v[10:13], v165
	ds_read_b128 v[14:17], v166
	ds_read_b128 v[156:159], v167
	ds_read_b128 v[160:163], v168
	s_add_u32 s34, s20, 0xfffe0080
	s_addc_u32 s35, s21, -1
	s_cmp_eq_u32 s73, 4
	s_cselect_b32 s43, s9, s35
	s_cselect_b32 s42, s67, s34
	s_cselect_b32 s35, s7, s72
	s_cselect_b32 s34, s68, s71
	s_mov_b32 m0, s69
	v_lshl_add_u64 v[2:3], s[20:21], 0, v[152:153]
	ds_read_b128 v[188:191], v181
	ds_read_b128 v[192:195], v181 offset:1024
	ds_read_b128 v[196:199], v181 offset:2048
	ds_read_b128 v[200:203], v181 offset:3072
	ds_read_b128 v[204:207], v181 offset:4096
	ds_read_b128 v[208:211], v181 offset:5120
	ds_read_b128 v[212:215], v181 offset:6144
	ds_read_b128 v[216:219], v181 offset:7168
	global_load_lds_dwordx4 v[2:3], off
	v_lshl_add_u64 v[2:3], s[20:21], 0, v[154:155]
	s_mov_b32 m0, s70
	s_nop 0
	global_load_lds_dwordx4 v[2:3], off
	s_waitcnt lgkmcnt(8)
	s_barrier
	s_waitcnt lgkmcnt(0)
	s_setprio 1
	s_waitcnt lgkmcnt(0)
	v_mfma_f32_16x16x128_f8f6f4 v[130:133], v[10:17], v[188:195], v[130:133]
	v_mfma_f32_16x16x128_f8f6f4 v[122:125], v[156:163], v[188:195], v[122:125]
	v_mfma_f32_16x16x128_f8f6f4 v[114:117], v[10:17], v[196:203], v[114:117]
	v_mfma_f32_16x16x128_f8f6f4 v[106:109], v[156:163], v[196:203], v[106:109]
	v_mfma_f32_16x16x128_f8f6f4 v[98:101], v[10:17], v[204:211], v[98:101]
	v_mfma_f32_16x16x128_f8f6f4 v[90:93], v[156:163], v[204:211], v[90:93]
	v_mfma_f32_16x16x128_f8f6f4 v[86:89], v[10:17], v[212:219], v[86:89]
	v_mfma_f32_16x16x128_f8f6f4 v[82:85], v[156:163], v[212:219], v[82:85]
	s_setprio 0
	s_barrier
	s_mov_b32 m0, s47
	v_lshl_add_u64 v[6:7], s[34:35], 0, v[0:1]
	ds_read_b128 v[232:235], v169
	ds_read_b128 v[236:239], v170
	ds_read_b128 v[240:243], v171
	ds_read_b128 v[244:247], v172
	global_load_lds_dwordx4 v[6:7], off
	v_lshl_add_u64 v[8:9], s[34:35], 0, v[146:147]
	s_mov_b32 m0, s48
	s_nop 0
	global_load_lds_dwordx4 v[8:9], off
	s_barrier
	s_waitcnt lgkmcnt(0)
	s_setprio 1
	s_waitcnt lgkmcnt(0)
	v_mfma_f32_16x16x128_f8f6f4 v[62:65], v[232:239], v[188:195], v[62:65]
	v_mfma_f32_16x16x128_f8f6f4 v[58:61], v[240:247], v[188:195], v[58:61]
	v_mfma_f32_16x16x128_f8f6f4 v[46:49], v[232:239], v[196:203], v[46:49]
	v_mfma_f32_16x16x128_f8f6f4 v[42:45], v[240:247], v[196:203], v[42:45]
	v_mfma_f32_16x16x128_f8f6f4 v[30:33], v[232:239], v[204:211], v[30:33]
	v_mfma_f32_16x16x128_f8f6f4 v[26:29], v[240:247], v[204:211], v[26:29]
	v_mfma_f32_16x16x128_f8f6f4 v[22:25], v[232:239], v[212:219], v[22:25]
	v_mfma_f32_16x16x128_f8f6f4 v[18:21], v[240:247], v[212:219], v[18:21]
	s_setprio 0
	s_mov_b32 m0, s46
	v_lshl_add_u64 v[2:3], s[42:43], 0, v[150:151]
	s_barrier
	ds_read_b128 v[188:191], v181 offset:16384
	ds_read_b128 v[192:195], v181 offset:17408
	ds_read_b128 v[196:199], v181 offset:18432
	ds_read_b128 v[200:203], v181 offset:19456
	ds_read_b128 v[204:207], v181 offset:20480
	ds_read_b128 v[208:211], v181 offset:21504
	ds_read_b128 v[212:215], v181 offset:22528
	ds_read_b128 v[216:219], v181 offset:23552
	global_load_lds_dwordx4 v[2:3], off
	v_lshl_add_u64 v[4:5], s[42:43], 0, v[148:149]
	s_mov_b32 m0, s49
	s_nop 0
	global_load_lds_dwordx4 v[4:5], off
	s_barrier
	s_waitcnt lgkmcnt(0)
	s_setprio 1
	s_waitcnt lgkmcnt(0)
	v_mfma_f32_16x16x128_f8f6f4 v[142:145], v[10:17], v[188:195], v[142:145]
	v_mfma_f32_16x16x128_f8f6f4 v[138:141], v[156:163], v[188:195], v[138:141]
	v_mfma_f32_16x16x128_f8f6f4 v[134:137], v[10:17], v[196:203], v[134:137]
	v_mfma_f32_16x16x128_f8f6f4 v[126:129], v[156:163], v[196:203], v[126:129]
	v_mfma_f32_16x16x128_f8f6f4 v[118:121], v[10:17], v[204:211], v[118:121]
	v_mfma_f32_16x16x128_f8f6f4 v[110:113], v[156:163], v[204:211], v[110:113]
	v_mfma_f32_16x16x128_f8f6f4 v[102:105], v[10:17], v[212:219], v[102:105]
	v_mfma_f32_16x16x128_f8f6f4 v[94:97], v[156:163], v[212:219], v[94:97]
	s_setprio 0
	s_barrier
	s_add_u32 s74, s34, 0x20000
	s_addc_u32 s75, s35, 0
	s_mov_b32 m0, s50
	v_lshl_add_u64 v[10:11], s[74:75], 0, v[0:1]
	global_load_lds_dwordx4 v[10:11], off
	v_lshl_add_u64 v[10:11], s[74:75], 0, v[146:147]
	s_mov_b32 m0, s51
	s_nop 0
	global_load_lds_dwordx4 v[10:11], off
	s_waitcnt vmcnt(6)
	s_barrier
	s_setprio 1
	v_mfma_f32_16x16x128_f8f6f4 v[78:81], v[232:239], v[188:195], v[78:81]
	v_mfma_f32_16x16x128_f8f6f4 v[74:77], v[240:247], v[188:195], v[74:77]
	v_mfma_f32_16x16x128_f8f6f4 v[70:73], v[232:239], v[196:203], v[70:73]
	v_mfma_f32_16x16x128_f8f6f4 v[66:69], v[240:247], v[196:203], v[66:69]
	v_mfma_f32_16x16x128_f8f6f4 v[54:57], v[232:239], v[204:211], v[54:57]
	v_mfma_f32_16x16x128_f8f6f4 v[50:53], v[240:247], v[204:211], v[50:53]
	v_mfma_f32_16x16x128_f8f6f4 v[38:41], v[232:239], v[212:219], v[38:41]
	v_mfma_f32_16x16x128_f8f6f4 v[34:37], v[240:247], v[212:219], v[34:37]
	s_setprio 0
	s_barrier
	ds_read_b128 v[10:13], v173
	ds_read_b128 v[14:17], v174
	ds_read_b128 v[156:159], v175
	ds_read_b128 v[160:163], v176
	s_add_u32 s42, s42, 0x20000
	s_addc_u32 s43, s43, 0
	s_mov_b32 m0, s52
	v_lshl_add_u64 v[182:183], s[42:43], 0, v[150:151]
	ds_read_b128 v[188:191], v181 offset:32768
	ds_read_b128 v[192:195], v181 offset:33792
	ds_read_b128 v[196:199], v181 offset:34816
	ds_read_b128 v[200:203], v181 offset:35840
	ds_read_b128 v[204:207], v181 offset:36864
	ds_read_b128 v[208:211], v181 offset:37888
	ds_read_b128 v[212:215], v181 offset:38912
	ds_read_b128 v[216:219], v181 offset:39936
	global_load_lds_dwordx4 v[182:183], off
	v_lshl_add_u64 v[182:183], s[42:43], 0, v[148:149]
	s_mov_b32 m0, s53
	s_nop 0
	global_load_lds_dwordx4 v[182:183], off
	s_waitcnt lgkmcnt(8)
	s_barrier
	s_waitcnt lgkmcnt(0)
	s_setprio 1
	s_waitcnt lgkmcnt(0)
	v_mfma_f32_16x16x128_f8f6f4 v[130:133], v[10:17], v[188:195], v[130:133]
	v_mfma_f32_16x16x128_f8f6f4 v[122:125], v[156:163], v[188:195], v[122:125]
	v_mfma_f32_16x16x128_f8f6f4 v[114:117], v[10:17], v[196:203], v[114:117]
	v_mfma_f32_16x16x128_f8f6f4 v[106:109], v[156:163], v[196:203], v[106:109]
	v_mfma_f32_16x16x128_f8f6f4 v[98:101], v[10:17], v[204:211], v[98:101]
	v_mfma_f32_16x16x128_f8f6f4 v[90:93], v[156:163], v[204:211], v[90:93]
	v_mfma_f32_16x16x128_f8f6f4 v[86:89], v[10:17], v[212:219], v[86:89]
	v_mfma_f32_16x16x128_f8f6f4 v[82:85], v[156:163], v[212:219], v[82:85]
	s_setprio 0
	s_barrier
	s_mov_b32 m0, s55
	v_lshl_add_u64 v[6:7], v[6:7], 0, s[24:25]
	ds_read_b128 v[232:235], v177
	ds_read_b128 v[236:239], v178
	ds_read_b128 v[240:243], v179
	ds_read_b128 v[244:247], v180
	global_load_lds_dwordx4 v[6:7], off
	v_lshl_add_u64 v[6:7], v[8:9], 0, s[24:25]
	s_mov_b32 m0, s56
	s_nop 0
	global_load_lds_dwordx4 v[6:7], off
	s_barrier
	s_waitcnt lgkmcnt(0)
	s_setprio 1
	s_waitcnt lgkmcnt(0)
	v_mfma_f32_16x16x128_f8f6f4 v[62:65], v[232:239], v[188:195], v[62:65]
	v_mfma_f32_16x16x128_f8f6f4 v[58:61], v[240:247], v[188:195], v[58:61]
	v_mfma_f32_16x16x128_f8f6f4 v[46:49], v[232:239], v[196:203], v[46:49]
	v_mfma_f32_16x16x128_f8f6f4 v[42:45], v[240:247], v[196:203], v[42:45]
	v_mfma_f32_16x16x128_f8f6f4 v[30:33], v[232:239], v[204:211], v[30:33]
	v_mfma_f32_16x16x128_f8f6f4 v[26:29], v[240:247], v[204:211], v[26:29]
	v_mfma_f32_16x16x128_f8f6f4 v[22:25], v[232:239], v[212:219], v[22:25]
	v_mfma_f32_16x16x128_f8f6f4 v[18:21], v[240:247], v[212:219], v[18:21]
	s_setprio 0
	s_mov_b32 m0, s57
	v_lshl_add_u64 v[2:3], v[2:3], 0, s[24:25]
	s_barrier
	ds_read_b128 v[188:191], v181 offset:49152
	ds_read_b128 v[192:195], v181 offset:50176
	ds_read_b128 v[196:199], v181 offset:51200
	ds_read_b128 v[200:203], v181 offset:52224
	ds_read_b128 v[204:207], v181 offset:53248
	ds_read_b128 v[208:211], v181 offset:54272
	ds_read_b128 v[212:215], v181 offset:55296
	ds_read_b128 v[216:219], v181 offset:56320
	global_load_lds_dwordx4 v[2:3], off
	v_lshl_add_u64 v[2:3], v[4:5], 0, s[24:25]
	s_mov_b32 m0, s58
	s_nop 0
	global_load_lds_dwordx4 v[2:3], off
	s_barrier
	s_waitcnt lgkmcnt(0)
	s_setprio 1
	s_waitcnt lgkmcnt(0)
	v_mfma_f32_16x16x128_f8f6f4 v[142:145], v[10:17], v[188:195], v[142:145]
	v_mfma_f32_16x16x128_f8f6f4 v[138:141], v[156:163], v[188:195], v[138:141]
	v_mfma_f32_16x16x128_f8f6f4 v[134:137], v[10:17], v[196:203], v[134:137]
	v_mfma_f32_16x16x128_f8f6f4 v[126:129], v[156:163], v[196:203], v[126:129]
	v_mfma_f32_16x16x128_f8f6f4 v[118:121], v[10:17], v[204:211], v[118:121]
	v_mfma_f32_16x16x128_f8f6f4 v[110:113], v[156:163], v[204:211], v[110:113]
	v_mfma_f32_16x16x128_f8f6f4 v[102:105], v[10:17], v[212:219], v[102:105]
	v_mfma_f32_16x16x128_f8f6f4 v[94:97], v[156:163], v[212:219], v[94:97]
	s_setprio 0
	s_barrier
	s_add_u32 s34, s34, 0x20080
	s_addc_u32 s35, s35, 0
	s_mov_b32 m0, s59
	v_lshl_add_u64 v[2:3], s[34:35], 0, v[0:1]
	global_load_lds_dwordx4 v[2:3], off
	v_lshl_add_u64 v[2:3], s[34:35], 0, v[146:147]
	s_mov_b32 m0, s61
	s_nop 0
	global_load_lds_dwordx4 v[2:3], off
	s_waitcnt vmcnt(6)
	s_barrier
	s_setprio 1
	v_mfma_f32_16x16x128_f8f6f4 v[78:81], v[232:239], v[188:195], v[78:81]
	v_mfma_f32_16x16x128_f8f6f4 v[74:77], v[240:247], v[188:195], v[74:77]
	v_mfma_f32_16x16x128_f8f6f4 v[70:73], v[232:239], v[196:203], v[70:73]
	v_mfma_f32_16x16x128_f8f6f4 v[66:69], v[240:247], v[196:203], v[66:69]
	v_mfma_f32_16x16x128_f8f6f4 v[54:57], v[232:239], v[204:211], v[54:57]
	v_mfma_f32_16x16x128_f8f6f4 v[50:53], v[240:247], v[204:211], v[50:53]
	v_mfma_f32_16x16x128_f8f6f4 v[38:41], v[232:239], v[212:219], v[38:41]
	v_mfma_f32_16x16x128_f8f6f4 v[34:37], v[240:247], v[212:219], v[34:37]
	s_setprio 0
	s_add_i32 s73, s73, 2
	s_add_u32 s20, s20, 0x100
	s_addc_u32 s21, s21, 0
	s_add_u32 s71, s71, 0x100
	s_addc_u32 s72, s72, 0
	s_cmp_gt_u32 s73, 5
	s_barrier
	s_cbranch_scc0 .LBB0_526
	s_ashr_i32 s21, s66, 1
	s_ashr_i32 s20, s65, 1
	s_and_b32 s21, s21, -4
	s_add_i32 s20, s21, s20
	s_ashr_i32 s21, s20, 31
	s_lshl_b64 s[20:21], s[20:21], 22
	s_add_u32 s20, s62, s20
	s_addc_u32 s21, s63, s21
	s_lshl_b32 s34, s66, 19
	s_and_b32 s34, s34, 0x380000
	s_nop 15
	s_nop 15
	v_mbcnt_lo_u32_b32 v2, -1, 0
	v_mbcnt_hi_u32_b32 v2, -1, v2
	s_add_u32 s20, s20, s34
	v_and_b32_e32 v3, 15, v2
	s_addc_u32 s21, s21, 0
	s_lshl_b32 s34, s65, 18
	v_lshrrev_b32_e32 v2, 1, v2
	v_readlane_b32 s7, v252, 51
	v_readlane_b32 s9, v252, 52
	s_and_b32 s34, s34, 0x40000
	v_and_b32_e32 v2, 24, v2
	s_add_u32 s20, s20, s34
	v_lshl_or_b32 v6, s9, 5, v2
	v_lshl_or_b32 v8, s7, 6, v3
	s_addc_u32 s21, s21, 0
	v_ashrrev_i32_e32 v7, 31, v6
	v_pk_mul_f32 v[4:5], v[132:133], s[22:23] op_sel_hi:[1,0]
	v_pk_mul_f32 v[2:3], v[130:131], s[22:23] op_sel_hi:[1,0]
	v_pk_mul_f32 v[12:13], v[124:125], s[22:23] op_sel_hi:[1,0]
	v_ashrrev_i32_e32 v9, 31, v8
	v_lshl_add_u64 v[10:11], v[6:7], 1, s[20:21]
	v_pk_mul_f32 v[14:15], v[122:123], s[22:23] op_sel_hi:[1,0]
	v_cvt_pk_bf16_f32 v2, v2, v3
	v_cvt_pk_bf16_f32 v3, v4, v5
	v_cvt_pk_bf16_f32 v5, v12, v13
	v_lshlrev_b64 v[12:13], 10, v[8:9]
	v_cvt_pk_bf16_f32 v4, v14, v15
	v_lshl_add_u64 v[14:15], v[10:11], 0, v[12:13]
	global_store_dwordx4 v[14:15], v[2:5], off
	v_pk_mul_f32 v[14:15], v[108:109], s[22:23] op_sel_hi:[1,0]
	v_pk_mul_f32 v[16:17], v[106:107], s[22:23] op_sel_hi:[1,0]
	v_pk_mul_f32 v[4:5], v[116:117], s[22:23] op_sel_hi:[1,0]
	v_pk_mul_f32 v[2:3], v[114:115], s[22:23] op_sel_hi:[1,0]
	v_pk_mul_f32 v[90:91], v[90:91], s[22:23] op_sel_hi:[1,0]
	v_cvt_pk_bf16_f32 v2, v2, v3
	v_cvt_pk_bf16_f32 v3, v4, v5
	v_cvt_pk_bf16_f32 v5, v14, v15
	v_or_b32_e32 v14, 16, v8
	v_ashrrev_i32_e32 v15, 31, v14
	v_lshlrev_b64 v[14:15], 10, v[14:15]
	v_cvt_pk_bf16_f32 v4, v16, v17
	v_lshl_add_u64 v[16:17], v[10:11], 0, v[14:15]
	global_store_dwordx4 v[16:17], v[2:5], off
	v_pk_mul_f32 v[16:17], v[92:93], s[22:23] op_sel_hi:[1,0]
	v_pk_mul_f32 v[82:83], v[82:83], s[22:23] op_sel_hi:[1,0]
	v_pk_mul_f32 v[4:5], v[100:101], s[22:23] op_sel_hi:[1,0]
	v_pk_mul_f32 v[2:3], v[98:99], s[22:23] op_sel_hi:[1,0]
	v_pk_mul_f32 v[84:85], v[84:85], s[22:23] op_sel_hi:[1,0]
	v_cvt_pk_bf16_f32 v2, v2, v3
	v_cvt_pk_bf16_f32 v3, v4, v5
	v_cvt_pk_bf16_f32 v5, v16, v17
	v_or_b32_e32 v16, 32, v8
	v_ashrrev_i32_e32 v17, 31, v16
	v_lshlrev_b64 v[16:17], 10, v[16:17]
	v_cvt_pk_bf16_f32 v4, v90, v91
	v_lshl_add_u64 v[90:91], v[10:11], 0, v[16:17]
	global_store_dwordx4 v[90:91], v[2:5], off
	v_pk_mul_f32 v[90:91], v[110:111], s[22:23] op_sel_hi:[1,0]
	v_pk_mul_f32 v[92:93], v[94:95], s[22:23] op_sel_hi:[1,0]
	v_pk_mul_f32 v[4:5], v[88:89], s[22:23] op_sel_hi:[1,0]
	v_pk_mul_f32 v[2:3], v[86:87], s[22:23] op_sel_hi:[1,0]
	v_pk_mul_f32 v[86:87], v[140:141], s[22:23] op_sel_hi:[1,0]
	v_cvt_pk_bf16_f32 v2, v2, v3
	v_cvt_pk_bf16_f32 v3, v4, v5
	v_cvt_pk_bf16_f32 v4, v82, v83
	v_or_b32_e32 v82, 48, v8
	v_ashrrev_i32_e32 v83, 31, v82
	v_lshlrev_b64 v[82:83], 10, v[82:83]
	v_cvt_pk_bf16_f32 v5, v84, v85
	v_lshl_add_u64 v[84:85], v[10:11], 0, v[82:83]
	global_store_dwordx4 v[84:85], v[2:5], off
	v_add_u32_e32 v84, 0x80, v8
	v_ashrrev_i32_e32 v85, 31, v84
	v_pk_mul_f32 v[4:5], v[144:145], s[22:23] op_sel_hi:[1,0]
	v_pk_mul_f32 v[2:3], v[142:143], s[22:23] op_sel_hi:[1,0]
	v_pk_mul_f32 v[88:89], v[138:139], s[22:23] op_sel_hi:[1,0]
	v_lshlrev_b64 v[84:85], 10, v[84:85]
	v_cvt_pk_bf16_f32 v2, v2, v3
	v_cvt_pk_bf16_f32 v3, v4, v5
	v_cvt_pk_bf16_f32 v4, v88, v89
	v_cvt_pk_bf16_f32 v5, v86, v87
	v_lshl_add_u64 v[86:87], v[10:11], 0, v[84:85]
	global_store_dwordx4 v[86:87], v[2:5], off
	v_pk_mul_f32 v[86:87], v[128:129], s[22:23] op_sel_hi:[1,0]
	v_pk_mul_f32 v[88:89], v[126:127], s[22:23] op_sel_hi:[1,0]
	v_pk_mul_f32 v[4:5], v[136:137], s[22:23] op_sel_hi:[1,0]
	v_pk_mul_f32 v[2:3], v[134:135], s[22:23] op_sel_hi:[1,0]
	v_pk_mul_f32 v[58:59], v[58:59], s[22:23] op_sel_hi:[1,0]
	v_cvt_pk_bf16_f32 v2, v2, v3
	v_cvt_pk_bf16_f32 v3, v4, v5
	v_cvt_pk_bf16_f32 v5, v86, v87
	v_add_u32_e32 v86, 0x90, v8
	v_ashrrev_i32_e32 v87, 31, v86
	v_lshlrev_b64 v[86:87], 10, v[86:87]
	v_cvt_pk_bf16_f32 v4, v88, v89
	v_lshl_add_u64 v[88:89], v[10:11], 0, v[86:87]
	global_store_dwordx4 v[88:89], v[2:5], off
	v_pk_mul_f32 v[88:89], v[112:113], s[22:23] op_sel_hi:[1,0]
	s_and_b64 vcc, exec, s[4:5]
	v_pk_mul_f32 v[4:5], v[120:121], s[22:23] op_sel_hi:[1,0]
	v_pk_mul_f32 v[2:3], v[118:119], s[22:23] op_sel_hi:[1,0]
	s_mov_b32 s66, s6
	v_cvt_pk_bf16_f32 v2, v2, v3
	v_cvt_pk_bf16_f32 v3, v4, v5
	v_cvt_pk_bf16_f32 v5, v88, v89
	v_add_u32_e32 v88, 0xa0, v8
	v_ashrrev_i32_e32 v89, 31, v88
	v_lshlrev_b64 v[88:89], 10, v[88:89]
	v_add_u32_e32 v8, 0xb0, v8
	v_cvt_pk_bf16_f32 v4, v90, v91
	v_lshl_add_u64 v[90:91], v[10:11], 0, v[88:89]
	v_ashrrev_i32_e32 v9, 31, v8
	global_store_dwordx4 v[90:91], v[2:5], off
	v_pk_mul_f32 v[90:91], v[96:97], s[22:23] op_sel_hi:[1,0]
	v_lshlrev_b64 v[8:9], 10, v[8:9]
	v_pk_mul_f32 v[4:5], v[104:105], s[22:23] op_sel_hi:[1,0]
	v_pk_mul_f32 v[2:3], v[102:103], s[22:23] op_sel_hi:[1,0]
	v_lshl_add_u64 v[10:11], v[10:11], 0, v[8:9]
	v_cvt_pk_bf16_f32 v2, v2, v3
	v_cvt_pk_bf16_f32 v3, v4, v5
	v_cvt_pk_bf16_f32 v4, v92, v93
	v_cvt_pk_bf16_f32 v5, v90, v91
	global_store_dwordx4 v[10:11], v[2:5], off
	v_pk_mul_f32 v[10:11], v[60:61], s[22:23] op_sel_hi:[1,0]
	s_mov_b32 s65, s8
	v_add_u32_e32 v2, 0x80, v6
	v_ashrrev_i32_e32 v3, 31, v2
	v_lshl_add_u64 v[6:7], v[2:3], 1, s[20:21]
	v_pk_mul_f32 v[4:5], v[64:65], s[22:23] op_sel_hi:[1,0]
	v_pk_mul_f32 v[2:3], v[62:63], s[22:23] op_sel_hi:[1,0]
	s_mov_b64 s[34:35], s[12:13]
	v_cvt_pk_bf16_f32 v2, v2, v3
	v_cvt_pk_bf16_f32 v3, v4, v5
	v_cvt_pk_bf16_f32 v4, v58, v59
	v_cvt_pk_bf16_f32 v5, v10, v11
	v_lshl_add_u64 v[10:11], v[6:7], 0, v[12:13]
	global_store_dwordx4 v[10:11], v[2:5], off
	v_pk_mul_f32 v[10:11], v[44:45], s[22:23] op_sel_hi:[1,0]
	v_pk_mul_f32 v[12:13], v[42:43], s[22:23] op_sel_hi:[1,0]
	v_pk_mul_f32 v[4:5], v[48:49], s[22:23] op_sel_hi:[1,0]
	v_pk_mul_f32 v[2:3], v[46:47], s[22:23] op_sel_hi:[1,0]
	s_mov_b64 s[42:43], s[10:11]
	v_cvt_pk_bf16_f32 v2, v2, v3
	v_cvt_pk_bf16_f32 v3, v4, v5
	v_cvt_pk_bf16_f32 v4, v12, v13
	v_cvt_pk_bf16_f32 v5, v10, v11
	v_lshl_add_u64 v[10:11], v[6:7], 0, v[14:15]
	global_store_dwordx4 v[10:11], v[2:5], off
	v_pk_mul_f32 v[10:11], v[28:29], s[22:23] op_sel_hi:[1,0]
	v_pk_mul_f32 v[12:13], v[26:27], s[22:23] op_sel_hi:[1,0]
	v_pk_mul_f32 v[4:5], v[32:33], s[22:23] op_sel_hi:[1,0]
	v_pk_mul_f32 v[2:3], v[30:31], s[22:23] op_sel_hi:[1,0]
	s_nop 0
	v_cvt_pk_bf16_f32 v2, v2, v3
	v_cvt_pk_bf16_f32 v3, v4, v5
	v_cvt_pk_bf16_f32 v4, v12, v13
	v_cvt_pk_bf16_f32 v5, v10, v11
	v_lshl_add_u64 v[10:11], v[6:7], 0, v[16:17]
	global_store_dwordx4 v[10:11], v[2:5], off
	v_pk_mul_f32 v[10:11], v[20:21], s[22:23] op_sel_hi:[1,0]
	v_pk_mul_f32 v[12:13], v[18:19], s[22:23] op_sel_hi:[1,0]
	v_pk_mul_f32 v[4:5], v[24:25], s[22:23] op_sel_hi:[1,0]
	v_pk_mul_f32 v[2:3], v[22:23], s[22:23] op_sel_hi:[1,0]
	s_nop 0
	v_cvt_pk_bf16_f32 v2, v2, v3
	v_cvt_pk_bf16_f32 v3, v4, v5
	v_cvt_pk_bf16_f32 v4, v12, v13
	v_cvt_pk_bf16_f32 v5, v10, v11
	v_lshl_add_u64 v[10:11], v[6:7], 0, v[82:83]
	global_store_dwordx4 v[10:11], v[2:5], off
	v_pk_mul_f32 v[10:11], v[76:77], s[22:23] op_sel_hi:[1,0]
	v_pk_mul_f32 v[12:13], v[74:75], s[22:23] op_sel_hi:[1,0]
	v_pk_mul_f32 v[4:5], v[80:81], s[22:23] op_sel_hi:[1,0]
	v_pk_mul_f32 v[2:3], v[78:79], s[22:23] op_sel_hi:[1,0]
	s_nop 0
	v_cvt_pk_bf16_f32 v2, v2, v3
	v_cvt_pk_bf16_f32 v3, v4, v5
	v_cvt_pk_bf16_f32 v4, v12, v13
	v_cvt_pk_bf16_f32 v5, v10, v11
	v_lshl_add_u64 v[10:11], v[6:7], 0, v[84:85]
	global_store_dwordx4 v[10:11], v[2:5], off
	v_pk_mul_f32 v[10:11], v[68:69], s[22:23] op_sel_hi:[1,0]
	v_pk_mul_f32 v[12:13], v[66:67], s[22:23] op_sel_hi:[1,0]
	v_pk_mul_f32 v[4:5], v[72:73], s[22:23] op_sel_hi:[1,0]
	v_pk_mul_f32 v[2:3], v[70:71], s[22:23] op_sel_hi:[1,0]
	s_nop 0
	v_cvt_pk_bf16_f32 v2, v2, v3
	v_cvt_pk_bf16_f32 v3, v4, v5
	v_cvt_pk_bf16_f32 v4, v12, v13
	v_cvt_pk_bf16_f32 v5, v10, v11
	v_lshl_add_u64 v[10:11], v[6:7], 0, v[86:87]
	global_store_dwordx4 v[10:11], v[2:5], off
	v_pk_mul_f32 v[10:11], v[52:53], s[22:23] op_sel_hi:[1,0]
	v_pk_mul_f32 v[12:13], v[50:51], s[22:23] op_sel_hi:[1,0]
	v_pk_mul_f32 v[4:5], v[56:57], s[22:23] op_sel_hi:[1,0]
	v_pk_mul_f32 v[2:3], v[54:55], s[22:23] op_sel_hi:[1,0]
	s_nop 0
	v_cvt_pk_bf16_f32 v2, v2, v3
	v_cvt_pk_bf16_f32 v3, v4, v5
	v_cvt_pk_bf16_f32 v4, v12, v13
	v_cvt_pk_bf16_f32 v5, v10, v11
	v_lshl_add_u64 v[10:11], v[6:7], 0, v[88:89]
	global_store_dwordx4 v[10:11], v[2:5], off
	v_pk_mul_f32 v[10:11], v[36:37], s[22:23] op_sel_hi:[1,0]
	v_pk_mul_f32 v[12:13], v[34:35], s[22:23] op_sel_hi:[1,0]
	v_pk_mul_f32 v[4:5], v[40:41], s[22:23] op_sel_hi:[1,0]
	v_pk_mul_f32 v[2:3], v[38:39], s[22:23] op_sel_hi:[1,0]
	v_lshl_add_u64 v[6:7], v[6:7], 0, v[8:9]
	v_cvt_pk_bf16_f32 v2, v2, v3
	v_cvt_pk_bf16_f32 v3, v4, v5
	v_cvt_pk_bf16_f32 v4, v12, v13
	v_cvt_pk_bf16_f32 v5, v10, v11
	global_store_dwordx4 v[6:7], v[2:5], off
	s_cbranch_vccz .LBB0_519
	s_waitcnt vmcnt(0)
	s_cmpk_gt_u32 s28, 0xff
	s_cbranch_scc1 .LBB0_530
	s_barrier

.LBB0_833:
	v_mov_b64_e32 v[2:3], 0x200
	s_ashr_i32 s21, s20, 31
	v_cmp_lt_i64_e32 vcc, s[34:35], v[2:3]
	s_lshl_b64 s[34:35], s[20:21], 19
	s_add_u32 s34, s28, s34
	s_addc_u32 s35, s50, s35
	s_and_b64 s[42:43], vcc, exec
	ds_read_b128 v[2:5], v175
	ds_read_b128 v[6:9], v176
	ds_read_b128 v[10:13], v177
	ds_read_b128 v[14:17], v178
	s_cselect_b32 s21, s35, s47
	s_cselect_b32 s71, s34, s46
	s_ashr_i32 s13, s12, 31
	s_lshl_b64 s[42:43], s[12:13], 19
	s_add_u32 s42, s51, s42
	s_addc_u32 s43, s52, s43
	s_and_b64 s[48:49], vcc, exec
	s_cselect_b32 s13, s43, s45
	s_cselect_b32 s72, s42, s44
	s_add_u32 s48, s46, 0x40080
	s_addc_u32 s49, s47, 0
	s_add_i32 s73, s53, 0xc000
	v_add_u32_e32 v0, s61, v174
	v_lshl_add_u64 v[50:51], s[48:49], 0, v[164:165]
	s_mov_b32 m0, s73
	s_add_i32 s74, s53, 0xe000
	ds_read_b128 v[18:21], v0
	ds_read_b128 v[22:25], v0 offset:1024
	ds_read_b128 v[26:29], v0 offset:2048
	ds_read_b128 v[30:33], v0 offset:3072
	ds_read_b128 v[34:37], v0 offset:4096
	ds_read_b128 v[38:41], v0 offset:5120
	ds_read_b128 v[42:45], v0 offset:6144
	ds_read_b128 v[46:49], v0 offset:7168
	global_load_lds_dwordx4 v[50:51], off
	v_lshl_add_u64 v[50:51], s[48:49], 0, v[160:161]
	s_mov_b32 m0, s74
	s_nop 0
	global_load_lds_dwordx4 v[50:51], off
	s_waitcnt lgkmcnt(8)
	s_barrier
	s_waitcnt lgkmcnt(0)
	s_setprio 1
	s_waitcnt lgkmcnt(0)
	v_mfma_f32_16x16x128_f8f6f4 v[134:137], v[2:9], v[18:25], 0
	v_mfma_f32_16x16x128_f8f6f4 v[130:133], v[10:17], v[18:25], 0
	v_mfma_f32_16x16x128_f8f6f4 v[118:121], v[2:9], v[26:33], 0
	v_mfma_f32_16x16x128_f8f6f4 v[114:117], v[10:17], v[26:33], 0
	v_mfma_f32_16x16x128_f8f6f4 v[102:105], v[2:9], v[34:41], 0
	v_mfma_f32_16x16x128_f8f6f4 v[98:101], v[10:17], v[34:41], 0
	v_mfma_f32_16x16x128_f8f6f4 v[74:77], v[2:9], v[42:49], 0
	v_mfma_f32_16x16x128_f8f6f4 v[66:69], v[10:17], v[42:49], 0
	s_setprio 0
	s_barrier
	v_lshl_add_u64 v[150:151], s[44:45], 0, v[162:163]
	s_mov_b64 s[48:49], 0x100
	s_mov_b32 m0, s54
	v_lshl_add_u64 v[50:51], v[150:151], 0, s[48:49]
	v_lshl_add_u64 v[152:153], s[44:45], 0, v[158:159]
	ds_read_b128 v[188:191], v179
	ds_read_b128 v[192:195], v180
	ds_read_b128 v[202:205], v181
	ds_read_b128 v[206:209], v182
	global_load_lds_dwordx4 v[50:51], off
	v_lshl_add_u64 v[50:51], v[152:153], 0, s[48:49]
	s_mov_b32 m0, s55
	s_nop 0
	global_load_lds_dwordx4 v[50:51], off
	s_barrier
	s_waitcnt lgkmcnt(0)
	s_setprio 1
	s_waitcnt lgkmcnt(0)
	v_mfma_f32_16x16x128_f8f6f4 v[142:145], v[188:195], v[18:25], 0
	v_mfma_f32_16x16x128_f8f6f4 v[138:141], v[202:209], v[18:25], 0
	v_mfma_f32_16x16x128_f8f6f4 v[126:129], v[188:195], v[26:33], 0
	v_mfma_f32_16x16x128_f8f6f4 v[122:125], v[202:209], v[26:33], 0
	v_mfma_f32_16x16x128_f8f6f4 v[110:113], v[188:195], v[34:41], 0
	v_mfma_f32_16x16x128_f8f6f4 v[106:109], v[202:209], v[34:41], 0
	v_mfma_f32_16x16x128_f8f6f4 v[78:81], v[188:195], v[42:49], 0
	v_mfma_f32_16x16x128_f8f6f4 v[70:73], v[202:209], v[42:49], 0
	s_setprio 0
	v_lshl_add_u64 v[146:147], s[46:47], 0, v[164:165]
	s_mov_b32 m0, s53
	v_lshl_add_u64 v[18:19], v[146:147], 0, s[48:49]
	v_lshl_add_u64 v[148:149], s[46:47], 0, v[160:161]
	s_barrier
	ds_read_b128 v[26:29], v0 offset:16384
	ds_read_b128 v[30:33], v0 offset:17408
	ds_read_b128 v[34:37], v0 offset:18432
	ds_read_b128 v[38:41], v0 offset:19456
	ds_read_b128 v[210:213], v0 offset:20480
	ds_read_b128 v[214:217], v0 offset:21504
	ds_read_b128 v[232:235], v0 offset:22528
	ds_read_b128 v[236:239], v0 offset:23552
	global_load_lds_dwordx4 v[18:19], off
	v_lshl_add_u64 v[18:19], v[148:149], 0, s[48:49]
	s_mov_b32 m0, s56
	s_nop 0
	global_load_lds_dwordx4 v[18:19], off
	s_barrier
	s_waitcnt lgkmcnt(0)
	s_setprio 1
	s_waitcnt lgkmcnt(0)
	v_mfma_f32_16x16x128_f8f6f4 v[94:97], v[2:9], v[26:33], 0
	v_mfma_f32_16x16x128_f8f6f4 v[90:93], v[10:17], v[26:33], 0
	v_mfma_f32_16x16x128_f8f6f4 v[62:65], v[2:9], v[34:41], 0
	v_mfma_f32_16x16x128_f8f6f4 v[58:61], v[10:17], v[34:41], 0
	v_mfma_f32_16x16x128_f8f6f4 v[46:49], v[2:9], v[210:217], 0
	v_mfma_f32_16x16x128_f8f6f4 v[42:45], v[10:17], v[210:217], 0
	v_mfma_f32_16x16x128_f8f6f4 v[22:25], v[2:9], v[232:239], 0
	v_mfma_f32_16x16x128_f8f6f4 v[18:21], v[10:17], v[232:239], 0
	s_setprio 0
	s_barrier
	s_add_u32 s48, s44, 0x40100
	s_addc_u32 s49, s45, 0
	s_mov_b32 m0, s57
	v_lshl_add_u64 v[2:3], s[48:49], 0, v[162:163]
	global_load_lds_dwordx4 v[2:3], off
	v_lshl_add_u64 v[2:3], s[48:49], 0, v[158:159]
	s_mov_b32 m0, s58
	s_nop 0
	global_load_lds_dwordx4 v[2:3], off
	s_waitcnt vmcnt(6)
	s_barrier
	s_setprio 1
	v_mfma_f32_16x16x128_f8f6f4 v[86:89], v[188:195], v[26:33], 0
	v_mfma_f32_16x16x128_f8f6f4 v[82:85], v[202:209], v[26:33], 0
	v_mfma_f32_16x16x128_f8f6f4 v[54:57], v[188:195], v[34:41], 0
	v_mfma_f32_16x16x128_f8f6f4 v[50:53], v[202:209], v[34:41], 0
	v_mfma_f32_16x16x128_f8f6f4 v[38:41], v[188:195], v[210:217], 0
	v_mfma_f32_16x16x128_f8f6f4 v[34:37], v[202:209], v[210:217], 0
	v_mfma_f32_16x16x128_f8f6f4 v[30:33], v[188:195], v[232:239], 0
	v_mfma_f32_16x16x128_f8f6f4 v[26:29], v[202:209], v[232:239], 0
	s_setprio 0
	s_barrier
	ds_read_b128 v[2:5], v183
	ds_read_b128 v[6:9], v184
	ds_read_b128 v[10:13], v185
	ds_read_b128 v[14:17], v196
	s_add_u32 s48, s46, 0x40100
	s_addc_u32 s49, s47, 0
	s_mov_b32 m0, s59
	v_lshl_add_u64 v[154:155], s[48:49], 0, v[164:165]
	ds_read_b128 v[188:191], v0 offset:32768
	ds_read_b128 v[192:195], v0 offset:33792
	ds_read_b128 v[202:205], v0 offset:34816
	ds_read_b128 v[206:209], v0 offset:35840
	ds_read_b128 v[210:213], v0 offset:36864
	ds_read_b128 v[214:217], v0 offset:37888
	ds_read_b128 v[232:235], v0 offset:38912
	ds_read_b128 v[236:239], v0 offset:39936
	global_load_lds_dwordx4 v[154:155], off
	v_lshl_add_u64 v[154:155], s[48:49], 0, v[160:161]
	s_mov_b32 m0, s60
	s_nop 0
	global_load_lds_dwordx4 v[154:155], off
	s_waitcnt lgkmcnt(8)
	s_barrier
	s_waitcnt lgkmcnt(0)
	s_setprio 1
	s_waitcnt lgkmcnt(0)
	v_mfma_f32_16x16x128_f8f6f4 v[134:137], v[2:9], v[188:195], v[134:137]
	v_mfma_f32_16x16x128_f8f6f4 v[130:133], v[10:17], v[188:195], v[130:133]
	v_mfma_f32_16x16x128_f8f6f4 v[118:121], v[2:9], v[202:209], v[118:121]
	v_mfma_f32_16x16x128_f8f6f4 v[114:117], v[10:17], v[202:209], v[114:117]
	v_mfma_f32_16x16x128_f8f6f4 v[102:105], v[2:9], v[210:217], v[102:105]
	v_mfma_f32_16x16x128_f8f6f4 v[98:101], v[10:17], v[210:217], v[98:101]
	v_mfma_f32_16x16x128_f8f6f4 v[74:77], v[2:9], v[232:239], v[74:77]
	v_mfma_f32_16x16x128_f8f6f4 v[66:69], v[10:17], v[232:239], v[66:69]
	s_setprio 0
	s_barrier
	s_mov_b64 s[48:49], 0x180
	s_mov_b32 m0, s62
	v_lshl_add_u64 v[150:151], v[150:151], 0, s[48:49]
	ds_read_b128 v[240:243], v197
	ds_read_b128 v[244:247], v198
	ds_read_b128 v[166:169], v199
	ds_read_b128 v[170:173], v200
	global_load_lds_dwordx4 v[150:151], off
	v_lshl_add_u64 v[150:151], v[152:153], 0, s[48:49]
	s_mov_b32 m0, s63
	s_nop 0
	global_load_lds_dwordx4 v[150:151], off
	s_barrier
	s_waitcnt lgkmcnt(0)
	s_setprio 1
	s_waitcnt lgkmcnt(0)
	v_mfma_f32_16x16x128_f8f6f4 v[142:145], v[240:247], v[188:195], v[142:145]
	v_mfma_f32_16x16x128_f8f6f4 v[138:141], v[166:173], v[188:195], v[138:141]
	v_mfma_f32_16x16x128_f8f6f4 v[126:129], v[240:247], v[202:209], v[126:129]
	v_mfma_f32_16x16x128_f8f6f4 v[122:125], v[166:173], v[202:209], v[122:125]
	v_mfma_f32_16x16x128_f8f6f4 v[110:113], v[240:247], v[210:217], v[110:113]
	v_mfma_f32_16x16x128_f8f6f4 v[106:109], v[166:173], v[210:217], v[106:109]
	v_mfma_f32_16x16x128_f8f6f4 v[78:81], v[240:247], v[232:239], v[78:81]
	v_mfma_f32_16x16x128_f8f6f4 v[70:73], v[166:173], v[232:239], v[70:73]
	s_setprio 0
	s_mov_b32 m0, s64
	v_lshl_add_u64 v[146:147], v[146:147], 0, s[48:49]
	s_barrier
	ds_read_b128 v[150:153], v0 offset:49152
	ds_read_b128 v[154:157], v0 offset:50176
	ds_read_b128 v[188:191], v0 offset:51200
	ds_read_b128 v[192:195], v0 offset:52224
	ds_read_b128 v[202:205], v0 offset:53248
	ds_read_b128 v[206:209], v0 offset:54272
	ds_read_b128 v[210:213], v0 offset:55296
	ds_read_b128 v[214:217], v0 offset:56320
	global_load_lds_dwordx4 v[146:147], off
	v_lshl_add_u64 v[146:147], v[148:149], 0, s[48:49]
	s_mov_b32 m0, s65
	s_nop 0
	global_load_lds_dwordx4 v[146:147], off
	s_barrier
	s_waitcnt lgkmcnt(0)
	s_setprio 1
	s_waitcnt lgkmcnt(0)
	v_mfma_f32_16x16x128_f8f6f4 v[94:97], v[2:9], v[150:157], v[94:97]
	v_mfma_f32_16x16x128_f8f6f4 v[90:93], v[10:17], v[150:157], v[90:93]
	v_mfma_f32_16x16x128_f8f6f4 v[62:65], v[2:9], v[188:195], v[62:65]
	v_mfma_f32_16x16x128_f8f6f4 v[58:61], v[10:17], v[188:195], v[58:61]
	v_mfma_f32_16x16x128_f8f6f4 v[46:49], v[2:9], v[202:209], v[46:49]
	v_mfma_f32_16x16x128_f8f6f4 v[42:45], v[10:17], v[202:209], v[42:45]
	v_mfma_f32_16x16x128_f8f6f4 v[22:25], v[2:9], v[210:217], v[22:25]
	v_mfma_f32_16x16x128_f8f6f4 v[18:21], v[10:17], v[210:217], v[18:21]
	s_setprio 0
	s_barrier
	s_add_u32 s48, s44, 0x40180
	s_addc_u32 s49, s45, 0
	s_mov_b32 m0, s66
	v_lshl_add_u64 v[2:3], s[48:49], 0, v[162:163]
	global_load_lds_dwordx4 v[2:3], off
	v_lshl_add_u64 v[2:3], s[48:49], 0, v[158:159]
	s_mov_b32 m0, s67
	s_nop 0
	global_load_lds_dwordx4 v[2:3], off
	s_waitcnt vmcnt(6)
	s_barrier
	s_setprio 1
	v_mfma_f32_16x16x128_f8f6f4 v[86:89], v[240:247], v[150:157], v[86:89]
	v_mfma_f32_16x16x128_f8f6f4 v[82:85], v[166:173], v[150:157], v[82:85]
	v_mfma_f32_16x16x128_f8f6f4 v[54:57], v[240:247], v[188:195], v[54:57]
	v_mfma_f32_16x16x128_f8f6f4 v[50:53], v[166:173], v[188:195], v[50:53]
	v_mfma_f32_16x16x128_f8f6f4 v[38:41], v[240:247], v[202:209], v[38:41]
	v_mfma_f32_16x16x128_f8f6f4 v[34:37], v[166:173], v[202:209], v[34:37]
	v_mfma_f32_16x16x128_f8f6f4 v[30:33], v[240:247], v[210:217], v[30:33]
	v_mfma_f32_16x16x128_f8f6f4 v[26:29], v[166:173], v[210:217], v[26:29]
	s_setprio 0
	s_add_u32 s46, s46, 0x40180
	s_addc_u32 s47, s47, 0
	s_add_u32 s75, s44, 0x200
	s_addc_u32 s76, s45, 0
	s_mov_b32 s77, 0
	s_barrier
.LBB0_834:
	ds_read_b128 v[10:13], v175
	ds_read_b128 v[14:17], v176
	ds_read_b128 v[146:149], v177
	ds_read_b128 v[150:153], v178
	s_add_u32 s44, s46, 0xfffc0080
	s_addc_u32 s45, s47, -1
	s_cmp_eq_u32 s77, 12
	s_cselect_b32 s49, s21, s45
	s_cselect_b32 s48, s71, s44
	s_cselect_b32 s45, s13, s76
	s_cselect_b32 s44, s72, s75
	s_mov_b32 m0, s73
	v_lshl_add_u64 v[2:3], s[46:47], 0, v[218:219]
	ds_read_b128 v[166:169], v0
	ds_read_b128 v[170:173], v0 offset:1024
	ds_read_b128 v[188:191], v0 offset:2048
	ds_read_b128 v[192:195], v0 offset:3072
	ds_read_b128 v[202:205], v0 offset:4096
	ds_read_b128 v[206:209], v0 offset:5120
	ds_read_b128 v[210:213], v0 offset:6144
	ds_read_b128 v[214:217], v0 offset:7168
	global_load_lds_dwordx4 v[2:3], off
	v_lshl_add_u64 v[2:3], s[46:47], 0, v[220:221]
	s_mov_b32 m0, s74
	s_nop 0
	global_load_lds_dwordx4 v[2:3], off
	s_waitcnt lgkmcnt(8)
	s_barrier
	s_waitcnt lgkmcnt(0)
	s_setprio 1
	s_waitcnt lgkmcnt(0)
	v_mfma_f32_16x16x128_f8f6f4 v[134:137], v[10:17], v[166:173], v[134:137]
	v_mfma_f32_16x16x128_f8f6f4 v[130:133], v[146:153], v[166:173], v[130:133]
	v_mfma_f32_16x16x128_f8f6f4 v[118:121], v[10:17], v[188:195], v[118:121]
	v_mfma_f32_16x16x128_f8f6f4 v[114:117], v[146:153], v[188:195], v[114:117]
	v_mfma_f32_16x16x128_f8f6f4 v[102:105], v[10:17], v[202:209], v[102:105]
	v_mfma_f32_16x16x128_f8f6f4 v[98:101], v[146:153], v[202:209], v[98:101]
	v_mfma_f32_16x16x128_f8f6f4 v[74:77], v[10:17], v[210:217], v[74:77]
	v_mfma_f32_16x16x128_f8f6f4 v[66:69], v[146:153], v[210:217], v[66:69]
	s_setprio 0
	s_barrier
	s_mov_b32 m0, s54
	v_lshl_add_u64 v[6:7], s[44:45], 0, v[162:163]
	ds_read_b128 v[232:235], v179
	ds_read_b128 v[236:239], v180
	ds_read_b128 v[240:243], v181
	ds_read_b128 v[244:247], v182
	global_load_lds_dwordx4 v[6:7], off
	v_lshl_add_u64 v[8:9], s[44:45], 0, v[158:159]
	s_mov_b32 m0, s55
	s_nop 0
	global_load_lds_dwordx4 v[8:9], off
	s_barrier
	s_waitcnt lgkmcnt(0)
	s_setprio 1
	s_waitcnt lgkmcnt(0)
	v_mfma_f32_16x16x128_f8f6f4 v[142:145], v[232:239], v[166:173], v[142:145]
	v_mfma_f32_16x16x128_f8f6f4 v[138:141], v[240:247], v[166:173], v[138:141]
	v_mfma_f32_16x16x128_f8f6f4 v[126:129], v[232:239], v[188:195], v[126:129]
	v_mfma_f32_16x16x128_f8f6f4 v[122:125], v[240:247], v[188:195], v[122:125]
	v_mfma_f32_16x16x128_f8f6f4 v[110:113], v[232:239], v[202:209], v[110:113]
	v_mfma_f32_16x16x128_f8f6f4 v[106:109], v[240:247], v[202:209], v[106:109]
	v_mfma_f32_16x16x128_f8f6f4 v[78:81], v[232:239], v[210:217], v[78:81]
	v_mfma_f32_16x16x128_f8f6f4 v[70:73], v[240:247], v[210:217], v[70:73]
	s_setprio 0
	s_mov_b32 m0, s53
	v_lshl_add_u64 v[2:3], s[48:49], 0, v[164:165]
	s_barrier
	ds_read_b128 v[166:169], v0 offset:16384
	ds_read_b128 v[170:173], v0 offset:17408
	ds_read_b128 v[188:191], v0 offset:18432
	ds_read_b128 v[192:195], v0 offset:19456
	ds_read_b128 v[202:205], v0 offset:20480
	ds_read_b128 v[206:209], v0 offset:21504
	ds_read_b128 v[210:213], v0 offset:22528
	ds_read_b128 v[214:217], v0 offset:23552
	global_load_lds_dwordx4 v[2:3], off
	v_lshl_add_u64 v[4:5], s[48:49], 0, v[160:161]
	s_mov_b32 m0, s56
	s_nop 0
	global_load_lds_dwordx4 v[4:5], off
	s_barrier
	s_waitcnt lgkmcnt(0)
	s_setprio 1
	s_waitcnt lgkmcnt(0)
	v_mfma_f32_16x16x128_f8f6f4 v[94:97], v[10:17], v[166:173], v[94:97]
	v_mfma_f32_16x16x128_f8f6f4 v[90:93], v[146:153], v[166:173], v[90:93]
	v_mfma_f32_16x16x128_f8f6f4 v[62:65], v[10:17], v[188:195], v[62:65]
	v_mfma_f32_16x16x128_f8f6f4 v[58:61], v[146:153], v[188:195], v[58:61]
	v_mfma_f32_16x16x128_f8f6f4 v[46:49], v[10:17], v[202:209], v[46:49]
	v_mfma_f32_16x16x128_f8f6f4 v[42:45], v[146:153], v[202:209], v[42:45]
	v_mfma_f32_16x16x128_f8f6f4 v[22:25], v[10:17], v[210:217], v[22:25]
	v_mfma_f32_16x16x128_f8f6f4 v[18:21], v[146:153], v[210:217], v[18:21]
	s_setprio 0
	s_barrier
	s_add_u32 s78, s44, 0x40000
	s_addc_u32 s79, s45, 0
	s_mov_b32 m0, s57
	v_lshl_add_u64 v[10:11], s[78:79], 0, v[162:163]
	global_load_lds_dwordx4 v[10:11], off
	v_lshl_add_u64 v[10:11], s[78:79], 0, v[158:159]
	s_mov_b32 m0, s58
	s_nop 0
	global_load_lds_dwordx4 v[10:11], off
	s_waitcnt vmcnt(6)
	s_barrier
	s_setprio 1
	v_mfma_f32_16x16x128_f8f6f4 v[86:89], v[232:239], v[166:173], v[86:89]
	v_mfma_f32_16x16x128_f8f6f4 v[82:85], v[240:247], v[166:173], v[82:85]
	v_mfma_f32_16x16x128_f8f6f4 v[54:57], v[232:239], v[188:195], v[54:57]
	v_mfma_f32_16x16x128_f8f6f4 v[50:53], v[240:247], v[188:195], v[50:53]
	v_mfma_f32_16x16x128_f8f6f4 v[38:41], v[232:239], v[202:209], v[38:41]
	v_mfma_f32_16x16x128_f8f6f4 v[34:37], v[240:247], v[202:209], v[34:37]
	v_mfma_f32_16x16x128_f8f6f4 v[30:33], v[232:239], v[210:217], v[30:33]
	v_mfma_f32_16x16x128_f8f6f4 v[26:29], v[240:247], v[210:217], v[26:29]
	s_setprio 0
	s_barrier
	ds_read_b128 v[10:13], v183
	ds_read_b128 v[14:17], v184
	ds_read_b128 v[146:149], v185
	ds_read_b128 v[150:153], v196
	s_add_u32 s48, s48, 0x40000
	s_addc_u32 s49, s49, 0
	s_mov_b32 m0, s59
	v_lshl_add_u64 v[154:155], s[48:49], 0, v[164:165]
	ds_read_b128 v[166:169], v0 offset:32768
	ds_read_b128 v[170:173], v0 offset:33792
	ds_read_b128 v[188:191], v0 offset:34816
	ds_read_b128 v[192:195], v0 offset:35840
	ds_read_b128 v[202:205], v0 offset:36864
	ds_read_b128 v[206:209], v0 offset:37888
	ds_read_b128 v[210:213], v0 offset:38912
	ds_read_b128 v[214:217], v0 offset:39936
	global_load_lds_dwordx4 v[154:155], off
	v_lshl_add_u64 v[154:155], s[48:49], 0, v[160:161]
	s_mov_b32 m0, s60
	s_nop 0
	global_load_lds_dwordx4 v[154:155], off
	s_waitcnt lgkmcnt(8)
	s_barrier
	s_waitcnt lgkmcnt(0)
	s_setprio 1
	s_waitcnt lgkmcnt(0)
	v_mfma_f32_16x16x128_f8f6f4 v[134:137], v[10:17], v[166:173], v[134:137]
	v_mfma_f32_16x16x128_f8f6f4 v[130:133], v[146:153], v[166:173], v[130:133]
	v_mfma_f32_16x16x128_f8f6f4 v[118:121], v[10:17], v[188:195], v[118:121]
	v_mfma_f32_16x16x128_f8f6f4 v[114:117], v[146:153], v[188:195], v[114:117]
	v_mfma_f32_16x16x128_f8f6f4 v[102:105], v[10:17], v[202:209], v[102:105]
	v_mfma_f32_16x16x128_f8f6f4 v[98:101], v[146:153], v[202:209], v[98:101]
	v_mfma_f32_16x16x128_f8f6f4 v[74:77], v[10:17], v[210:217], v[74:77]
	v_mfma_f32_16x16x128_f8f6f4 v[66:69], v[146:153], v[210:217], v[66:69]
	s_setprio 0
	s_barrier
	s_mov_b32 m0, s62
	v_lshl_add_u64 v[6:7], v[6:7], 0, s[24:25]
	ds_read_b128 v[232:235], v197
	ds_read_b128 v[236:239], v198
	ds_read_b128 v[240:243], v199
	ds_read_b128 v[244:247], v200
	global_load_lds_dwordx4 v[6:7], off
	v_lshl_add_u64 v[6:7], v[8:9], 0, s[24:25]
	s_mov_b32 m0, s63
	s_nop 0
	global_load_lds_dwordx4 v[6:7], off
	s_barrier
	s_waitcnt lgkmcnt(0)
	s_setprio 1
	s_waitcnt lgkmcnt(0)
	v_mfma_f32_16x16x128_f8f6f4 v[142:145], v[232:239], v[166:173], v[142:145]
	v_mfma_f32_16x16x128_f8f6f4 v[138:141], v[240:247], v[166:173], v[138:141]
	v_mfma_f32_16x16x128_f8f6f4 v[126:129], v[232:239], v[188:195], v[126:129]
	v_mfma_f32_16x16x128_f8f6f4 v[122:125], v[240:247], v[188:195], v[122:125]
	v_mfma_f32_16x16x128_f8f6f4 v[110:113], v[232:239], v[202:209], v[110:113]
	v_mfma_f32_16x16x128_f8f6f4 v[106:109], v[240:247], v[202:209], v[106:109]
	v_mfma_f32_16x16x128_f8f6f4 v[78:81], v[232:239], v[210:217], v[78:81]
	v_mfma_f32_16x16x128_f8f6f4 v[70:73], v[240:247], v[210:217], v[70:73]
	s_setprio 0
	s_mov_b32 m0, s64
	v_lshl_add_u64 v[2:3], v[2:3], 0, s[24:25]
	s_barrier
	ds_read_b128 v[166:169], v0 offset:49152
	ds_read_b128 v[170:173], v0 offset:50176
	ds_read_b128 v[188:191], v0 offset:51200
	ds_read_b128 v[192:195], v0 offset:52224
	ds_read_b128 v[202:205], v0 offset:53248
	ds_read_b128 v[206:209], v0 offset:54272
	ds_read_b128 v[210:213], v0 offset:55296
	ds_read_b128 v[214:217], v0 offset:56320
	global_load_lds_dwordx4 v[2:3], off
	v_lshl_add_u64 v[2:3], v[4:5], 0, s[24:25]
	s_mov_b32 m0, s65
	s_nop 0
	global_load_lds_dwordx4 v[2:3], off
	s_barrier
	s_waitcnt lgkmcnt(0)
	s_setprio 1
	s_waitcnt lgkmcnt(0)
	v_mfma_f32_16x16x128_f8f6f4 v[94:97], v[10:17], v[166:173], v[94:97]
	v_mfma_f32_16x16x128_f8f6f4 v[90:93], v[146:153], v[166:173], v[90:93]
	v_mfma_f32_16x16x128_f8f6f4 v[62:65], v[10:17], v[188:195], v[62:65]
	v_mfma_f32_16x16x128_f8f6f4 v[58:61], v[146:153], v[188:195], v[58:61]
	v_mfma_f32_16x16x128_f8f6f4 v[46:49], v[10:17], v[202:209], v[46:49]
	v_mfma_f32_16x16x128_f8f6f4 v[42:45], v[146:153], v[202:209], v[42:45]
	v_mfma_f32_16x16x128_f8f6f4 v[22:25], v[10:17], v[210:217], v[22:25]
	v_mfma_f32_16x16x128_f8f6f4 v[18:21], v[146:153], v[210:217], v[18:21]
	s_setprio 0
	s_barrier
	s_add_u32 s44, s44, 0x40080
	s_addc_u32 s45, s45, 0
	s_mov_b32 m0, s66
	v_lshl_add_u64 v[2:3], s[44:45], 0, v[162:163]
	global_load_lds_dwordx4 v[2:3], off
	v_lshl_add_u64 v[2:3], s[44:45], 0, v[158:159]
	s_mov_b32 m0, s67
	s_nop 0
	global_load_lds_dwordx4 v[2:3], off
	s_waitcnt vmcnt(6)
	s_barrier
	s_setprio 1
	v_mfma_f32_16x16x128_f8f6f4 v[86:89], v[232:239], v[166:173], v[86:89]
	v_mfma_f32_16x16x128_f8f6f4 v[82:85], v[240:247], v[166:173], v[82:85]
	v_mfma_f32_16x16x128_f8f6f4 v[54:57], v[232:239], v[188:195], v[54:57]
	v_mfma_f32_16x16x128_f8f6f4 v[50:53], v[240:247], v[188:195], v[50:53]
	v_mfma_f32_16x16x128_f8f6f4 v[38:41], v[232:239], v[202:209], v[38:41]
	v_mfma_f32_16x16x128_f8f6f4 v[34:37], v[240:247], v[202:209], v[34:37]
	v_mfma_f32_16x16x128_f8f6f4 v[30:33], v[232:239], v[210:217], v[30:33]
	v_mfma_f32_16x16x128_f8f6f4 v[26:29], v[240:247], v[210:217], v[26:29]
	s_setprio 0
	s_add_i32 s77, s77, 2
	s_add_u32 s46, s46, 0x100
	s_addc_u32 s47, s47, 0
	s_add_u32 s75, s75, 0x100
	s_addc_u32 s76, s76, 0
	s_cmp_gt_u32 s77, 13
	s_barrier
	s_cbranch_scc0 .LBB0_834
	s_nop 15
	s_nop 15
	v_mbcnt_lo_u32_b32 v0, -1, 0
	v_mbcnt_hi_u32_b32 v0, -1, v0
	v_readlane_b32 s13, v252, 51
	v_and_b32_e32 v202, 15, v0
	v_bfe_u32 v201, v0, 4, 2
	v_readlane_b32 s21, v252, 52
	s_mov_b64 s[44:45], -1
	s_and_b64 vcc, exec, s[8:9]
	s_cbranch_vccz .LBB0_837
	s_lshl_b32 s44, s69, 8
	s_ashr_i32 s45, s44, 31
	s_lshl_b32 s46, s21, 5
	s_lshl_b32 s48, s70, 8
	s_lshl_b32 s49, s13, 6
	s_ashr_i32 s47, s46, 31
	s_lshl_b64 s[44:45], s[44:45], 1
	s_add_u32 s71, s10, s44
	v_or_b32_e32 v5, s48, v202
	s_addc_u32 s73, s11, s45
	s_lshl_b64 s[46:47], s[46:47], 1
	s_add_u32 s72, s71, s46
	v_or_b32_e32 v203, s49, v202
	v_add_u32_e32 v6, s49, v5
	s_addc_u32 s73, s73, s47
	v_lshlrev_b32_e32 v0, 4, v201
	v_add_u32_e32 v188, s48, v203
	v_ashrrev_i32_e32 v7, 31, v6
	v_lshl_add_u64 v[2:3], s[72:73], 0, v[0:1]
	v_or_b32_e32 v4, 32, v188
	v_lshlrev_b64 v[8:9], 11, v[6:7]
	v_lshl_add_u64 v[8:9], v[2:3], 0, v[8:9]
	v_ashrrev_i32_e32 v5, 31, v4
	global_load_dwordx4 v[166:169], v[8:9], off
	v_lshlrev_b64 v[170:171], 11, v[4:5]
	v_lshl_add_u64 v[4:5], v[2:3], 0, v[170:171]
	global_load_dwordx4 v[14:17], v[4:5], off
	global_load_dwordx4 v[154:157], v[8:9], off offset:256
	global_load_dwordx4 v[10:13], v[4:5], off offset:256
	v_or_b32_e32 v4, 16, v6
	v_ashrrev_i32_e32 v5, 31, v4
	v_lshlrev_b64 v[4:5], 11, v[4:5]
	v_lshl_add_u64 v[4:5], v[2:3], 0, v[4:5]
	global_load_dwordx4 v[150:153], v[4:5], off
	v_or_b32_e32 v6, 48, v188
	v_ashrrev_i32_e32 v7, 31, v6
	v_lshlrev_b64 v[6:7], 11, v[6:7]
	v_lshl_add_u64 v[2:3], v[2:3], 0, v[6:7]
	global_load_dwordx4 v[6:9], v[2:3], off
	global_load_dwordx4 v[146:149], v[4:5], off offset:256
	s_nop 0
	global_load_dwordx4 v[2:5], v[2:3], off offset:256
	v_ashrrev_i32_e32 v189, 31, v188
	v_lshlrev_b64 v[188:189], 11, v[188:189]
	v_lshl_add_u64 v[188:189], s[6:7], 0, v[188:189]
	v_lshl_add_u64 v[188:189], v[188:189], 0, s[44:45]
	v_lshl_add_u64 v[188:189], v[188:189], 0, s[46:47]
	v_lshl_add_u64 v[188:189], v[188:189], 0, v[0:1]
	s_add_u32 s72, s10, s46
	s_addc_u32 s73, s11, s47
	s_or_b32 s71, s48, 16
	s_add_i32 s49, s48, s49
	v_or_b32_e32 v204, s49, v202
	v_lshl_add_u64 v[172:173], s[72:73], 0, v[0:1]
	v_lshl_add_u64 v[172:173], v[172:173], 0, s[44:45]
	v_lshl_add_u64 v[170:171], s[6:7], 0, v[170:171]
	v_lshl_add_u64 v[170:171], v[170:171], 0, s[44:45]
	v_lshl_add_u64 v[170:171], v[170:171], 0, s[46:47]
	v_lshl_add_u64 v[170:171], v[170:171], 0, v[0:1]
	s_or_b32 s49, s48, 48
	s_waitcnt vmcnt(0)
	v_lshlrev_b32_e32 v190, 16, v166
	v_and_b32_e32 v191, 0xffff0000, v166
	v_lshlrev_b32_e32 v166, 16, v167
	v_and_b32_e32 v167, 0xffff0000, v167
	v_lshlrev_b32_e32 v192, 16, v168
	v_and_b32_e32 v193, 0xffff0000, v168
	v_lshlrev_b32_e32 v168, 16, v169
	v_and_b32_e32 v169, 0xffff0000, v169
	v_pk_fma_f32 v[194:195], v[136:137], s[16:17], v[166:167] op_sel_hi:[1,0,1]
	v_pk_fma_f32 v[166:167], v[134:135], s[16:17], v[190:191] op_sel_hi:[1,0,1]
	v_pk_fma_f32 v[190:191], v[132:133], s[16:17], v[168:169] op_sel_hi:[1,0,1]
	v_pk_fma_f32 v[168:169], v[130:131], s[16:17], v[192:193] op_sel_hi:[1,0,1]
	v_cvt_pk_bf16_f32 v166, v166, v167
	v_cvt_pk_bf16_f32 v167, v194, v195
	v_cvt_pk_bf16_f32 v168, v168, v169
	v_cvt_pk_bf16_f32 v169, v190, v191
	global_store_dwordx4 v[188:189], v[166:169], off
	v_lshlrev_b32_e32 v192, 16, v16
	v_and_b32_e32 v193, 0xffff0000, v16
	v_lshlrev_b32_e32 v166, 16, v154
	v_and_b32_e32 v167, 0xffff0000, v154
	v_lshlrev_b32_e32 v154, 16, v155
	v_and_b32_e32 v155, 0xffff0000, v155
	v_lshlrev_b32_e32 v168, 16, v156
	v_and_b32_e32 v169, 0xffff0000, v156
	v_lshlrev_b32_e32 v156, 16, v157
	v_and_b32_e32 v157, 0xffff0000, v157
	v_pk_fma_f32 v[190:191], v[144:145], s[16:17], v[154:155] op_sel_hi:[1,0,1]
	v_pk_fma_f32 v[154:155], v[142:143], s[16:17], v[166:167] op_sel_hi:[1,0,1]
	v_pk_fma_f32 v[166:167], v[140:141], s[16:17], v[156:157] op_sel_hi:[1,0,1]
	v_pk_fma_f32 v[156:157], v[138:139], s[16:17], v[168:169] op_sel_hi:[1,0,1]
	v_cvt_pk_bf16_f32 v154, v154, v155
	v_cvt_pk_bf16_f32 v155, v190, v191
	v_cvt_pk_bf16_f32 v156, v156, v157
	v_cvt_pk_bf16_f32 v157, v166, v167
	global_store_dwordx4 v[188:189], v[154:157], off offset:256
	v_lshlrev_b32_e32 v190, 16, v14
	v_and_b32_e32 v191, 0xffff0000, v14
	v_lshlrev_b32_e32 v154, 16, v150
	v_and_b32_e32 v155, 0xffff0000, v150
	v_lshlrev_b32_e32 v150, 16, v151
	v_and_b32_e32 v151, 0xffff0000, v151
	v_lshlrev_b32_e32 v156, 16, v152
	v_and_b32_e32 v157, 0xffff0000, v152
	v_lshlrev_b32_e32 v152, 16, v153
	v_and_b32_e32 v153, 0xffff0000, v153
	v_pk_fma_f32 v[166:167], v[120:121], s[16:17], v[150:151] op_sel_hi:[1,0,1]
	v_pk_fma_f32 v[150:151], v[118:119], s[16:17], v[154:155] op_sel_hi:[1,0,1]
	v_pk_fma_f32 v[154:155], v[116:117], s[16:17], v[152:153] op_sel_hi:[1,0,1]
	v_pk_fma_f32 v[152:153], v[114:115], s[16:17], v[156:157] op_sel_hi:[1,0,1]
	v_cvt_pk_bf16_f32 v150, v150, v151
	v_cvt_pk_bf16_f32 v152, v152, v153
	v_cvt_pk_bf16_f32 v153, v154, v155
	v_add_u32_e32 v154, s71, v203
	v_ashrrev_i32_e32 v155, 31, v154
	v_lshlrev_b64 v[154:155], 11, v[154:155]
	v_lshl_add_u64 v[154:155], s[6:7], 0, v[154:155]
	v_lshl_add_u64 v[154:155], v[154:155], 0, s[44:45]
	v_lshl_add_u64 v[154:155], v[154:155], 0, s[46:47]
	v_cvt_pk_bf16_f32 v151, v166, v167
	v_lshl_add_u64 v[154:155], v[154:155], 0, v[0:1]
	global_store_dwordx4 v[154:155], v[150:153], off
	v_lshlrev_b32_e32 v14, 16, v15
	v_and_b32_e32 v15, 0xffff0000, v15
	v_lshlrev_b32_e32 v150, 16, v146
	v_and_b32_e32 v151, 0xffff0000, v146
	v_lshlrev_b32_e32 v146, 16, v147
	v_and_b32_e32 v147, 0xffff0000, v147
	v_lshlrev_b32_e32 v152, 16, v148
	v_and_b32_e32 v153, 0xffff0000, v148
	v_lshlrev_b32_e32 v148, 16, v149
	v_and_b32_e32 v149, 0xffff0000, v149
	v_pk_fma_f32 v[156:157], v[128:129], s[16:17], v[146:147] op_sel_hi:[1,0,1]
	v_pk_fma_f32 v[146:147], v[126:127], s[16:17], v[150:151] op_sel_hi:[1,0,1]
	v_pk_fma_f32 v[150:151], v[124:125], s[16:17], v[148:149] op_sel_hi:[1,0,1]
	v_pk_fma_f32 v[148:149], v[122:123], s[16:17], v[152:153] op_sel_hi:[1,0,1]
	v_cvt_pk_bf16_f32 v146, v146, v147
	v_cvt_pk_bf16_f32 v147, v156, v157
	v_cvt_pk_bf16_f32 v148, v148, v149
	v_cvt_pk_bf16_f32 v149, v150, v151
	global_store_dwordx4 v[154:155], v[146:149], off offset:256
	v_lshlrev_b32_e32 v16, 16, v17
	v_and_b32_e32 v17, 0xffff0000, v17
	v_add_u32_e32 v146, 0x80, v204
	v_ashrrev_i32_e32 v147, 31, v146
	v_lshlrev_b64 v[188:189], 11, v[146:147]
	v_lshl_add_u64 v[146:147], v[172:173], 0, v[188:189]
	global_load_dwordx4 v[150:153], v[146:147], off
	global_load_dwordx4 v[154:157], v[146:147], off offset:256
	v_add_u32_e32 v146, 0x90, v204
	v_ashrrev_i32_e32 v147, 31, v146
	v_lshlrev_b64 v[146:147], 11, v[146:147]
	v_pk_fma_f32 v[194:195], v[104:105], s[16:17], v[14:15] op_sel_hi:[1,0,1]
	v_pk_fma_f32 v[14:15], v[102:103], s[16:17], v[190:191] op_sel_hi:[1,0,1]
	v_pk_fma_f32 v[190:191], v[100:101], s[16:17], v[16:17] op_sel_hi:[1,0,1]
	v_pk_fma_f32 v[16:17], v[98:99], s[16:17], v[192:193] op_sel_hi:[1,0,1]
	v_lshl_add_u64 v[146:147], v[172:173], 0, v[146:147]
	v_cvt_pk_bf16_f32 v14, v14, v15
	v_cvt_pk_bf16_f32 v15, v194, v195
	v_cvt_pk_bf16_f32 v16, v16, v17
	v_cvt_pk_bf16_f32 v17, v190, v191
	global_load_dwordx4 v[166:169], v[146:147], off
	s_nop 0
	global_load_dwordx4 v[146:149], v[146:147], off offset:256
	global_store_dwordx4 v[170:171], v[14:17], off
	v_add_u32_e32 v192, 0x80, v203
	s_nop 0
	v_lshlrev_b32_e32 v14, 16, v10
	v_and_b32_e32 v15, 0xffff0000, v10
	v_lshlrev_b32_e32 v10, 16, v11
	v_and_b32_e32 v11, 0xffff0000, v11
	v_lshlrev_b32_e32 v16, 16, v12
	v_and_b32_e32 v17, 0xffff0000, v12
	v_lshlrev_b32_e32 v12, 16, v13
	v_and_b32_e32 v13, 0xffff0000, v13
	v_pk_fma_f32 v[190:191], v[112:113], s[16:17], v[10:11] op_sel_hi:[1,0,1]
	v_pk_fma_f32 v[10:11], v[110:111], s[16:17], v[14:15] op_sel_hi:[1,0,1]
	v_pk_fma_f32 v[14:15], v[108:109], s[16:17], v[12:13] op_sel_hi:[1,0,1]
	v_pk_fma_f32 v[12:13], v[106:107], s[16:17], v[16:17] op_sel_hi:[1,0,1]
	v_cvt_pk_bf16_f32 v10, v10, v11
	v_cvt_pk_bf16_f32 v11, v190, v191
	v_cvt_pk_bf16_f32 v12, v12, v13
	v_cvt_pk_bf16_f32 v13, v14, v15
	global_store_dwordx4 v[170:171], v[10:13], off offset:256
	s_waitcnt vmcnt(0)
	v_lshlrev_b32_e32 v170, 16, v150
	v_lshlrev_b32_e32 v10, 16, v6
	v_and_b32_e32 v11, 0xffff0000, v6
	v_lshlrev_b32_e32 v6, 16, v7
	v_and_b32_e32 v7, 0xffff0000, v7
	v_lshlrev_b32_e32 v12, 16, v8
	v_and_b32_e32 v13, 0xffff0000, v8
	v_lshlrev_b32_e32 v8, 16, v9
	v_and_b32_e32 v9, 0xffff0000, v9
	v_pk_fma_f32 v[14:15], v[76:77], s[16:17], v[6:7] op_sel_hi:[1,0,1]
	v_pk_fma_f32 v[6:7], v[74:75], s[16:17], v[10:11] op_sel_hi:[1,0,1]
	v_pk_fma_f32 v[10:11], v[68:69], s[16:17], v[8:9] op_sel_hi:[1,0,1]
	v_pk_fma_f32 v[8:9], v[66:67], s[16:17], v[12:13] op_sel_hi:[1,0,1]
	v_cvt_pk_bf16_f32 v6, v6, v7
	v_cvt_pk_bf16_f32 v8, v8, v9
	v_cvt_pk_bf16_f32 v9, v10, v11
	v_add_u32_e32 v10, s49, v203
	v_ashrrev_i32_e32 v11, 31, v10
	v_lshlrev_b64 v[10:11], 11, v[10:11]
	v_lshl_add_u64 v[10:11], s[6:7], 0, v[10:11]
	v_lshl_add_u64 v[10:11], v[10:11], 0, s[44:45]
	v_lshl_add_u64 v[10:11], v[10:11], 0, s[46:47]
	v_cvt_pk_bf16_f32 v7, v14, v15
	v_lshl_add_u64 v[10:11], v[10:11], 0, v[0:1]
	global_store_dwordx4 v[10:11], v[6:9], off
	v_and_b32_e32 v171, 0xffff0000, v150
	v_lshlrev_b32_e32 v150, 16, v151
	v_lshlrev_b32_e32 v6, 16, v2
	v_and_b32_e32 v7, 0xffff0000, v2
	v_lshlrev_b32_e32 v2, 16, v3
	v_and_b32_e32 v3, 0xffff0000, v3
	v_lshlrev_b32_e32 v8, 16, v4
	v_and_b32_e32 v9, 0xffff0000, v4
	v_lshlrev_b32_e32 v4, 16, v5
	v_and_b32_e32 v5, 0xffff0000, v5
	v_pk_fma_f32 v[12:13], v[80:81], s[16:17], v[2:3] op_sel_hi:[1,0,1]
	v_pk_fma_f32 v[2:3], v[78:79], s[16:17], v[6:7] op_sel_hi:[1,0,1]
	v_pk_fma_f32 v[6:7], v[72:73], s[16:17], v[4:5] op_sel_hi:[1,0,1]
	v_pk_fma_f32 v[4:5], v[70:71], s[16:17], v[8:9] op_sel_hi:[1,0,1]
	v_cvt_pk_bf16_f32 v2, v2, v3
	v_cvt_pk_bf16_f32 v3, v12, v13
	v_cvt_pk_bf16_f32 v4, v4, v5
	v_cvt_pk_bf16_f32 v5, v6, v7
	global_store_dwordx4 v[10:11], v[2:5], off offset:256
	v_and_b32_e32 v151, 0xffff0000, v151
	v_pk_fma_f32 v[190:191], v[96:97], s[16:17], v[150:151] op_sel_hi:[1,0,1]
	v_add_u32_e32 v2, 0xa0, v204
	v_ashrrev_i32_e32 v3, 31, v2
	v_lshlrev_b64 v[2:3], 11, v[2:3]
	v_lshl_add_u64 v[2:3], v[172:173], 0, v[2:3]
	global_load_dwordx4 v[6:9], v[2:3], off
	global_load_dwordx4 v[10:13], v[2:3], off offset:256
	v_add_u32_e32 v2, 0xb0, v204
	v_ashrrev_i32_e32 v3, 31, v2
	v_lshlrev_b64 v[2:3], 11, v[2:3]
	v_lshl_add_u64 v[2:3], v[172:173], 0, v[2:3]
	global_load_dwordx4 v[14:17], v[2:3], off
	s_nop 0
	global_load_dwordx4 v[2:5], v[2:3], off offset:256
	v_lshlrev_b32_e32 v172, 16, v152
	v_and_b32_e32 v173, 0xffff0000, v152
	v_lshlrev_b32_e32 v152, 16, v153
	v_and_b32_e32 v153, 0xffff0000, v153
	v_pk_fma_f32 v[150:151], v[94:95], s[16:17], v[170:171] op_sel_hi:[1,0,1]
	v_pk_fma_f32 v[170:171], v[92:93], s[16:17], v[152:153] op_sel_hi:[1,0,1]
	v_pk_fma_f32 v[152:153], v[90:91], s[16:17], v[172:173] op_sel_hi:[1,0,1]
	v_cvt_pk_bf16_f32 v150, v150, v151
	v_cvt_pk_bf16_f32 v152, v152, v153
	v_cvt_pk_bf16_f32 v153, v170, v171
	v_lshl_add_u64 v[170:171], s[6:7], 0, v[188:189]
	v_lshl_add_u64 v[170:171], v[170:171], 0, s[44:45]
	v_lshl_add_u64 v[170:171], v[170:171], 0, s[46:47]
	v_cvt_pk_bf16_f32 v151, v190, v191
	v_lshl_add_u64 v[170:171], v[170:171], 0, v[0:1]
	global_store_dwordx4 v[170:171], v[150:153], off
	s_nop 1
	v_lshlrev_b32_e32 v150, 16, v154
	v_and_b32_e32 v151, 0xffff0000, v154
	v_lshlrev_b32_e32 v152, 16, v155
	v_and_b32_e32 v153, 0xffff0000, v155
	v_lshlrev_b32_e32 v154, 16, v156
	v_and_b32_e32 v155, 0xffff0000, v156
	v_lshlrev_b32_e32 v156, 16, v157
	v_and_b32_e32 v157, 0xffff0000, v157
	v_pk_fma_f32 v[152:153], v[88:89], s[16:17], v[152:153] op_sel_hi:[1,0,1]
	v_pk_fma_f32 v[150:151], v[86:87], s[16:17], v[150:151] op_sel_hi:[1,0,1]
	v_pk_fma_f32 v[156:157], v[84:85], s[16:17], v[156:157] op_sel_hi:[1,0,1]
	v_pk_fma_f32 v[154:155], v[82:83], s[16:17], v[154:155] op_sel_hi:[1,0,1]
	v_cvt_pk_bf16_f32 v150, v150, v151
	v_cvt_pk_bf16_f32 v151, v152, v153
	v_cvt_pk_bf16_f32 v152, v154, v155
	v_cvt_pk_bf16_f32 v153, v156, v157
	global_store_dwordx4 v[170:171], v[150:153], off offset:256
	v_lshlrev_b32_e32 v154, 16, v168
	v_and_b32_e32 v155, 0xffff0000, v168
	v_lshlrev_b32_e32 v150, 16, v166
	v_and_b32_e32 v151, 0xffff0000, v166
	v_lshlrev_b32_e32 v152, 16, v167
	v_and_b32_e32 v153, 0xffff0000, v167
	v_pk_fma_f32 v[152:153], v[64:65], s[16:17], v[152:153] op_sel_hi:[1,0,1]
	v_pk_fma_f32 v[150:151], v[62:63], s[16:17], v[150:151] op_sel_hi:[1,0,1]
	v_pk_fma_f32 v[154:155], v[58:59], s[16:17], v[154:155] op_sel_hi:[1,0,1]
	v_cvt_pk_bf16_f32 v150, v150, v151
	v_cvt_pk_bf16_f32 v151, v152, v153
	v_cvt_pk_bf16_f32 v152, v154, v155
	v_add_u32_e32 v154, s71, v192
	v_ashrrev_i32_e32 v155, 31, v154
	v_lshlrev_b64 v[154:155], 11, v[154:155]
	v_lshl_add_u64 v[154:155], s[6:7], 0, v[154:155]
	v_lshlrev_b32_e32 v156, 16, v169
	v_and_b32_e32 v157, 0xffff0000, v169
	v_lshl_add_u64 v[154:155], v[154:155], 0, s[44:45]
	v_pk_fma_f32 v[156:157], v[60:61], s[16:17], v[156:157] op_sel_hi:[1,0,1]
	v_lshl_add_u64 v[154:155], v[154:155], 0, s[46:47]
	v_cvt_pk_bf16_f32 v153, v156, v157
	v_lshl_add_u64 v[154:155], v[154:155], 0, v[0:1]
	global_store_dwordx4 v[154:155], v[150:153], off
	s_nop 1
	v_lshlrev_b32_e32 v150, 16, v146
	v_and_b32_e32 v151, 0xffff0000, v146
	v_lshlrev_b32_e32 v146, 16, v147
	v_and_b32_e32 v147, 0xffff0000, v147
	v_lshlrev_b32_e32 v152, 16, v148
	v_and_b32_e32 v153, 0xffff0000, v148
	v_lshlrev_b32_e32 v148, 16, v149
	v_and_b32_e32 v149, 0xffff0000, v149
	v_pk_fma_f32 v[156:157], v[56:57], s[16:17], v[146:147] op_sel_hi:[1,0,1]
	v_pk_fma_f32 v[146:147], v[54:55], s[16:17], v[150:151] op_sel_hi:[1,0,1]
	v_pk_fma_f32 v[150:151], v[52:53], s[16:17], v[148:149] op_sel_hi:[1,0,1]
	v_pk_fma_f32 v[148:149], v[50:51], s[16:17], v[152:153] op_sel_hi:[1,0,1]
	v_cvt_pk_bf16_f32 v146, v146, v147
	v_cvt_pk_bf16_f32 v147, v156, v157
	v_cvt_pk_bf16_f32 v148, v148, v149
	v_cvt_pk_bf16_f32 v149, v150, v151
	global_store_dwordx4 v[154:155], v[146:149], off offset:256
	s_waitcnt vmcnt(0)
	s_nop 0
	v_lshlrev_b32_e32 v146, 16, v6
	v_and_b32_e32 v147, 0xffff0000, v6
	v_lshlrev_b32_e32 v6, 16, v7
	v_and_b32_e32 v7, 0xffff0000, v7
	v_lshlrev_b32_e32 v148, 16, v8
	v_and_b32_e32 v149, 0xffff0000, v8
	v_lshlrev_b32_e32 v8, 16, v9
	v_and_b32_e32 v9, 0xffff0000, v9
	v_pk_fma_f32 v[150:151], v[48:49], s[16:17], v[6:7] op_sel_hi:[1,0,1]
	v_pk_fma_f32 v[6:7], v[46:47], s[16:17], v[146:147] op_sel_hi:[1,0,1]
	v_pk_fma_f32 v[146:147], v[44:45], s[16:17], v[8:9] op_sel_hi:[1,0,1]
	v_pk_fma_f32 v[8:9], v[42:43], s[16:17], v[148:149] op_sel_hi:[1,0,1]
	v_cvt_pk_bf16_f32 v6, v6, v7
	v_cvt_pk_bf16_f32 v8, v8, v9
	v_cvt_pk_bf16_f32 v9, v146, v147
	v_add_u32_e32 v146, s48, v192
	v_or_b32_e32 v146, 32, v146
	v_ashrrev_i32_e32 v147, 31, v146
	v_lshlrev_b64 v[146:147], 11, v[146:147]
	v_lshl_add_u64 v[146:147], s[6:7], 0, v[146:147]
	v_lshl_add_u64 v[146:147], v[146:147], 0, s[44:45]
	v_lshl_add_u64 v[146:147], v[146:147], 0, s[46:47]
	v_cvt_pk_bf16_f32 v7, v150, v151
	v_lshl_add_u64 v[146:147], v[146:147], 0, v[0:1]
	global_store_dwordx4 v[146:147], v[6:9], off
	s_nop 1
	v_lshlrev_b32_e32 v6, 16, v10
	v_and_b32_e32 v7, 0xffff0000, v10
	v_lshlrev_b32_e32 v8, 16, v11
	v_and_b32_e32 v9, 0xffff0000, v11
	v_lshlrev_b32_e32 v10, 16, v12
	v_and_b32_e32 v11, 0xffff0000, v12
	v_lshlrev_b32_e32 v12, 16, v13
	v_and_b32_e32 v13, 0xffff0000, v13
	v_pk_fma_f32 v[8:9], v[40:41], s[16:17], v[8:9] op_sel_hi:[1,0,1]
	v_pk_fma_f32 v[6:7], v[38:39], s[16:17], v[6:7] op_sel_hi:[1,0,1]
	v_pk_fma_f32 v[12:13], v[36:37], s[16:17], v[12:13] op_sel_hi:[1,0,1]
	v_pk_fma_f32 v[10:11], v[34:35], s[16:17], v[10:11] op_sel_hi:[1,0,1]
	v_cvt_pk_bf16_f32 v6, v6, v7
	v_cvt_pk_bf16_f32 v7, v8, v9
	v_cvt_pk_bf16_f32 v8, v10, v11
	v_cvt_pk_bf16_f32 v9, v12, v13
	global_store_dwordx4 v[146:147], v[6:9], off offset:256
	v_lshlrev_b32_e32 v10, 16, v16
	v_and_b32_e32 v11, 0xffff0000, v16
	v_lshlrev_b32_e32 v6, 16, v14
	v_and_b32_e32 v7, 0xffff0000, v14
	v_lshlrev_b32_e32 v8, 16, v15
	v_and_b32_e32 v9, 0xffff0000, v15
	v_pk_fma_f32 v[8:9], v[24:25], s[16:17], v[8:9] op_sel_hi:[1,0,1]
	v_pk_fma_f32 v[6:7], v[22:23], s[16:17], v[6:7] op_sel_hi:[1,0,1]
	v_pk_fma_f32 v[10:11], v[18:19], s[16:17], v[10:11] op_sel_hi:[1,0,1]
	v_cvt_pk_bf16_f32 v6, v6, v7
	v_cvt_pk_bf16_f32 v7, v8, v9
	v_cvt_pk_bf16_f32 v8, v10, v11
	v_add_u32_e32 v10, s49, v192
	v_ashrrev_i32_e32 v11, 31, v10
	v_lshlrev_b64 v[10:11], 11, v[10:11]
	v_lshl_add_u64 v[10:11], s[6:7], 0, v[10:11]
	v_lshlrev_b32_e32 v12, 16, v17
	v_and_b32_e32 v13, 0xffff0000, v17
	v_lshl_add_u64 v[10:11], v[10:11], 0, s[44:45]
	v_pk_fma_f32 v[12:13], v[20:21], s[16:17], v[12:13] op_sel_hi:[1,0,1]
	v_lshl_add_u64 v[10:11], v[10:11], 0, s[46:47]
	v_cvt_pk_bf16_f32 v9, v12, v13
	v_lshl_add_u64 v[10:11], v[10:11], 0, v[0:1]
	global_store_dwordx4 v[10:11], v[6:9], off
	s_mov_b64 s[44:45], 0
	s_nop 0
	v_lshlrev_b32_e32 v6, 16, v2
	v_and_b32_e32 v7, 0xffff0000, v2
	v_lshlrev_b32_e32 v2, 16, v3
	v_and_b32_e32 v3, 0xffff0000, v3
	v_lshlrev_b32_e32 v8, 16, v4
	v_and_b32_e32 v9, 0xffff0000, v4
	v_lshlrev_b32_e32 v4, 16, v5
	v_and_b32_e32 v5, 0xffff0000, v5
	v_pk_fma_f32 v[12:13], v[32:33], s[16:17], v[2:3] op_sel_hi:[1,0,1]
	v_pk_fma_f32 v[2:3], v[30:31], s[16:17], v[6:7] op_sel_hi:[1,0,1]
	v_pk_fma_f32 v[6:7], v[28:29], s[16:17], v[4:5] op_sel_hi:[1,0,1]
	v_pk_fma_f32 v[4:5], v[26:27], s[16:17], v[8:9] op_sel_hi:[1,0,1]
	v_cvt_pk_bf16_f32 v2, v2, v3
	v_cvt_pk_bf16_f32 v3, v12, v13
	v_cvt_pk_bf16_f32 v4, v4, v5
	v_cvt_pk_bf16_f32 v5, v6, v7
	global_store_dwordx4 v[10:11], v[2:5], off offset:256

.LBB0_1474:
	v_mov_b64_e32 v[2:3], 0x200
	s_ashr_i32 s15, s14, 31
	v_cmp_lt_i64_e32 vcc, s[20:21], v[2:3]
	s_lshl_b64 s[20:21], s[14:15], 18
	s_add_u32 s20, s28, s20
	s_addc_u32 s21, s44, s21
	s_and_b64 s[34:35], vcc, exec
	ds_read_b128 v[2:5], v175
	ds_read_b128 v[6:9], v176
	ds_read_b128 v[10:13], v177
	ds_read_b128 v[14:17], v178
	s_cselect_b32 s15, s21, s41
	s_cselect_b32 s65, s20, s40
	s_ashr_i32 s13, s12, 31
	s_lshl_b64 s[34:35], s[12:13], 18
	s_add_u32 s34, s45, s34
	s_addc_u32 s35, s46, s35
	s_and_b64 s[42:43], vcc, exec
	s_cselect_b32 s13, s35, s39
	s_cselect_b32 s66, s34, s38
	s_add_u32 s42, s40, 0x20080
	s_addc_u32 s43, s41, 0
	s_add_i32 s67, s47, 0xc000
	v_add_u32_e32 v0, s55, v174
	v_lshl_add_u64 v[50:51], s[42:43], 0, v[164:165]
	s_mov_b32 m0, s67
	s_add_i32 s68, s47, 0xe000
	ds_read_b128 v[18:21], v0
	ds_read_b128 v[22:25], v0 offset:1024
	ds_read_b128 v[26:29], v0 offset:2048
	ds_read_b128 v[30:33], v0 offset:3072
	ds_read_b128 v[34:37], v0 offset:4096
	ds_read_b128 v[38:41], v0 offset:5120
	ds_read_b128 v[42:45], v0 offset:6144
	ds_read_b128 v[46:49], v0 offset:7168
	global_load_lds_dwordx4 v[50:51], off
	v_lshl_add_u64 v[50:51], s[42:43], 0, v[160:161]
	s_mov_b32 m0, s68
	s_nop 0
	global_load_lds_dwordx4 v[50:51], off
	s_waitcnt lgkmcnt(8)
	s_barrier
	s_waitcnt lgkmcnt(0)
	s_setprio 1
	s_waitcnt lgkmcnt(0)
	v_mfma_f32_16x16x128_f8f6f4 v[142:145], v[2:9], v[18:25], 0
	v_mfma_f32_16x16x128_f8f6f4 v[138:141], v[10:17], v[18:25], 0
	v_mfma_f32_16x16x128_f8f6f4 v[122:125], v[2:9], v[26:33], 0
	v_mfma_f32_16x16x128_f8f6f4 v[114:117], v[10:17], v[26:33], 0
	v_mfma_f32_16x16x128_f8f6f4 v[102:105], v[2:9], v[34:41], 0
	v_mfma_f32_16x16x128_f8f6f4 v[98:101], v[10:17], v[34:41], 0
	v_mfma_f32_16x16x128_f8f6f4 v[82:85], v[2:9], v[42:49], 0
	v_mfma_f32_16x16x128_f8f6f4 v[70:73], v[10:17], v[42:49], 0
	s_setprio 0
	s_barrier
	v_lshl_add_u64 v[150:151], s[38:39], 0, v[162:163]
	s_mov_b64 s[42:43], 0x100
	s_mov_b32 m0, s48
	v_lshl_add_u64 v[50:51], v[150:151], 0, s[42:43]
	v_lshl_add_u64 v[152:153], s[38:39], 0, v[158:159]
	ds_read_b128 v[202:205], v179
	ds_read_b128 v[206:209], v180
	ds_read_b128 v[210:213], v181
	ds_read_b128 v[214:217], v182
	global_load_lds_dwordx4 v[50:51], off
	v_lshl_add_u64 v[50:51], v[152:153], 0, s[42:43]
	s_mov_b32 m0, s49
	s_nop 0
	global_load_lds_dwordx4 v[50:51], off
	s_barrier
	s_waitcnt lgkmcnt(0)
	s_setprio 1
	s_waitcnt lgkmcnt(0)
	v_mfma_f32_16x16x128_f8f6f4 v[134:137], v[202:209], v[18:25], 0
	v_mfma_f32_16x16x128_f8f6f4 v[130:133], v[210:217], v[18:25], 0
	v_mfma_f32_16x16x128_f8f6f4 v[126:129], v[202:209], v[26:33], 0
	v_mfma_f32_16x16x128_f8f6f4 v[118:121], v[210:217], v[26:33], 0
	v_mfma_f32_16x16x128_f8f6f4 v[110:113], v[202:209], v[34:41], 0
	v_mfma_f32_16x16x128_f8f6f4 v[106:109], v[210:217], v[34:41], 0
	v_mfma_f32_16x16x128_f8f6f4 v[90:93], v[202:209], v[42:49], 0
	v_mfma_f32_16x16x128_f8f6f4 v[74:77], v[210:217], v[42:49], 0
	s_setprio 0
	v_lshl_add_u64 v[146:147], s[40:41], 0, v[164:165]
	s_mov_b32 m0, s47
	v_lshl_add_u64 v[26:27], v[146:147], 0, s[42:43]
	v_lshl_add_u64 v[148:149], s[40:41], 0, v[160:161]
	s_barrier
	ds_read_b128 v[18:21], v0 offset:16384
	ds_read_b128 v[22:25], v0 offset:17408
	ds_read_b128 v[34:37], v0 offset:18432
	ds_read_b128 v[38:41], v0 offset:19456
	ds_read_b128 v[232:235], v0 offset:20480
	ds_read_b128 v[236:239], v0 offset:21504
	ds_read_b128 v[240:243], v0 offset:22528
	ds_read_b128 v[244:247], v0 offset:23552
	global_load_lds_dwordx4 v[26:27], off
	v_lshl_add_u64 v[26:27], v[148:149], 0, s[42:43]
	s_mov_b32 m0, s50
	s_nop 0
	global_load_lds_dwordx4 v[26:27], off
	s_barrier
	s_waitcnt lgkmcnt(0)
	s_setprio 1
	s_waitcnt lgkmcnt(0)
	v_mfma_f32_16x16x128_f8f6f4 v[94:97], v[2:9], v[18:25], 0
	v_mfma_f32_16x16x128_f8f6f4 v[86:89], v[10:17], v[18:25], 0
	v_mfma_f32_16x16x128_f8f6f4 v[62:65], v[2:9], v[34:41], 0
	v_mfma_f32_16x16x128_f8f6f4 v[58:61], v[10:17], v[34:41], 0
	v_mfma_f32_16x16x128_f8f6f4 v[46:49], v[2:9], v[232:239], 0
	v_mfma_f32_16x16x128_f8f6f4 v[42:45], v[10:17], v[232:239], 0
	v_mfma_f32_16x16x128_f8f6f4 v[30:33], v[2:9], v[240:247], 0
	v_mfma_f32_16x16x128_f8f6f4 v[26:29], v[10:17], v[240:247], 0
	s_setprio 0
	s_barrier
	s_add_u32 s42, s38, 0x20100
	s_addc_u32 s43, s39, 0
	s_mov_b32 m0, s51
	v_lshl_add_u64 v[2:3], s[42:43], 0, v[162:163]
	global_load_lds_dwordx4 v[2:3], off
	v_lshl_add_u64 v[2:3], s[42:43], 0, v[158:159]
	s_mov_b32 m0, s52
	s_nop 0
	global_load_lds_dwordx4 v[2:3], off
	s_waitcnt vmcnt(6)
	s_barrier
	s_setprio 1
	v_mfma_f32_16x16x128_f8f6f4 v[78:81], v[202:209], v[18:25], 0
	v_mfma_f32_16x16x128_f8f6f4 v[66:69], v[210:217], v[18:25], 0
	v_mfma_f32_16x16x128_f8f6f4 v[54:57], v[202:209], v[34:41], 0
	v_mfma_f32_16x16x128_f8f6f4 v[50:53], v[210:217], v[34:41], 0
	v_mfma_f32_16x16x128_f8f6f4 v[38:41], v[202:209], v[232:239], 0
	v_mfma_f32_16x16x128_f8f6f4 v[34:37], v[210:217], v[232:239], 0
	v_mfma_f32_16x16x128_f8f6f4 v[22:25], v[202:209], v[240:247], 0
	v_mfma_f32_16x16x128_f8f6f4 v[18:21], v[210:217], v[240:247], 0
	s_setprio 0
	s_barrier
	ds_read_b128 v[2:5], v183
	ds_read_b128 v[6:9], v184
	ds_read_b128 v[10:13], v185
	ds_read_b128 v[14:17], v196
	s_add_u32 s42, s40, 0x20100
	s_addc_u32 s43, s41, 0
	s_mov_b32 m0, s53
	v_lshl_add_u64 v[154:155], s[42:43], 0, v[164:165]
	ds_read_b128 v[202:205], v0 offset:32768
	ds_read_b128 v[206:209], v0 offset:33792
	ds_read_b128 v[210:213], v0 offset:34816
	ds_read_b128 v[214:217], v0 offset:35840
	ds_read_b128 v[232:235], v0 offset:36864
	ds_read_b128 v[236:239], v0 offset:37888
	ds_read_b128 v[240:243], v0 offset:38912
	ds_read_b128 v[244:247], v0 offset:39936
	global_load_lds_dwordx4 v[154:155], off
	v_lshl_add_u64 v[154:155], s[42:43], 0, v[160:161]
	s_mov_b32 m0, s54
	s_nop 0
	global_load_lds_dwordx4 v[154:155], off
	s_waitcnt lgkmcnt(8)
	s_barrier
	s_waitcnt lgkmcnt(0)
	s_setprio 1
	s_waitcnt lgkmcnt(0)
	v_mfma_f32_16x16x128_f8f6f4 v[142:145], v[2:9], v[202:209], v[142:145]
	v_mfma_f32_16x16x128_f8f6f4 v[138:141], v[10:17], v[202:209], v[138:141]
	v_mfma_f32_16x16x128_f8f6f4 v[122:125], v[2:9], v[210:217], v[122:125]
	v_mfma_f32_16x16x128_f8f6f4 v[114:117], v[10:17], v[210:217], v[114:117]
	v_mfma_f32_16x16x128_f8f6f4 v[102:105], v[2:9], v[232:239], v[102:105]
	v_mfma_f32_16x16x128_f8f6f4 v[98:101], v[10:17], v[232:239], v[98:101]
	v_mfma_f32_16x16x128_f8f6f4 v[82:85], v[2:9], v[240:247], v[82:85]
	v_mfma_f32_16x16x128_f8f6f4 v[70:73], v[10:17], v[240:247], v[70:73]
	s_setprio 0
	s_barrier
	s_mov_b64 s[42:43], 0x180
	s_mov_b32 m0, s56
	v_lshl_add_u64 v[150:151], v[150:151], 0, s[42:43]
	ds_read_b128 v[188:191], v197
	ds_read_b128 v[192:195], v198
	ds_read_b128 v[166:169], v199
	ds_read_b128 v[170:173], v200
	global_load_lds_dwordx4 v[150:151], off
	v_lshl_add_u64 v[150:151], v[152:153], 0, s[42:43]
	s_mov_b32 m0, s57
	s_nop 0
	global_load_lds_dwordx4 v[150:151], off
	s_barrier
	s_waitcnt lgkmcnt(0)
	s_setprio 1
	s_waitcnt lgkmcnt(0)
	v_mfma_f32_16x16x128_f8f6f4 v[134:137], v[188:195], v[202:209], v[134:137]
	v_mfma_f32_16x16x128_f8f6f4 v[130:133], v[166:173], v[202:209], v[130:133]
	v_mfma_f32_16x16x128_f8f6f4 v[126:129], v[188:195], v[210:217], v[126:129]
	v_mfma_f32_16x16x128_f8f6f4 v[118:121], v[166:173], v[210:217], v[118:121]
	v_mfma_f32_16x16x128_f8f6f4 v[110:113], v[188:195], v[232:239], v[110:113]
	v_mfma_f32_16x16x128_f8f6f4 v[106:109], v[166:173], v[232:239], v[106:109]
	v_mfma_f32_16x16x128_f8f6f4 v[90:93], v[188:195], v[240:247], v[90:93]
	v_mfma_f32_16x16x128_f8f6f4 v[74:77], v[166:173], v[240:247], v[74:77]
	s_setprio 0
	s_mov_b32 m0, s58
	v_lshl_add_u64 v[146:147], v[146:147], 0, s[42:43]
	s_barrier
	ds_read_b128 v[150:153], v0 offset:49152
	ds_read_b128 v[154:157], v0 offset:50176
	ds_read_b128 v[202:205], v0 offset:51200
	ds_read_b128 v[206:209], v0 offset:52224
	ds_read_b128 v[210:213], v0 offset:53248
	ds_read_b128 v[214:217], v0 offset:54272
	ds_read_b128 v[232:235], v0 offset:55296
	ds_read_b128 v[236:239], v0 offset:56320
	global_load_lds_dwordx4 v[146:147], off
	v_lshl_add_u64 v[146:147], v[148:149], 0, s[42:43]
	s_mov_b32 m0, s59
	s_nop 0
	global_load_lds_dwordx4 v[146:147], off
	s_barrier
	s_waitcnt lgkmcnt(0)
	s_setprio 1
	s_waitcnt lgkmcnt(0)
	v_mfma_f32_16x16x128_f8f6f4 v[94:97], v[2:9], v[150:157], v[94:97]
	v_mfma_f32_16x16x128_f8f6f4 v[86:89], v[10:17], v[150:157], v[86:89]
	v_mfma_f32_16x16x128_f8f6f4 v[62:65], v[2:9], v[202:209], v[62:65]
	v_mfma_f32_16x16x128_f8f6f4 v[58:61], v[10:17], v[202:209], v[58:61]
	v_mfma_f32_16x16x128_f8f6f4 v[46:49], v[2:9], v[210:217], v[46:49]
	v_mfma_f32_16x16x128_f8f6f4 v[42:45], v[10:17], v[210:217], v[42:45]
	v_mfma_f32_16x16x128_f8f6f4 v[30:33], v[2:9], v[232:239], v[30:33]
	v_mfma_f32_16x16x128_f8f6f4 v[26:29], v[10:17], v[232:239], v[26:29]
	s_setprio 0
	s_barrier
	s_add_u32 s42, s38, 0x20180
	s_addc_u32 s43, s39, 0
	s_mov_b32 m0, s60
	v_lshl_add_u64 v[2:3], s[42:43], 0, v[162:163]
	global_load_lds_dwordx4 v[2:3], off
	v_lshl_add_u64 v[2:3], s[42:43], 0, v[158:159]
	s_mov_b32 m0, s61
	s_nop 0
	global_load_lds_dwordx4 v[2:3], off
	s_waitcnt vmcnt(6)
	s_barrier
	s_setprio 1
	v_mfma_f32_16x16x128_f8f6f4 v[78:81], v[188:195], v[150:157], v[78:81]
	v_mfma_f32_16x16x128_f8f6f4 v[66:69], v[166:173], v[150:157], v[66:69]
	v_mfma_f32_16x16x128_f8f6f4 v[54:57], v[188:195], v[202:209], v[54:57]
	v_mfma_f32_16x16x128_f8f6f4 v[50:53], v[166:173], v[202:209], v[50:53]
	v_mfma_f32_16x16x128_f8f6f4 v[38:41], v[188:195], v[210:217], v[38:41]
	v_mfma_f32_16x16x128_f8f6f4 v[34:37], v[166:173], v[210:217], v[34:37]
	v_mfma_f32_16x16x128_f8f6f4 v[22:25], v[188:195], v[232:239], v[22:25]
	v_mfma_f32_16x16x128_f8f6f4 v[18:21], v[166:173], v[232:239], v[18:21]
	s_setprio 0
	s_add_u32 s40, s40, 0x20180
	s_addc_u32 s41, s41, 0
	s_add_u32 s69, s38, 0x200
	s_addc_u32 s70, s39, 0
	s_mov_b32 s71, 0
	s_barrier
.LBB0_1475:
	ds_read_b128 v[10:13], v175
	ds_read_b128 v[14:17], v176
	ds_read_b128 v[146:149], v177
	ds_read_b128 v[150:153], v178
	s_add_u32 s38, s40, 0xfffe0080
	s_addc_u32 s39, s41, -1
	s_cmp_eq_u32 s71, 4
	s_cselect_b32 s43, s15, s39
	s_cselect_b32 s42, s65, s38
	s_cselect_b32 s39, s13, s70
	s_cselect_b32 s38, s66, s69
	s_mov_b32 m0, s67
	v_lshl_add_u64 v[2:3], s[40:41], 0, v[218:219]
	ds_read_b128 v[166:169], v0
	ds_read_b128 v[170:173], v0 offset:1024
	ds_read_b128 v[188:191], v0 offset:2048
	ds_read_b128 v[192:195], v0 offset:3072
	ds_read_b128 v[202:205], v0 offset:4096
	ds_read_b128 v[206:209], v0 offset:5120
	ds_read_b128 v[210:213], v0 offset:6144
	ds_read_b128 v[214:217], v0 offset:7168
	global_load_lds_dwordx4 v[2:3], off
	v_lshl_add_u64 v[2:3], s[40:41], 0, v[220:221]
	s_mov_b32 m0, s68
	s_nop 0
	global_load_lds_dwordx4 v[2:3], off
	s_waitcnt lgkmcnt(8)
	s_barrier
	s_waitcnt lgkmcnt(0)
	s_setprio 1
	s_waitcnt lgkmcnt(0)
	v_mfma_f32_16x16x128_f8f6f4 v[142:145], v[10:17], v[166:173], v[142:145]
	v_mfma_f32_16x16x128_f8f6f4 v[138:141], v[146:153], v[166:173], v[138:141]
	v_mfma_f32_16x16x128_f8f6f4 v[122:125], v[10:17], v[188:195], v[122:125]
	v_mfma_f32_16x16x128_f8f6f4 v[114:117], v[146:153], v[188:195], v[114:117]
	v_mfma_f32_16x16x128_f8f6f4 v[102:105], v[10:17], v[202:209], v[102:105]
	v_mfma_f32_16x16x128_f8f6f4 v[98:101], v[146:153], v[202:209], v[98:101]
	v_mfma_f32_16x16x128_f8f6f4 v[82:85], v[10:17], v[210:217], v[82:85]
	v_mfma_f32_16x16x128_f8f6f4 v[70:73], v[146:153], v[210:217], v[70:73]
	s_setprio 0
	s_barrier
	s_mov_b32 m0, s48
	v_lshl_add_u64 v[6:7], s[38:39], 0, v[162:163]
	ds_read_b128 v[232:235], v179
	ds_read_b128 v[236:239], v180
	ds_read_b128 v[240:243], v181
	ds_read_b128 v[244:247], v182
	global_load_lds_dwordx4 v[6:7], off
	v_lshl_add_u64 v[8:9], s[38:39], 0, v[158:159]
	s_mov_b32 m0, s49
	s_nop 0
	global_load_lds_dwordx4 v[8:9], off
	s_barrier
	s_waitcnt lgkmcnt(0)
	s_setprio 1
	s_waitcnt lgkmcnt(0)
	v_mfma_f32_16x16x128_f8f6f4 v[134:137], v[232:239], v[166:173], v[134:137]
	v_mfma_f32_16x16x128_f8f6f4 v[130:133], v[240:247], v[166:173], v[130:133]
	v_mfma_f32_16x16x128_f8f6f4 v[126:129], v[232:239], v[188:195], v[126:129]
	v_mfma_f32_16x16x128_f8f6f4 v[118:121], v[240:247], v[188:195], v[118:121]
	v_mfma_f32_16x16x128_f8f6f4 v[110:113], v[232:239], v[202:209], v[110:113]
	v_mfma_f32_16x16x128_f8f6f4 v[106:109], v[240:247], v[202:209], v[106:109]
	v_mfma_f32_16x16x128_f8f6f4 v[90:93], v[232:239], v[210:217], v[90:93]
	v_mfma_f32_16x16x128_f8f6f4 v[74:77], v[240:247], v[210:217], v[74:77]
	s_setprio 0
	s_mov_b32 m0, s47
	v_lshl_add_u64 v[2:3], s[42:43], 0, v[164:165]
	s_barrier
	ds_read_b128 v[166:169], v0 offset:16384
	ds_read_b128 v[170:173], v0 offset:17408
	ds_read_b128 v[188:191], v0 offset:18432
	ds_read_b128 v[192:195], v0 offset:19456
	ds_read_b128 v[202:205], v0 offset:20480
	ds_read_b128 v[206:209], v0 offset:21504
	ds_read_b128 v[210:213], v0 offset:22528
	ds_read_b128 v[214:217], v0 offset:23552
	global_load_lds_dwordx4 v[2:3], off
	v_lshl_add_u64 v[4:5], s[42:43], 0, v[160:161]
	s_mov_b32 m0, s50
	s_nop 0
	global_load_lds_dwordx4 v[4:5], off
	s_barrier
	s_waitcnt lgkmcnt(0)
	s_setprio 1
	s_waitcnt lgkmcnt(0)
	v_mfma_f32_16x16x128_f8f6f4 v[94:97], v[10:17], v[166:173], v[94:97]
	v_mfma_f32_16x16x128_f8f6f4 v[86:89], v[146:153], v[166:173], v[86:89]
	v_mfma_f32_16x16x128_f8f6f4 v[62:65], v[10:17], v[188:195], v[62:65]
	v_mfma_f32_16x16x128_f8f6f4 v[58:61], v[146:153], v[188:195], v[58:61]
	v_mfma_f32_16x16x128_f8f6f4 v[46:49], v[10:17], v[202:209], v[46:49]
	v_mfma_f32_16x16x128_f8f6f4 v[42:45], v[146:153], v[202:209], v[42:45]
	v_mfma_f32_16x16x128_f8f6f4 v[30:33], v[10:17], v[210:217], v[30:33]
	v_mfma_f32_16x16x128_f8f6f4 v[26:29], v[146:153], v[210:217], v[26:29]
	s_setprio 0
	s_barrier
	s_add_u32 s72, s38, 0x20000
	s_addc_u32 s73, s39, 0
	s_mov_b32 m0, s51
	v_lshl_add_u64 v[10:11], s[72:73], 0, v[162:163]
	global_load_lds_dwordx4 v[10:11], off
	v_lshl_add_u64 v[10:11], s[72:73], 0, v[158:159]
	s_mov_b32 m0, s52
	s_nop 0
	global_load_lds_dwordx4 v[10:11], off
	s_waitcnt vmcnt(6)
	s_barrier
	s_setprio 1
	v_mfma_f32_16x16x128_f8f6f4 v[78:81], v[232:239], v[166:173], v[78:81]
	v_mfma_f32_16x16x128_f8f6f4 v[66:69], v[240:247], v[166:173], v[66:69]
	v_mfma_f32_16x16x128_f8f6f4 v[54:57], v[232:239], v[188:195], v[54:57]
	v_mfma_f32_16x16x128_f8f6f4 v[50:53], v[240:247], v[188:195], v[50:53]
	v_mfma_f32_16x16x128_f8f6f4 v[38:41], v[232:239], v[202:209], v[38:41]
	v_mfma_f32_16x16x128_f8f6f4 v[34:37], v[240:247], v[202:209], v[34:37]
	v_mfma_f32_16x16x128_f8f6f4 v[22:25], v[232:239], v[210:217], v[22:25]
	v_mfma_f32_16x16x128_f8f6f4 v[18:21], v[240:247], v[210:217], v[18:21]
	s_setprio 0
	s_barrier
	ds_read_b128 v[10:13], v183
	ds_read_b128 v[14:17], v184
	ds_read_b128 v[146:149], v185
	ds_read_b128 v[150:153], v196
	s_add_u32 s42, s42, 0x20000
	s_addc_u32 s43, s43, 0
	s_mov_b32 m0, s53
	v_lshl_add_u64 v[154:155], s[42:43], 0, v[164:165]
	ds_read_b128 v[166:169], v0 offset:32768
	ds_read_b128 v[170:173], v0 offset:33792
	ds_read_b128 v[188:191], v0 offset:34816
	ds_read_b128 v[192:195], v0 offset:35840
	ds_read_b128 v[202:205], v0 offset:36864
	ds_read_b128 v[206:209], v0 offset:37888
	ds_read_b128 v[210:213], v0 offset:38912
	ds_read_b128 v[214:217], v0 offset:39936
	global_load_lds_dwordx4 v[154:155], off
	v_lshl_add_u64 v[154:155], s[42:43], 0, v[160:161]
	s_mov_b32 m0, s54
	s_nop 0
	global_load_lds_dwordx4 v[154:155], off
	s_waitcnt lgkmcnt(8)
	s_barrier
	s_waitcnt lgkmcnt(0)
	s_setprio 1
	s_waitcnt lgkmcnt(0)
	v_mfma_f32_16x16x128_f8f6f4 v[142:145], v[10:17], v[166:173], v[142:145]
	v_mfma_f32_16x16x128_f8f6f4 v[138:141], v[146:153], v[166:173], v[138:141]
	v_mfma_f32_16x16x128_f8f6f4 v[122:125], v[10:17], v[188:195], v[122:125]
	v_mfma_f32_16x16x128_f8f6f4 v[114:117], v[146:153], v[188:195], v[114:117]
	v_mfma_f32_16x16x128_f8f6f4 v[102:105], v[10:17], v[202:209], v[102:105]
	v_mfma_f32_16x16x128_f8f6f4 v[98:101], v[146:153], v[202:209], v[98:101]
	v_mfma_f32_16x16x128_f8f6f4 v[82:85], v[10:17], v[210:217], v[82:85]
	v_mfma_f32_16x16x128_f8f6f4 v[70:73], v[146:153], v[210:217], v[70:73]
	s_setprio 0
	s_barrier
	s_mov_b32 m0, s56
	v_lshl_add_u64 v[6:7], v[6:7], 0, s[24:25]
	ds_read_b128 v[232:235], v197
	ds_read_b128 v[236:239], v198
	ds_read_b128 v[240:243], v199
	ds_read_b128 v[244:247], v200
	global_load_lds_dwordx4 v[6:7], off
	v_lshl_add_u64 v[6:7], v[8:9], 0, s[24:25]
	s_mov_b32 m0, s57
	s_nop 0
	global_load_lds_dwordx4 v[6:7], off
	s_barrier
	s_waitcnt lgkmcnt(0)
	s_setprio 1
	s_waitcnt lgkmcnt(0)
	v_mfma_f32_16x16x128_f8f6f4 v[134:137], v[232:239], v[166:173], v[134:137]
	v_mfma_f32_16x16x128_f8f6f4 v[130:133], v[240:247], v[166:173], v[130:133]
	v_mfma_f32_16x16x128_f8f6f4 v[126:129], v[232:239], v[188:195], v[126:129]
	v_mfma_f32_16x16x128_f8f6f4 v[118:121], v[240:247], v[188:195], v[118:121]
	v_mfma_f32_16x16x128_f8f6f4 v[110:113], v[232:239], v[202:209], v[110:113]
	v_mfma_f32_16x16x128_f8f6f4 v[106:109], v[240:247], v[202:209], v[106:109]
	v_mfma_f32_16x16x128_f8f6f4 v[90:93], v[232:239], v[210:217], v[90:93]
	v_mfma_f32_16x16x128_f8f6f4 v[74:77], v[240:247], v[210:217], v[74:77]
	s_setprio 0
	s_mov_b32 m0, s58
	v_lshl_add_u64 v[2:3], v[2:3], 0, s[24:25]
	s_barrier
	ds_read_b128 v[166:169], v0 offset:49152
	ds_read_b128 v[170:173], v0 offset:50176
	ds_read_b128 v[188:191], v0 offset:51200
	ds_read_b128 v[192:195], v0 offset:52224
	ds_read_b128 v[202:205], v0 offset:53248
	ds_read_b128 v[206:209], v0 offset:54272
	ds_read_b128 v[210:213], v0 offset:55296
	ds_read_b128 v[214:217], v0 offset:56320
	global_load_lds_dwordx4 v[2:3], off
	v_lshl_add_u64 v[2:3], v[4:5], 0, s[24:25]
	s_mov_b32 m0, s59
	s_nop 0
	global_load_lds_dwordx4 v[2:3], off
	s_barrier
	s_waitcnt lgkmcnt(0)
	s_setprio 1
	s_waitcnt lgkmcnt(0)
	v_mfma_f32_16x16x128_f8f6f4 v[94:97], v[10:17], v[166:173], v[94:97]
	v_mfma_f32_16x16x128_f8f6f4 v[86:89], v[146:153], v[166:173], v[86:89]
	v_mfma_f32_16x16x128_f8f6f4 v[62:65], v[10:17], v[188:195], v[62:65]
	v_mfma_f32_16x16x128_f8f6f4 v[58:61], v[146:153], v[188:195], v[58:61]
	v_mfma_f32_16x16x128_f8f6f4 v[46:49], v[10:17], v[202:209], v[46:49]
	v_mfma_f32_16x16x128_f8f6f4 v[42:45], v[146:153], v[202:209], v[42:45]
	v_mfma_f32_16x16x128_f8f6f4 v[30:33], v[10:17], v[210:217], v[30:33]
	v_mfma_f32_16x16x128_f8f6f4 v[26:29], v[146:153], v[210:217], v[26:29]
	s_setprio 0
	s_barrier
	s_add_u32 s38, s38, 0x20080
	s_addc_u32 s39, s39, 0
	s_mov_b32 m0, s60
	v_lshl_add_u64 v[2:3], s[38:39], 0, v[162:163]
	global_load_lds_dwordx4 v[2:3], off
	v_lshl_add_u64 v[2:3], s[38:39], 0, v[158:159]
	s_mov_b32 m0, s61
	s_nop 0
	global_load_lds_dwordx4 v[2:3], off
	s_waitcnt vmcnt(6)
	s_barrier
	s_setprio 1
	v_mfma_f32_16x16x128_f8f6f4 v[78:81], v[232:239], v[166:173], v[78:81]
	v_mfma_f32_16x16x128_f8f6f4 v[66:69], v[240:247], v[166:173], v[66:69]
	v_mfma_f32_16x16x128_f8f6f4 v[54:57], v[232:239], v[188:195], v[54:57]
	v_mfma_f32_16x16x128_f8f6f4 v[50:53], v[240:247], v[188:195], v[50:53]
	v_mfma_f32_16x16x128_f8f6f4 v[38:41], v[232:239], v[202:209], v[38:41]
	v_mfma_f32_16x16x128_f8f6f4 v[34:37], v[240:247], v[202:209], v[34:37]
	v_mfma_f32_16x16x128_f8f6f4 v[22:25], v[232:239], v[210:217], v[22:25]
	v_mfma_f32_16x16x128_f8f6f4 v[18:21], v[240:247], v[210:217], v[18:21]
	s_setprio 0
	s_add_i32 s71, s71, 2
	s_add_u32 s40, s40, 0x100
	s_addc_u32 s41, s41, 0
	s_add_u32 s69, s69, 0x100
	s_addc_u32 s70, s70, 0
	s_cmp_gt_u32 s71, 5
	s_barrier
	s_cbranch_scc0 .LBB0_1475
	s_nop 15
	s_nop 15
	v_mbcnt_lo_u32_b32 v0, -1, 0
	v_mbcnt_hi_u32_b32 v0, -1, v0
	v_readlane_b32 s15, v252, 51
	v_and_b32_e32 v201, 15, v0
	v_bfe_u32 v0, v0, 4, 2
	v_readlane_b32 s13, v252, 52
	s_mov_b64 s[38:39], -1
	s_and_b64 vcc, exec, s[10:11]
	s_cbranch_vccz .LBB0_1478
	v_lshl_or_b32 v6, s15, 6, v201
	s_lshl_b32 s38, s13, 5
	s_lshl_b32 s41, s64, 8
	s_ashr_i32 s39, s38, 31
	v_lshl_or_b32 v2, v0, 3, s38
	v_add_u32_e32 v4, s41, v6
	s_lshl_b32 s38, s63, 8
	v_mov_b32_e32 v3, s39
	v_ashrrev_i32_e32 v5, 31, v4
	s_ashr_i32 s39, s38, 31
	v_lshlrev_b64 v[16:17], 10, v[4:5]
	v_lshl_add_u64 v[4:5], v[2:3], 0, s[38:39]
	v_lshl_add_u64 v[2:3], v[16:17], 0, v[4:5]
	v_lshl_add_u64 v[146:147], v[2:3], 2, s[8:9]
	global_load_dwordx4 v[8:11], v[146:147], off offset:16
	global_load_dwordx4 v[12:15], v[146:147], off
	v_lshl_add_u64 v[2:3], v[2:3], 1, s[6:7]
	s_or_b32 s38, s41, 16
	s_or_b32 s39, s41, 32
	s_or_b32 s40, s41, 48
	s_waitcnt vmcnt(0)
	v_pk_fma_f32 v[148:149], v[140:141], s[26:27], v[10:11] op_sel_hi:[1,0,1]
	v_pk_fma_f32 v[14:15], v[144:145], s[26:27], v[14:15] op_sel_hi:[1,0,1]
	v_pk_fma_f32 v[12:13], v[142:143], s[26:27], v[12:13] op_sel_hi:[1,0,1]
	v_pk_fma_f32 v[10:11], v[138:139], s[26:27], v[8:9] op_sel_hi:[1,0,1]
	v_cvt_pk_bf16_f32 v8, v12, v13
	v_cvt_pk_bf16_f32 v9, v14, v15
	v_cvt_pk_bf16_f32 v10, v10, v11
	v_cvt_pk_bf16_f32 v11, v148, v149
	global_store_dwordx4 v[2:3], v[8:11], off
	global_load_dwordx4 v[8:11], v[146:147], off offset:528
	s_nop 0
	global_load_dwordx4 v[12:15], v[146:147], off offset:512
	v_lshl_add_u64 v[2:3], v[4:5], 0, s[24:25]
	v_lshl_add_u64 v[16:17], v[2:3], 0, v[16:17]
	s_waitcnt vmcnt(0)
	v_pk_fma_f32 v[146:147], v[132:133], s[26:27], v[10:11] op_sel_hi:[1,0,1]
	v_pk_fma_f32 v[14:15], v[136:137], s[26:27], v[14:15] op_sel_hi:[1,0,1]
	v_pk_fma_f32 v[12:13], v[134:135], s[26:27], v[12:13] op_sel_hi:[1,0,1]
	v_pk_fma_f32 v[10:11], v[130:131], s[26:27], v[8:9] op_sel_hi:[1,0,1]
	v_cvt_pk_bf16_f32 v8, v12, v13
	v_cvt_pk_bf16_f32 v9, v14, v15
	v_cvt_pk_bf16_f32 v10, v10, v11
	v_cvt_pk_bf16_f32 v11, v146, v147
	v_lshl_add_u64 v[12:13], v[16:17], 1, s[6:7]
	global_store_dwordx4 v[12:13], v[8:11], off
	s_nop 1
	v_add_u32_e32 v8, s38, v6
	v_ashrrev_i32_e32 v9, 31, v8
	v_lshlrev_b64 v[16:17], 10, v[8:9]
	v_lshl_add_u64 v[146:147], v[16:17], 0, v[4:5]
	v_lshl_add_u64 v[148:149], v[146:147], 2, s[8:9]
	global_load_dwordx4 v[8:11], v[148:149], off offset:16
	global_load_dwordx4 v[12:15], v[148:149], off
	v_lshl_add_u64 v[16:17], v[16:17], 0, v[2:3]
	s_waitcnt vmcnt(0)
	v_pk_fma_f32 v[150:151], v[116:117], s[26:27], v[10:11] op_sel_hi:[1,0,1]
	v_pk_fma_f32 v[14:15], v[124:125], s[26:27], v[14:15] op_sel_hi:[1,0,1]
	v_pk_fma_f32 v[12:13], v[122:123], s[26:27], v[12:13] op_sel_hi:[1,0,1]
	v_pk_fma_f32 v[10:11], v[114:115], s[26:27], v[8:9] op_sel_hi:[1,0,1]
	v_cvt_pk_bf16_f32 v8, v12, v13
	v_cvt_pk_bf16_f32 v9, v14, v15
	v_cvt_pk_bf16_f32 v10, v10, v11
	v_cvt_pk_bf16_f32 v11, v150, v151
	v_lshl_add_u64 v[12:13], v[146:147], 1, s[6:7]
	global_store_dwordx4 v[12:13], v[8:11], off
	global_load_dwordx4 v[8:11], v[148:149], off offset:528
	s_nop 0
	global_load_dwordx4 v[12:15], v[148:149], off offset:512
	s_waitcnt vmcnt(0)
	v_pk_fma_f32 v[146:147], v[120:121], s[26:27], v[10:11] op_sel_hi:[1,0,1]
	v_pk_fma_f32 v[14:15], v[128:129], s[26:27], v[14:15] op_sel_hi:[1,0,1]
	v_pk_fma_f32 v[12:13], v[126:127], s[26:27], v[12:13] op_sel_hi:[1,0,1]
	v_pk_fma_f32 v[10:11], v[118:119], s[26:27], v[8:9] op_sel_hi:[1,0,1]
	v_cvt_pk_bf16_f32 v8, v12, v13
	v_cvt_pk_bf16_f32 v9, v14, v15
	v_cvt_pk_bf16_f32 v10, v10, v11
	v_cvt_pk_bf16_f32 v11, v146, v147
	v_lshl_add_u64 v[12:13], v[16:17], 1, s[6:7]
	global_store_dwordx4 v[12:13], v[8:11], off
	s_nop 1
	v_add_u32_e32 v8, s39, v6
	v_ashrrev_i32_e32 v9, 31, v8
	v_lshlrev_b64 v[16:17], 10, v[8:9]
	v_lshl_add_u64 v[146:147], v[16:17], 0, v[4:5]
	v_lshl_add_u64 v[148:149], v[146:147], 2, s[8:9]
	global_load_dwordx4 v[8:11], v[148:149], off offset:16
	global_load_dwordx4 v[12:15], v[148:149], off
	v_lshl_add_u64 v[16:17], v[16:17], 0, v[2:3]
	s_waitcnt vmcnt(0)
	v_pk_fma_f32 v[150:151], v[100:101], s[26:27], v[10:11] op_sel_hi:[1,0,1]
	v_pk_fma_f32 v[14:15], v[104:105], s[26:27], v[14:15] op_sel_hi:[1,0,1]
	v_pk_fma_f32 v[12:13], v[102:103], s[26:27], v[12:13] op_sel_hi:[1,0,1]
	v_pk_fma_f32 v[10:11], v[98:99], s[26:27], v[8:9] op_sel_hi:[1,0,1]
	v_cvt_pk_bf16_f32 v8, v12, v13
	v_cvt_pk_bf16_f32 v9, v14, v15
	v_cvt_pk_bf16_f32 v10, v10, v11
	v_cvt_pk_bf16_f32 v11, v150, v151
	v_lshl_add_u64 v[12:13], v[146:147], 1, s[6:7]
	global_store_dwordx4 v[12:13], v[8:11], off
	global_load_dwordx4 v[8:11], v[148:149], off offset:528
	s_nop 0
	global_load_dwordx4 v[12:15], v[148:149], off offset:512
	s_waitcnt vmcnt(0)
	v_pk_fma_f32 v[146:147], v[108:109], s[26:27], v[10:11] op_sel_hi:[1,0,1]
	v_pk_fma_f32 v[14:15], v[112:113], s[26:27], v[14:15] op_sel_hi:[1,0,1]
	v_pk_fma_f32 v[12:13], v[110:111], s[26:27], v[12:13] op_sel_hi:[1,0,1]
	v_pk_fma_f32 v[10:11], v[106:107], s[26:27], v[8:9] op_sel_hi:[1,0,1]
	v_cvt_pk_bf16_f32 v8, v12, v13
	v_cvt_pk_bf16_f32 v9, v14, v15
	v_cvt_pk_bf16_f32 v10, v10, v11
	v_cvt_pk_bf16_f32 v11, v146, v147
	v_lshl_add_u64 v[12:13], v[16:17], 1, s[6:7]
	global_store_dwordx4 v[12:13], v[8:11], off
	s_nop 1
	v_add_u32_e32 v8, s40, v6
	v_ashrrev_i32_e32 v9, 31, v8
	v_lshlrev_b64 v[16:17], 10, v[8:9]
	v_lshl_add_u64 v[146:147], v[16:17], 0, v[4:5]
	v_lshl_add_u64 v[148:149], v[146:147], 2, s[8:9]
	global_load_dwordx4 v[8:11], v[148:149], off offset:16
	global_load_dwordx4 v[12:15], v[148:149], off
	v_lshl_add_u64 v[16:17], v[16:17], 0, v[2:3]
	v_add_u32_e32 v6, 0x80, v6
	s_waitcnt vmcnt(0)
	v_pk_fma_f32 v[150:151], v[72:73], s[26:27], v[10:11] op_sel_hi:[1,0,1]
	v_pk_fma_f32 v[14:15], v[84:85], s[26:27], v[14:15] op_sel_hi:[1,0,1]
	v_pk_fma_f32 v[12:13], v[82:83], s[26:27], v[12:13] op_sel_hi:[1,0,1]
	v_pk_fma_f32 v[10:11], v[70:71], s[26:27], v[8:9] op_sel_hi:[1,0,1]
	v_cvt_pk_bf16_f32 v8, v12, v13
	v_cvt_pk_bf16_f32 v9, v14, v15
	v_cvt_pk_bf16_f32 v10, v10, v11
	v_cvt_pk_bf16_f32 v11, v150, v151
	v_lshl_add_u64 v[12:13], v[146:147], 1, s[6:7]
	global_store_dwordx4 v[12:13], v[8:11], off
	global_load_dwordx4 v[8:11], v[148:149], off offset:528
	s_nop 0
	global_load_dwordx4 v[12:15], v[148:149], off offset:512
	s_waitcnt vmcnt(0)
	v_pk_fma_f32 v[146:147], v[76:77], s[26:27], v[10:11] op_sel_hi:[1,0,1]
	v_pk_fma_f32 v[14:15], v[92:93], s[26:27], v[14:15] op_sel_hi:[1,0,1]
	v_pk_fma_f32 v[12:13], v[90:91], s[26:27], v[12:13] op_sel_hi:[1,0,1]
	v_pk_fma_f32 v[10:11], v[74:75], s[26:27], v[8:9] op_sel_hi:[1,0,1]
	v_cvt_pk_bf16_f32 v8, v12, v13
	v_cvt_pk_bf16_f32 v9, v14, v15
	v_cvt_pk_bf16_f32 v10, v10, v11
	v_cvt_pk_bf16_f32 v11, v146, v147
	v_lshl_add_u64 v[12:13], v[16:17], 1, s[6:7]
	global_store_dwordx4 v[12:13], v[8:11], off
	s_nop 1
	v_add_u32_e32 v8, s41, v6
	v_ashrrev_i32_e32 v9, 31, v8
	v_lshlrev_b64 v[16:17], 10, v[8:9]
	v_lshl_add_u64 v[146:147], v[16:17], 0, v[4:5]
	v_lshl_add_u64 v[148:149], v[146:147], 2, s[8:9]
	global_load_dwordx4 v[8:11], v[148:149], off offset:16
	global_load_dwordx4 v[12:15], v[148:149], off
	v_lshl_add_u64 v[16:17], v[16:17], 0, v[2:3]
	s_waitcnt vmcnt(0)
	v_pk_fma_f32 v[150:151], v[88:89], s[26:27], v[10:11] op_sel_hi:[1,0,1]
	v_pk_fma_f32 v[14:15], v[96:97], s[26:27], v[14:15] op_sel_hi:[1,0,1]
	v_pk_fma_f32 v[12:13], v[94:95], s[26:27], v[12:13] op_sel_hi:[1,0,1]
	v_pk_fma_f32 v[10:11], v[86:87], s[26:27], v[8:9] op_sel_hi:[1,0,1]
	v_cvt_pk_bf16_f32 v8, v12, v13
	v_cvt_pk_bf16_f32 v9, v14, v15
	v_cvt_pk_bf16_f32 v10, v10, v11
	v_cvt_pk_bf16_f32 v11, v150, v151
	v_lshl_add_u64 v[12:13], v[146:147], 1, s[6:7]
	global_store_dwordx4 v[12:13], v[8:11], off
	global_load_dwordx4 v[8:11], v[148:149], off offset:528
	s_nop 0
	global_load_dwordx4 v[12:15], v[148:149], off offset:512
	s_waitcnt vmcnt(0)
	v_pk_fma_f32 v[146:147], v[68:69], s[26:27], v[10:11] op_sel_hi:[1,0,1]
	v_pk_fma_f32 v[14:15], v[80:81], s[26:27], v[14:15] op_sel_hi:[1,0,1]
	v_pk_fma_f32 v[12:13], v[78:79], s[26:27], v[12:13] op_sel_hi:[1,0,1]
	v_pk_fma_f32 v[10:11], v[66:67], s[26:27], v[8:9] op_sel_hi:[1,0,1]
	v_cvt_pk_bf16_f32 v8, v12, v13
	v_cvt_pk_bf16_f32 v9, v14, v15
	v_cvt_pk_bf16_f32 v10, v10, v11
	v_cvt_pk_bf16_f32 v11, v146, v147
	v_lshl_add_u64 v[12:13], v[16:17], 1, s[6:7]
	global_store_dwordx4 v[12:13], v[8:11], off
	s_nop 1
	v_add_u32_e32 v8, s38, v6
	v_ashrrev_i32_e32 v9, 31, v8
	v_lshlrev_b64 v[16:17], 10, v[8:9]
	v_lshl_add_u64 v[146:147], v[16:17], 0, v[4:5]
	v_lshl_add_u64 v[148:149], v[146:147], 2, s[8:9]
	global_load_dwordx4 v[8:11], v[148:149], off offset:16
	global_load_dwordx4 v[12:15], v[148:149], off
	v_lshl_add_u64 v[16:17], v[16:17], 0, v[2:3]
	s_waitcnt vmcnt(0)
	v_pk_fma_f32 v[150:151], v[60:61], s[26:27], v[10:11] op_sel_hi:[1,0,1]
	v_pk_fma_f32 v[14:15], v[64:65], s[26:27], v[14:15] op_sel_hi:[1,0,1]
	v_pk_fma_f32 v[12:13], v[62:63], s[26:27], v[12:13] op_sel_hi:[1,0,1]
	v_pk_fma_f32 v[10:11], v[58:59], s[26:27], v[8:9] op_sel_hi:[1,0,1]
	v_cvt_pk_bf16_f32 v8, v12, v13
	v_cvt_pk_bf16_f32 v9, v14, v15
	v_cvt_pk_bf16_f32 v10, v10, v11
	v_cvt_pk_bf16_f32 v11, v150, v151
	v_lshl_add_u64 v[12:13], v[146:147], 1, s[6:7]
	global_store_dwordx4 v[12:13], v[8:11], off
	global_load_dwordx4 v[8:11], v[148:149], off offset:528
	s_nop 0
	global_load_dwordx4 v[12:15], v[148:149], off offset:512
	s_waitcnt vmcnt(0)
	v_pk_fma_f32 v[146:147], v[52:53], s[26:27], v[10:11] op_sel_hi:[1,0,1]
	v_pk_fma_f32 v[14:15], v[56:57], s[26:27], v[14:15] op_sel_hi:[1,0,1]
	v_pk_fma_f32 v[12:13], v[54:55], s[26:27], v[12:13] op_sel_hi:[1,0,1]
	v_pk_fma_f32 v[10:11], v[50:51], s[26:27], v[8:9] op_sel_hi:[1,0,1]
	v_cvt_pk_bf16_f32 v8, v12, v13
	v_cvt_pk_bf16_f32 v9, v14, v15
	v_cvt_pk_bf16_f32 v10, v10, v11
	v_cvt_pk_bf16_f32 v11, v146, v147
	v_lshl_add_u64 v[12:13], v[16:17], 1, s[6:7]
	global_store_dwordx4 v[12:13], v[8:11], off
	s_nop 1
	v_add_u32_e32 v8, s39, v6
	v_ashrrev_i32_e32 v9, 31, v8
	v_lshlrev_b64 v[16:17], 10, v[8:9]
	v_lshl_add_u64 v[146:147], v[16:17], 0, v[4:5]
	v_lshl_add_u64 v[148:149], v[146:147], 2, s[8:9]
	global_load_dwordx4 v[8:11], v[148:149], off offset:16
	global_load_dwordx4 v[12:15], v[148:149], off
	v_lshl_add_u64 v[16:17], v[16:17], 0, v[2:3]
	v_add_u32_e32 v6, s40, v6
	v_ashrrev_i32_e32 v7, 31, v6
	s_mov_b64 s[38:39], 0
	s_waitcnt vmcnt(0)
	v_pk_fma_f32 v[150:151], v[44:45], s[26:27], v[10:11] op_sel_hi:[1,0,1]
	v_pk_fma_f32 v[14:15], v[48:49], s[26:27], v[14:15] op_sel_hi:[1,0,1]
	v_pk_fma_f32 v[12:13], v[46:47], s[26:27], v[12:13] op_sel_hi:[1,0,1]
	v_pk_fma_f32 v[10:11], v[42:43], s[26:27], v[8:9] op_sel_hi:[1,0,1]
	v_cvt_pk_bf16_f32 v8, v12, v13
	v_cvt_pk_bf16_f32 v9, v14, v15
	v_cvt_pk_bf16_f32 v10, v10, v11
	v_cvt_pk_bf16_f32 v11, v150, v151
	v_lshl_add_u64 v[12:13], v[146:147], 1, s[6:7]
	global_store_dwordx4 v[12:13], v[8:11], off
	global_load_dwordx4 v[8:11], v[148:149], off offset:528
	s_nop 0
	global_load_dwordx4 v[12:15], v[148:149], off offset:512
	s_waitcnt vmcnt(0)
	v_pk_fma_f32 v[146:147], v[36:37], s[26:27], v[10:11] op_sel_hi:[1,0,1]
	v_pk_fma_f32 v[14:15], v[40:41], s[26:27], v[14:15] op_sel_hi:[1,0,1]
	v_pk_fma_f32 v[12:13], v[38:39], s[26:27], v[12:13] op_sel_hi:[1,0,1]
	v_pk_fma_f32 v[10:11], v[34:35], s[26:27], v[8:9] op_sel_hi:[1,0,1]
	v_cvt_pk_bf16_f32 v8, v12, v13
	v_cvt_pk_bf16_f32 v9, v14, v15
	v_cvt_pk_bf16_f32 v10, v10, v11
	v_cvt_pk_bf16_f32 v11, v146, v147
	v_lshl_add_u64 v[12:13], v[16:17], 1, s[6:7]
	global_store_dwordx4 v[12:13], v[8:11], off
	v_lshlrev_b64 v[12:13], 10, v[6:7]
	v_lshl_add_u64 v[14:15], v[12:13], 0, v[4:5]
	v_lshl_add_u64 v[16:17], v[14:15], 2, s[8:9]
	global_load_dwordx4 v[4:7], v[16:17], off offset:16
	global_load_dwordx4 v[8:11], v[16:17], off
	s_waitcnt vmcnt(0)
	v_pk_fma_f32 v[146:147], v[28:29], s[26:27], v[6:7] op_sel_hi:[1,0,1]
	v_pk_fma_f32 v[10:11], v[32:33], s[26:27], v[10:11] op_sel_hi:[1,0,1]
	v_pk_fma_f32 v[8:9], v[30:31], s[26:27], v[8:9] op_sel_hi:[1,0,1]
	v_pk_fma_f32 v[6:7], v[26:27], s[26:27], v[4:5] op_sel_hi:[1,0,1]
	v_cvt_pk_bf16_f32 v4, v8, v9
	v_cvt_pk_bf16_f32 v5, v10, v11
	v_cvt_pk_bf16_f32 v6, v6, v7
	v_cvt_pk_bf16_f32 v7, v146, v147
	v_lshl_add_u64 v[8:9], v[14:15], 1, s[6:7]
	global_store_dwordx4 v[8:9], v[4:7], off
	v_lshl_add_u64 v[10:11], v[12:13], 0, v[2:3]
	global_load_dwordx4 v[2:5], v[16:17], off offset:528
	global_load_dwordx4 v[6:9], v[16:17], off offset:512
	s_waitcnt vmcnt(0)
	v_pk_fma_f32 v[12:13], v[20:21], s[26:27], v[4:5] op_sel_hi:[1,0,1]
	v_pk_fma_f32 v[8:9], v[24:25], s[26:27], v[8:9] op_sel_hi:[1,0,1]
	v_pk_fma_f32 v[6:7], v[22:23], s[26:27], v[6:7] op_sel_hi:[1,0,1]
	v_pk_fma_f32 v[4:5], v[18:19], s[26:27], v[2:3] op_sel_hi:[1,0,1]
	v_cvt_pk_bf16_f32 v2, v6, v7
	v_cvt_pk_bf16_f32 v3, v8, v9
	v_cvt_pk_bf16_f32 v4, v4, v5
	v_cvt_pk_bf16_f32 v5, v12, v13
	v_lshl_add_u64 v[6:7], v[10:11], 1, s[6:7]
	global_store_dwordx4 v[6:7], v[2:5], off

.LBB0_1694:
	ds_read_b128 v[2:5], v205
	ds_read_b128 v[6:9], v206
	ds_read_b128 v[10:13], v207
	ds_read_b128 v[14:17], v208
	s_lshl_b32 s46, s46, 7
	s_ashr_i32 s47, s46, 31
	s_add_i32 s41, s60, 0xc000
	v_add_u32_e32 v221, s72, v204
	s_mov_b32 m0, s41
	s_add_i32 s43, s60, 0xe000
	ds_read_b128 v[18:21], v221
	ds_read_b128 v[22:25], v221 offset:1024
	ds_read_b128 v[26:29], v221 offset:2048
	ds_read_b128 v[30:33], v221 offset:3072
	ds_read_b128 v[34:37], v221 offset:4096
	ds_read_b128 v[38:41], v221 offset:5120
	ds_read_b128 v[42:45], v221 offset:6144
	ds_read_b128 v[46:49], v221 offset:7168
	global_load_lds_dwordx4 v184, s[14:15]
	s_mov_b32 m0, s43
	s_nop 0
	global_load_lds_dwordx4 v198, s[14:15]
	s_waitcnt lgkmcnt(8)
	s_barrier
	s_waitcnt lgkmcnt(0)
	s_setprio 1
	s_waitcnt lgkmcnt(0)
	v_mfma_f32_16x16x128_f8f6f4 v[166:169], v[2:9], v[18:25], 0
	v_mfma_f32_16x16x128_f8f6f4 v[162:165], v[10:17], v[18:25], 0
	v_mfma_f32_16x16x128_f8f6f4 v[150:153], v[2:9], v[26:33], 0
	v_mfma_f32_16x16x128_f8f6f4 v[146:149], v[10:17], v[26:33], 0
	v_mfma_f32_16x16x128_f8f6f4 v[134:137], v[2:9], v[34:41], 0
	v_mfma_f32_16x16x128_f8f6f4 v[130:133], v[10:17], v[34:41], 0
	v_mfma_f32_16x16x128_f8f6f4 v[118:121], v[2:9], v[42:49], 0
	v_mfma_f32_16x16x128_f8f6f4 v[114:117], v[10:17], v[42:49], 0
	s_setprio 0
	s_barrier
	v_lshl_add_u64 v[200:201], s[50:51], 0, v[182:183]
	s_mov_b64 s[8:9], 0x100
	s_mov_b32 m0, s61
	v_lshl_add_u64 v[50:51], v[200:201], 0, s[8:9]
	v_lshl_add_u64 v[202:203], s[50:51], 0, v[180:181]
	ds_read_b128 v[188:191], v209
	ds_read_b128 v[192:195], v210
	ds_read_b128 v[232:235], v211
	ds_read_b128 v[236:239], v212
	global_load_lds_dwordx4 v[50:51], off
	v_lshl_add_u64 v[50:51], v[202:203], 0, s[8:9]
	s_mov_b32 m0, s62
	s_nop 0
	global_load_lds_dwordx4 v[50:51], off
	s_barrier
	s_waitcnt lgkmcnt(0)
	s_setprio 1
	s_waitcnt lgkmcnt(0)
	v_mfma_f32_16x16x128_f8f6f4 v[174:177], v[188:195], v[18:25], 0
	v_mfma_f32_16x16x128_f8f6f4 v[170:173], v[232:239], v[18:25], 0
	v_mfma_f32_16x16x128_f8f6f4 v[158:161], v[188:195], v[26:33], 0
	v_mfma_f32_16x16x128_f8f6f4 v[154:157], v[232:239], v[26:33], 0
	v_mfma_f32_16x16x128_f8f6f4 v[142:145], v[188:195], v[34:41], 0
	v_mfma_f32_16x16x128_f8f6f4 v[138:141], v[232:239], v[34:41], 0
	v_mfma_f32_16x16x128_f8f6f4 v[126:129], v[188:195], v[42:49], 0
	v_mfma_f32_16x16x128_f8f6f4 v[122:125], v[232:239], v[42:49], 0
	s_setprio 0
	s_mov_b32 m0, s60
	s_barrier
	ds_read_b128 v[18:21], v221 offset:16384
	ds_read_b128 v[22:25], v221 offset:17408
	ds_read_b128 v[26:29], v221 offset:18432
	ds_read_b128 v[30:33], v221 offset:19456
	ds_read_b128 v[34:37], v221 offset:20480
	ds_read_b128 v[38:41], v221 offset:21504
	ds_read_b128 v[42:45], v221 offset:22528
	ds_read_b128 v[46:49], v221 offset:23552
	global_load_lds_dwordx4 v0, s[34:35]
	s_mov_b32 m0, s63
	s_nop 0
	global_load_lds_dwordx4 v196, s[34:35]
	s_barrier
	s_waitcnt lgkmcnt(0)
	s_setprio 1
	s_waitcnt lgkmcnt(0)
	v_mfma_f32_16x16x128_f8f6f4 v[102:105], v[2:9], v[18:25], 0
	v_mfma_f32_16x16x128_f8f6f4 v[98:101], v[10:17], v[18:25], 0
	v_mfma_f32_16x16x128_f8f6f4 v[86:89], v[2:9], v[26:33], 0
	v_mfma_f32_16x16x128_f8f6f4 v[82:85], v[10:17], v[26:33], 0
	v_mfma_f32_16x16x128_f8f6f4 v[70:73], v[2:9], v[34:41], 0
	v_mfma_f32_16x16x128_f8f6f4 v[66:69], v[10:17], v[34:41], 0
	v_mfma_f32_16x16x128_f8f6f4 v[54:57], v[2:9], v[42:49], 0
	v_mfma_f32_16x16x128_f8f6f4 v[50:53], v[10:17], v[42:49], 0
	s_setprio 0
	s_barrier
	s_add_u32 s8, s50, 0x20100
	s_addc_u32 s9, s51, 0
	s_mov_b32 m0, s64
	v_lshl_add_u64 v[2:3], s[8:9], 0, v[182:183]
	global_load_lds_dwordx4 v[2:3], off
	v_lshl_add_u64 v[2:3], s[8:9], 0, v[180:181]
	s_mov_b32 m0, s65
	s_nop 0
	global_load_lds_dwordx4 v[2:3], off
	s_waitcnt vmcnt(6)
	s_barrier
	s_setprio 1
	v_mfma_f32_16x16x128_f8f6f4 v[110:113], v[188:195], v[18:25], 0
	v_mfma_f32_16x16x128_f8f6f4 v[106:109], v[232:239], v[18:25], 0
	v_mfma_f32_16x16x128_f8f6f4 v[94:97], v[188:195], v[26:33], 0
	v_mfma_f32_16x16x128_f8f6f4 v[90:93], v[232:239], v[26:33], 0
	v_mfma_f32_16x16x128_f8f6f4 v[78:81], v[188:195], v[34:41], 0
	v_mfma_f32_16x16x128_f8f6f4 v[74:77], v[232:239], v[34:41], 0
	v_mfma_f32_16x16x128_f8f6f4 v[62:65], v[188:195], v[42:49], 0
	v_mfma_f32_16x16x128_f8f6f4 v[58:61], v[232:239], v[42:49], 0
	s_setprio 0
	s_barrier
	ds_read_b128 v[2:5], v213
	ds_read_b128 v[6:9], v214
	ds_read_b128 v[10:13], v215
	ds_read_b128 v[14:17], v216
	s_mov_b32 m0, s66
	ds_read_b128 v[18:21], v221 offset:32768
	ds_read_b128 v[22:25], v221 offset:33792
	ds_read_b128 v[26:29], v221 offset:34816
	ds_read_b128 v[30:33], v221 offset:35840
	ds_read_b128 v[34:37], v221 offset:36864
	ds_read_b128 v[38:41], v221 offset:37888
	ds_read_b128 v[42:45], v221 offset:38912
	ds_read_b128 v[46:49], v221 offset:39936
	global_load_lds_dwordx4 v184, s[34:35]
	s_mov_b32 m0, s67
	s_nop 0
	global_load_lds_dwordx4 v198, s[34:35]
	s_waitcnt lgkmcnt(8)
	s_barrier
	s_waitcnt lgkmcnt(0)
	s_setprio 1
	s_waitcnt lgkmcnt(0)
	v_mfma_f32_16x16x128_f8f6f4 v[166:169], v[2:9], v[18:25], v[166:169]
	v_mfma_f32_16x16x128_f8f6f4 v[162:165], v[10:17], v[18:25], v[162:165]
	v_mfma_f32_16x16x128_f8f6f4 v[150:153], v[2:9], v[26:33], v[150:153]
	v_mfma_f32_16x16x128_f8f6f4 v[146:149], v[10:17], v[26:33], v[146:149]
	v_mfma_f32_16x16x128_f8f6f4 v[134:137], v[2:9], v[34:41], v[134:137]
	v_mfma_f32_16x16x128_f8f6f4 v[130:133], v[10:17], v[34:41], v[130:133]
	v_mfma_f32_16x16x128_f8f6f4 v[118:121], v[2:9], v[42:49], v[118:121]
	v_mfma_f32_16x16x128_f8f6f4 v[114:117], v[10:17], v[42:49], v[114:117]
	s_setprio 0
	s_barrier
	s_mov_b64 s[8:9], 0x180
	s_mov_b32 m0, s73
	v_lshl_add_u64 v[200:201], v[200:201], 0, s[8:9]
	ds_read_b128 v[188:191], v217
	ds_read_b128 v[192:195], v218
	ds_read_b128 v[232:235], v219
	ds_read_b128 v[236:239], v220
	global_load_lds_dwordx4 v[200:201], off
	v_lshl_add_u64 v[200:201], v[202:203], 0, s[8:9]
	s_mov_b32 m0, s74
	s_nop 0
	global_load_lds_dwordx4 v[200:201], off
	s_barrier
	s_waitcnt lgkmcnt(0)
	s_setprio 1
	s_waitcnt lgkmcnt(0)
	v_mfma_f32_16x16x128_f8f6f4 v[174:177], v[188:195], v[18:25], v[174:177]
	v_mfma_f32_16x16x128_f8f6f4 v[170:173], v[232:239], v[18:25], v[170:173]
	v_mfma_f32_16x16x128_f8f6f4 v[158:161], v[188:195], v[26:33], v[158:161]
	v_mfma_f32_16x16x128_f8f6f4 v[154:157], v[232:239], v[26:33], v[154:157]
	v_mfma_f32_16x16x128_f8f6f4 v[142:145], v[188:195], v[34:41], v[142:145]
	v_mfma_f32_16x16x128_f8f6f4 v[138:141], v[232:239], v[34:41], v[138:141]
	v_mfma_f32_16x16x128_f8f6f4 v[126:129], v[188:195], v[42:49], v[126:129]
	v_mfma_f32_16x16x128_f8f6f4 v[122:125], v[232:239], v[42:49], v[122:125]
	s_setprio 0
	s_mov_b32 m0, s75
	s_barrier
	ds_read_b128 v[18:21], v221 offset:49152
	ds_read_b128 v[22:25], v221 offset:50176
	ds_read_b128 v[26:29], v221 offset:51200
	ds_read_b128 v[30:33], v221 offset:52224
	ds_read_b128 v[34:37], v221 offset:53248
	ds_read_b128 v[38:41], v221 offset:54272
	ds_read_b128 v[42:45], v221 offset:55296
	ds_read_b128 v[46:49], v221 offset:56320
	global_load_lds_dwordx4 v0, s[38:39]
	s_mov_b32 m0, s76
	s_nop 0
	global_load_lds_dwordx4 v196, s[38:39]
	s_barrier
	s_waitcnt lgkmcnt(0)
	s_setprio 1
	s_waitcnt lgkmcnt(0)
	v_mfma_f32_16x16x128_f8f6f4 v[102:105], v[2:9], v[18:25], v[102:105]
	v_mfma_f32_16x16x128_f8f6f4 v[98:101], v[10:17], v[18:25], v[98:101]
	v_mfma_f32_16x16x128_f8f6f4 v[86:89], v[2:9], v[26:33], v[86:89]
	v_mfma_f32_16x16x128_f8f6f4 v[82:85], v[10:17], v[26:33], v[82:85]
	v_mfma_f32_16x16x128_f8f6f4 v[70:73], v[2:9], v[34:41], v[70:73]
	v_mfma_f32_16x16x128_f8f6f4 v[66:69], v[10:17], v[34:41], v[66:69]
	v_mfma_f32_16x16x128_f8f6f4 v[54:57], v[2:9], v[42:49], v[54:57]
	v_mfma_f32_16x16x128_f8f6f4 v[50:53], v[10:17], v[42:49], v[50:53]
	s_setprio 0
	s_barrier
	s_add_u32 s8, s50, 0x20180
	s_addc_u32 s9, s51, 0
	s_mov_b32 m0, s77
	v_lshl_add_u64 v[2:3], s[8:9], 0, v[182:183]
	global_load_lds_dwordx4 v[2:3], off
	v_lshl_add_u64 v[2:3], s[8:9], 0, v[180:181]
	s_mov_b32 m0, s78
	s_nop 0
	global_load_lds_dwordx4 v[2:3], off
	s_waitcnt vmcnt(6)
	s_barrier
	s_setprio 1
	v_mfma_f32_16x16x128_f8f6f4 v[110:113], v[188:195], v[18:25], v[110:113]
	v_mfma_f32_16x16x128_f8f6f4 v[106:109], v[232:239], v[18:25], v[106:109]
	v_mfma_f32_16x16x128_f8f6f4 v[94:97], v[188:195], v[26:33], v[94:97]
	v_mfma_f32_16x16x128_f8f6f4 v[90:93], v[232:239], v[26:33], v[90:93]
	v_mfma_f32_16x16x128_f8f6f4 v[78:81], v[188:195], v[34:41], v[78:81]
	v_mfma_f32_16x16x128_f8f6f4 v[74:77], v[232:239], v[34:41], v[74:77]
	v_mfma_f32_16x16x128_f8f6f4 v[62:65], v[188:195], v[42:49], v[62:65]
	v_mfma_f32_16x16x128_f8f6f4 v[58:61], v[232:239], v[42:49], v[58:61]
	s_setprio 0
	s_lshl_b64 s[8:9], s[46:47], 2
	s_add_u32 s49, s70, s8
	s_addc_u32 s80, s71, s9
	s_add_u32 s81, s50, 0x200
	s_addc_u32 s82, s51, 0
	s_mov_b32 s83, 0
	s_mov_b64 s[50:51], 0
	s_barrier
	s_branch .LBB0_1696
.LBB0_1695:
	s_add_u32 s54, s50, 0x200
	s_addc_u32 s55, s51, 0
	s_and_b64 s[8:9], s[52:53], exec
	s_cselect_b32 s9, 0, s54
	s_cselect_b32 s8, 0, s55
	s_add_u32 s54, s12, s9
	s_addc_u32 s55, s13, s8
	s_add_u32 s84, s81, s50
	s_waitcnt lgkmcnt(8)
	s_barrier
	s_waitcnt lgkmcnt(0)
	s_addc_u32 s85, s82, s51
	s_and_b64 s[8:9], s[52:53], exec
	v_mov_b32_e32 v185, v1
	v_mov_b32_e32 v199, v1
	s_cselect_b32 s9, s45, s85
	s_cselect_b32 s8, s44, s84
	s_setprio 1
	s_waitcnt lgkmcnt(0)
	v_mfma_f32_16x16x128_f8f6f4 v[166:169], v[10:17], v[42:49], v[166:169]
	v_mfma_f32_16x16x128_f8f6f4 v[162:165], v[2:9], v[42:49], v[162:165]
	v_mfma_f32_16x16x128_f8f6f4 v[150:153], v[10:17], v[34:41], v[150:153]
	v_mfma_f32_16x16x128_f8f6f4 v[146:149], v[2:9], v[34:41], v[146:149]
	v_mfma_f32_16x16x128_f8f6f4 v[134:137], v[10:17], v[26:33], v[134:137]
	v_mfma_f32_16x16x128_f8f6f4 v[130:133], v[2:9], v[26:33], v[130:133]
	v_mfma_f32_16x16x128_f8f6f4 v[118:121], v[10:17], v[18:25], v[118:121]
	v_mfma_f32_16x16x128_f8f6f4 v[114:117], v[2:9], v[18:25], v[114:117]
	s_setprio 0
	s_barrier
	s_mov_b32 m0, s61
	v_lshl_add_u64 v[200:201], s[8:9], 0, v[182:183]
	ds_read_b128 v[188:191], v209
	ds_read_b128 v[192:195], v210
	ds_read_b128 v[232:235], v211
	ds_read_b128 v[236:239], v212
	global_load_lds_dwordx4 v[200:201], off
	v_lshl_add_u64 v[202:203], s[8:9], 0, v[180:181]
	s_mov_b32 m0, s62
	s_nop 0
	global_load_lds_dwordx4 v[202:203], off
	s_barrier
	s_waitcnt lgkmcnt(0)
	s_setprio 1
	s_waitcnt lgkmcnt(0)
	v_mfma_f32_16x16x128_f8f6f4 v[174:177], v[188:195], v[42:49], v[174:177]
	v_mfma_f32_16x16x128_f8f6f4 v[170:173], v[232:239], v[42:49], v[170:173]
	v_mfma_f32_16x16x128_f8f6f4 v[158:161], v[188:195], v[34:41], v[158:161]
	v_mfma_f32_16x16x128_f8f6f4 v[154:157], v[232:239], v[34:41], v[154:157]
	v_mfma_f32_16x16x128_f8f6f4 v[142:145], v[188:195], v[26:33], v[142:145]
	v_mfma_f32_16x16x128_f8f6f4 v[138:141], v[232:239], v[26:33], v[138:141]
	v_mfma_f32_16x16x128_f8f6f4 v[126:129], v[188:195], v[18:25], v[126:129]
	v_mfma_f32_16x16x128_f8f6f4 v[122:125], v[232:239], v[18:25], v[122:125]
	s_setprio 0
	s_mov_b32 m0, s60
	s_barrier
	ds_read_b128 v[22:25], v221 offset:16384
	ds_read_b128 v[26:29], v221 offset:17408
	ds_read_b128 v[30:33], v221 offset:18432
	ds_read_b128 v[34:37], v221 offset:19456
	ds_read_b128 v[38:41], v221 offset:20480
	ds_read_b128 v[42:45], v221 offset:21504
	ds_read_b128 v[240:243], v221 offset:22528
	ds_read_b128 v[244:247], v221 offset:23552
	global_load_lds_dwordx4 v0, s[54:55]
	s_mov_b32 m0, s63
	v_mov_b32_e32 v197, v1
	global_load_lds_dwordx4 v196, s[54:55]
	s_barrier
	s_waitcnt lgkmcnt(0)
	v_lshl_add_u64 v[20:21], s[54:55], 0, v[0:1]
	v_lshl_add_u64 v[18:19], s[54:55], 0, v[196:197]
	s_setprio 1
	s_waitcnt lgkmcnt(0)
	v_mfma_f32_16x16x128_f8f6f4 v[102:105], v[10:17], v[22:29], v[102:105]
	v_mfma_f32_16x16x128_f8f6f4 v[98:101], v[2:9], v[22:29], v[98:101]
	v_mfma_f32_16x16x128_f8f6f4 v[86:89], v[10:17], v[30:37], v[86:89]
	v_mfma_f32_16x16x128_f8f6f4 v[82:85], v[2:9], v[30:37], v[82:85]
	v_mfma_f32_16x16x128_f8f6f4 v[70:73], v[10:17], v[38:45], v[70:73]
	v_mfma_f32_16x16x128_f8f6f4 v[66:69], v[2:9], v[38:45], v[66:69]
	v_mfma_f32_16x16x128_f8f6f4 v[54:57], v[10:17], v[240:247], v[54:57]
	v_mfma_f32_16x16x128_f8f6f4 v[50:53], v[2:9], v[240:247], v[50:53]
	s_setprio 0
	s_barrier
	s_add_u32 s52, s8, 0x20000
	s_addc_u32 s53, s9, 0
	s_mov_b32 m0, s64
	v_lshl_add_u64 v[2:3], s[52:53], 0, v[182:183]
	global_load_lds_dwordx4 v[2:3], off
	v_lshl_add_u64 v[2:3], s[52:53], 0, v[180:181]
	s_mov_b32 m0, s65
	s_nop 0
	global_load_lds_dwordx4 v[2:3], off
	s_waitcnt vmcnt(6)
	s_barrier
	s_setprio 1
	v_mfma_f32_16x16x128_f8f6f4 v[110:113], v[188:195], v[22:29], v[110:113]
	v_mfma_f32_16x16x128_f8f6f4 v[106:109], v[232:239], v[22:29], v[106:109]
	v_mfma_f32_16x16x128_f8f6f4 v[94:97], v[188:195], v[30:37], v[94:97]
	v_mfma_f32_16x16x128_f8f6f4 v[90:93], v[232:239], v[30:37], v[90:93]
	v_mfma_f32_16x16x128_f8f6f4 v[78:81], v[188:195], v[38:45], v[78:81]
	v_mfma_f32_16x16x128_f8f6f4 v[74:77], v[232:239], v[38:45], v[74:77]
	v_mfma_f32_16x16x128_f8f6f4 v[62:65], v[188:195], v[240:247], v[62:65]
	v_mfma_f32_16x16x128_f8f6f4 v[58:61], v[232:239], v[240:247], v[58:61]
	s_setprio 0
	s_barrier
	ds_read_b128 v[2:5], v213
	ds_read_b128 v[6:9], v214
	ds_read_b128 v[10:13], v215
	ds_read_b128 v[14:17], v216
	s_mov_b32 m0, s66
	v_lshl_add_u64 v[46:47], s[54:55], 0, v[184:185]
	ds_read_b128 v[22:25], v221 offset:32768
	ds_read_b128 v[26:29], v221 offset:33792
	ds_read_b128 v[30:33], v221 offset:34816
	ds_read_b128 v[34:37], v221 offset:35840
	ds_read_b128 v[38:41], v221 offset:36864
	ds_read_b128 v[42:45], v221 offset:37888
	ds_read_b128 v[188:191], v221 offset:38912
	ds_read_b128 v[192:195], v221 offset:39936
	global_load_lds_dwordx4 v[46:47], off
	v_lshl_add_u64 v[46:47], s[54:55], 0, v[198:199]
	s_mov_b32 m0, s67
	s_nop 0
	global_load_lds_dwordx4 v[46:47], off
	s_waitcnt lgkmcnt(8)
	s_barrier
	s_waitcnt lgkmcnt(0)
	s_setprio 1
	s_waitcnt lgkmcnt(0)
	v_mfma_f32_16x16x128_f8f6f4 v[166:169], v[2:9], v[22:29], v[166:169]
	v_mfma_f32_16x16x128_f8f6f4 v[162:165], v[10:17], v[22:29], v[162:165]
	v_mfma_f32_16x16x128_f8f6f4 v[150:153], v[2:9], v[30:37], v[150:153]
	v_mfma_f32_16x16x128_f8f6f4 v[146:149], v[10:17], v[30:37], v[146:149]
	v_mfma_f32_16x16x128_f8f6f4 v[134:137], v[2:9], v[38:45], v[134:137]
	v_mfma_f32_16x16x128_f8f6f4 v[130:133], v[10:17], v[38:45], v[130:133]
	v_mfma_f32_16x16x128_f8f6f4 v[118:121], v[2:9], v[188:195], v[118:121]
	v_mfma_f32_16x16x128_f8f6f4 v[114:117], v[10:17], v[188:195], v[114:117]
	s_setprio 0
	s_barrier
	s_mov_b32 m0, s73
	v_lshl_add_u64 v[46:47], v[200:201], 0, s[24:25]
	ds_read_b128 v[232:235], v217
	ds_read_b128 v[236:239], v218
	ds_read_b128 v[240:243], v219
	ds_read_b128 v[244:247], v220
	global_load_lds_dwordx4 v[46:47], off
	v_lshl_add_u64 v[46:47], v[202:203], 0, s[24:25]
	s_mov_b32 m0, s74
	s_nop 0
	global_load_lds_dwordx4 v[46:47], off
	s_barrier
	s_waitcnt lgkmcnt(0)
	s_setprio 1
	s_waitcnt lgkmcnt(0)
	v_mfma_f32_16x16x128_f8f6f4 v[174:177], v[232:239], v[22:29], v[174:177]
	v_mfma_f32_16x16x128_f8f6f4 v[170:173], v[240:247], v[22:29], v[170:173]
	v_mfma_f32_16x16x128_f8f6f4 v[158:161], v[232:239], v[30:37], v[158:161]
	v_mfma_f32_16x16x128_f8f6f4 v[154:157], v[240:247], v[30:37], v[154:157]
	v_mfma_f32_16x16x128_f8f6f4 v[142:145], v[232:239], v[38:45], v[142:145]
	v_mfma_f32_16x16x128_f8f6f4 v[138:141], v[240:247], v[38:45], v[138:141]
	v_mfma_f32_16x16x128_f8f6f4 v[126:129], v[232:239], v[188:195], v[126:129]
	v_mfma_f32_16x16x128_f8f6f4 v[122:125], v[240:247], v[188:195], v[122:125]
	s_setprio 0
	s_mov_b32 m0, s75
	v_lshl_add_u64 v[20:21], v[20:21], 0, s[24:25]
	s_barrier
	ds_read_b128 v[22:25], v221 offset:49152
	ds_read_b128 v[26:29], v221 offset:50176
	ds_read_b128 v[30:33], v221 offset:51200
	ds_read_b128 v[34:37], v221 offset:52224
	ds_read_b128 v[38:41], v221 offset:53248
	ds_read_b128 v[42:45], v221 offset:54272
	ds_read_b128 v[188:191], v221 offset:55296
	ds_read_b128 v[192:195], v221 offset:56320
	global_load_lds_dwordx4 v[20:21], off
	v_lshl_add_u64 v[18:19], v[18:19], 0, s[24:25]
	s_mov_b32 m0, s76
	s_nop 0
	global_load_lds_dwordx4 v[18:19], off
	s_barrier
	s_waitcnt lgkmcnt(0)
	s_setprio 1
	s_waitcnt lgkmcnt(0)
	v_mfma_f32_16x16x128_f8f6f4 v[102:105], v[2:9], v[22:29], v[102:105]
	v_mfma_f32_16x16x128_f8f6f4 v[98:101], v[10:17], v[22:29], v[98:101]
	v_mfma_f32_16x16x128_f8f6f4 v[86:89], v[2:9], v[30:37], v[86:89]
	v_mfma_f32_16x16x128_f8f6f4 v[82:85], v[10:17], v[30:37], v[82:85]
	v_mfma_f32_16x16x128_f8f6f4 v[70:73], v[2:9], v[38:45], v[70:73]
	v_mfma_f32_16x16x128_f8f6f4 v[66:69], v[10:17], v[38:45], v[66:69]
	v_mfma_f32_16x16x128_f8f6f4 v[54:57], v[2:9], v[188:195], v[54:57]
	v_mfma_f32_16x16x128_f8f6f4 v[50:53], v[10:17], v[188:195], v[50:53]
	s_setprio 0
	s_barrier
	s_add_u32 s8, s8, 0x20080
	s_addc_u32 s9, s9, 0
	s_mov_b32 m0, s77
	v_lshl_add_u64 v[2:3], s[8:9], 0, v[182:183]
	global_load_lds_dwordx4 v[2:3], off
	v_lshl_add_u64 v[2:3], s[8:9], 0, v[180:181]
	s_mov_b32 m0, s78
	s_nop 0
	global_load_lds_dwordx4 v[2:3], off
	s_waitcnt vmcnt(6)
	s_barrier
	s_setprio 1
	v_mfma_f32_16x16x128_f8f6f4 v[110:113], v[232:239], v[22:29], v[110:113]
	v_mfma_f32_16x16x128_f8f6f4 v[106:109], v[240:247], v[22:29], v[106:109]
	v_mfma_f32_16x16x128_f8f6f4 v[94:97], v[232:239], v[30:37], v[94:97]
	v_mfma_f32_16x16x128_f8f6f4 v[90:93], v[240:247], v[30:37], v[90:93]
	v_mfma_f32_16x16x128_f8f6f4 v[78:81], v[232:239], v[38:45], v[78:81]
	v_mfma_f32_16x16x128_f8f6f4 v[74:77], v[240:247], v[38:45], v[74:77]
	v_mfma_f32_16x16x128_f8f6f4 v[62:65], v[232:239], v[188:195], v[62:65]
	v_mfma_f32_16x16x128_f8f6f4 v[58:61], v[240:247], v[188:195], v[58:61]
	s_setprio 0
	s_add_i32 s83, s83, 2
	s_add_u32 s50, s50, 0x100
	s_addc_u32 s51, s51, 0
	s_cmp_gt_u32 s83, 5
	s_barrier
	s_cbranch_scc1 .LBB0_1689

.LBB0_1791:
	s_ashr_i32 s21, s20, 31
	ds_read_b128 v[2:5], v165
	ds_read_b128 v[6:9], v166
	ds_read_b128 v[10:13], v167
	ds_read_b128 v[14:17], v168
	s_lshl_b64 s[34:35], s[20:21], 18
	s_add_u32 s34, s51, s34
	s_addc_u32 s35, s52, s35
	s_and_b64 s[6:7], s[6:7], exec
	s_cselect_b32 s15, s35, s45
	s_cselect_b32 s21, s34, s44
	s_lshl_b32 s40, s40, 8
	s_ashr_i32 s41, s40, 31
	s_add_u32 s6, s44, 0x20080
	s_addc_u32 s7, s45, 0
	s_add_i32 s39, s55, 0xc000
	v_add_u32_e32 v181, s66, v164
	v_lshl_add_u64 v[42:43], s[6:7], 0, v[146:147]
	s_mov_b32 m0, s39
	s_add_i32 s74, s55, 0xe000
	ds_read_b128 v[18:21], v181
	ds_read_b128 v[22:25], v181 offset:1024
	ds_read_b128 v[26:29], v181 offset:2048
	ds_read_b128 v[30:33], v181 offset:3072
	ds_read_b128 v[34:37], v181 offset:4096
	ds_read_b128 v[38:41], v181 offset:5120
	ds_read_b128 v[50:53], v181 offset:6144
	ds_read_b128 v[54:57], v181 offset:7168
	global_load_lds_dwordx4 v[42:43], off
	v_lshl_add_u64 v[42:43], s[6:7], 0, v[148:149]
	s_mov_b32 m0, s74
	s_nop 0
	global_load_lds_dwordx4 v[42:43], off
	s_waitcnt lgkmcnt(8)
	s_barrier
	s_waitcnt lgkmcnt(0)
	s_setprio 1
	s_waitcnt lgkmcnt(0)
	v_mfma_f32_16x16x128_f8f6f4 v[142:145], v[2:9], v[18:25], 0
	v_mfma_f32_16x16x128_f8f6f4 v[138:141], v[10:17], v[18:25], 0
	v_mfma_f32_16x16x128_f8f6f4 v[134:137], v[2:9], v[26:33], 0
	v_mfma_f32_16x16x128_f8f6f4 v[130:133], v[10:17], v[26:33], 0
	v_mfma_f32_16x16x128_f8f6f4 v[122:125], v[2:9], v[34:41], 0
	v_mfma_f32_16x16x128_f8f6f4 v[114:117], v[10:17], v[34:41], 0
	v_mfma_f32_16x16x128_f8f6f4 v[106:109], v[2:9], v[50:57], 0
	v_mfma_f32_16x16x128_f8f6f4 v[98:101], v[10:17], v[50:57], 0
	s_setprio 0
	s_barrier
	v_lshl_add_u64 v[160:161], s[42:43], 0, v[0:1]
	s_mov_b64 s[6:7], 0x100
	s_mov_b32 m0, s56
	v_lshl_add_u64 v[42:43], v[160:161], 0, s[6:7]
	v_lshl_add_u64 v[162:163], s[42:43], 0, v[150:151]
	ds_read_b128 v[188:191], v169
	ds_read_b128 v[192:195], v170
	ds_read_b128 v[196:199], v171
	ds_read_b128 v[200:203], v172
	global_load_lds_dwordx4 v[42:43], off
	v_lshl_add_u64 v[42:43], v[162:163], 0, s[6:7]
	s_mov_b32 m0, s57
	s_nop 0
	global_load_lds_dwordx4 v[42:43], off
	s_barrier
	s_waitcnt lgkmcnt(0)
	s_setprio 1
	s_waitcnt lgkmcnt(0)
	v_mfma_f32_16x16x128_f8f6f4 v[78:81], v[188:195], v[18:25], 0
	v_mfma_f32_16x16x128_f8f6f4 v[74:77], v[196:203], v[18:25], 0
	v_mfma_f32_16x16x128_f8f6f4 v[70:73], v[188:195], v[26:33], 0
	v_mfma_f32_16x16x128_f8f6f4 v[66:69], v[196:203], v[26:33], 0
	v_mfma_f32_16x16x128_f8f6f4 v[62:65], v[188:195], v[34:41], 0
	v_mfma_f32_16x16x128_f8f6f4 v[58:61], v[196:203], v[34:41], 0
	v_mfma_f32_16x16x128_f8f6f4 v[46:49], v[188:195], v[50:57], 0
	v_mfma_f32_16x16x128_f8f6f4 v[42:45], v[196:203], v[50:57], 0
	s_setprio 0
	v_lshl_add_u64 v[156:157], s[44:45], 0, v[146:147]
	s_mov_b32 m0, s55
	v_lshl_add_u64 v[34:35], v[156:157], 0, s[6:7]
	v_lshl_add_u64 v[158:159], s[44:45], 0, v[148:149]
	s_barrier
	ds_read_b128 v[18:21], v181 offset:16384
	ds_read_b128 v[22:25], v181 offset:17408
	ds_read_b128 v[26:29], v181 offset:18432
	ds_read_b128 v[30:33], v181 offset:19456
	ds_read_b128 v[204:207], v181 offset:20480
	ds_read_b128 v[208:211], v181 offset:21504
	ds_read_b128 v[212:215], v181 offset:22528
	ds_read_b128 v[216:219], v181 offset:23552
	global_load_lds_dwordx4 v[34:35], off
	v_lshl_add_u64 v[34:35], v[158:159], 0, s[6:7]
	s_mov_b32 m0, s58
	s_nop 0
	global_load_lds_dwordx4 v[34:35], off
	s_barrier
	s_waitcnt lgkmcnt(0)
	s_setprio 1
	s_waitcnt lgkmcnt(0)
	v_mfma_f32_16x16x128_f8f6f4 v[126:129], v[2:9], v[18:25], 0
	v_mfma_f32_16x16x128_f8f6f4 v[118:121], v[10:17], v[18:25], 0
	v_mfma_f32_16x16x128_f8f6f4 v[110:113], v[2:9], v[26:33], 0
	v_mfma_f32_16x16x128_f8f6f4 v[102:105], v[10:17], v[26:33], 0
	v_mfma_f32_16x16x128_f8f6f4 v[94:97], v[2:9], v[204:211], 0
	v_mfma_f32_16x16x128_f8f6f4 v[90:93], v[10:17], v[204:211], 0
	v_mfma_f32_16x16x128_f8f6f4 v[86:89], v[2:9], v[212:219], 0
	v_mfma_f32_16x16x128_f8f6f4 v[82:85], v[10:17], v[212:219], 0
	s_setprio 0
	s_barrier
	s_add_u32 s6, s42, 0x20100
	s_addc_u32 s7, s43, 0
	s_mov_b32 m0, s59
	v_lshl_add_u64 v[2:3], s[6:7], 0, v[0:1]
	global_load_lds_dwordx4 v[2:3], off
	v_lshl_add_u64 v[2:3], s[6:7], 0, v[150:151]
	s_mov_b32 m0, s60
	s_nop 0
	global_load_lds_dwordx4 v[2:3], off
	s_waitcnt vmcnt(6)
	s_barrier
	s_setprio 1
	v_mfma_f32_16x16x128_f8f6f4 v[54:57], v[188:195], v[18:25], 0
	v_mfma_f32_16x16x128_f8f6f4 v[50:53], v[196:203], v[18:25], 0
	v_mfma_f32_16x16x128_f8f6f4 v[38:41], v[188:195], v[26:33], 0
	v_mfma_f32_16x16x128_f8f6f4 v[34:37], v[196:203], v[26:33], 0
	v_mfma_f32_16x16x128_f8f6f4 v[30:33], v[188:195], v[204:211], 0
	v_mfma_f32_16x16x128_f8f6f4 v[26:29], v[196:203], v[204:211], 0
	v_mfma_f32_16x16x128_f8f6f4 v[22:25], v[188:195], v[212:219], 0
	v_mfma_f32_16x16x128_f8f6f4 v[18:21], v[196:203], v[212:219], 0
	s_setprio 0
	s_barrier
	ds_read_b128 v[2:5], v173
	ds_read_b128 v[6:9], v174
	ds_read_b128 v[10:13], v175
	ds_read_b128 v[14:17], v176
	s_add_u32 s6, s44, 0x20100
	s_addc_u32 s7, s45, 0
	s_mov_b32 m0, s61
	v_lshl_add_u64 v[182:183], s[6:7], 0, v[146:147]
	ds_read_b128 v[188:191], v181 offset:32768
	ds_read_b128 v[192:195], v181 offset:33792
	ds_read_b128 v[196:199], v181 offset:34816
	ds_read_b128 v[200:203], v181 offset:35840
	ds_read_b128 v[204:207], v181 offset:36864
	ds_read_b128 v[208:211], v181 offset:37888
	ds_read_b128 v[212:215], v181 offset:38912
	ds_read_b128 v[216:219], v181 offset:39936
	global_load_lds_dwordx4 v[182:183], off
	v_lshl_add_u64 v[182:183], s[6:7], 0, v[148:149]
	s_mov_b32 m0, s62
	s_nop 0
	global_load_lds_dwordx4 v[182:183], off
	s_waitcnt lgkmcnt(8)
	s_barrier
	s_waitcnt lgkmcnt(0)
	s_setprio 1
	s_waitcnt lgkmcnt(0)
	v_mfma_f32_16x16x128_f8f6f4 v[142:145], v[2:9], v[188:195], v[142:145]
	v_mfma_f32_16x16x128_f8f6f4 v[138:141], v[10:17], v[188:195], v[138:141]
	v_mfma_f32_16x16x128_f8f6f4 v[134:137], v[2:9], v[196:203], v[134:137]
	v_mfma_f32_16x16x128_f8f6f4 v[130:133], v[10:17], v[196:203], v[130:133]
	v_mfma_f32_16x16x128_f8f6f4 v[122:125], v[2:9], v[204:211], v[122:125]
	v_mfma_f32_16x16x128_f8f6f4 v[114:117], v[10:17], v[204:211], v[114:117]
	v_mfma_f32_16x16x128_f8f6f4 v[106:109], v[2:9], v[212:219], v[106:109]
	v_mfma_f32_16x16x128_f8f6f4 v[98:101], v[10:17], v[212:219], v[98:101]
	s_setprio 0
	s_barrier
	s_mov_b64 s[6:7], 0x180
	s_mov_b32 m0, s67
	v_lshl_add_u64 v[160:161], v[160:161], 0, s[6:7]
	ds_read_b128 v[232:235], v177
	ds_read_b128 v[236:239], v178
	ds_read_b128 v[240:243], v179
	ds_read_b128 v[244:247], v180
	global_load_lds_dwordx4 v[160:161], off
	v_lshl_add_u64 v[160:161], v[162:163], 0, s[6:7]
	s_mov_b32 m0, s68
	s_nop 0
	global_load_lds_dwordx4 v[160:161], off
	s_barrier
	s_waitcnt lgkmcnt(0)
	s_setprio 1
	s_waitcnt lgkmcnt(0)
	v_mfma_f32_16x16x128_f8f6f4 v[78:81], v[232:239], v[188:195], v[78:81]
	v_mfma_f32_16x16x128_f8f6f4 v[74:77], v[240:247], v[188:195], v[74:77]
	v_mfma_f32_16x16x128_f8f6f4 v[70:73], v[232:239], v[196:203], v[70:73]
	v_mfma_f32_16x16x128_f8f6f4 v[66:69], v[240:247], v[196:203], v[66:69]
	v_mfma_f32_16x16x128_f8f6f4 v[62:65], v[232:239], v[204:211], v[62:65]
	v_mfma_f32_16x16x128_f8f6f4 v[58:61], v[240:247], v[204:211], v[58:61]
	v_mfma_f32_16x16x128_f8f6f4 v[46:49], v[232:239], v[212:219], v[46:49]
	v_mfma_f32_16x16x128_f8f6f4 v[42:45], v[240:247], v[212:219], v[42:45]
	s_setprio 0
	s_mov_b32 m0, s69
	v_lshl_add_u64 v[156:157], v[156:157], 0, s[6:7]
	s_barrier
	ds_read_b128 v[188:191], v181 offset:49152
	ds_read_b128 v[192:195], v181 offset:50176
	ds_read_b128 v[196:199], v181 offset:51200
	ds_read_b128 v[200:203], v181 offset:52224
	ds_read_b128 v[204:207], v181 offset:53248
	ds_read_b128 v[208:211], v181 offset:54272
	ds_read_b128 v[212:215], v181 offset:55296
	ds_read_b128 v[216:219], v181 offset:56320
	global_load_lds_dwordx4 v[156:157], off
	v_lshl_add_u64 v[156:157], v[158:159], 0, s[6:7]
	s_mov_b32 m0, s70
	s_nop 0
	global_load_lds_dwordx4 v[156:157], off
	s_barrier
	s_waitcnt lgkmcnt(0)
	s_setprio 1
	s_waitcnt lgkmcnt(0)
	v_mfma_f32_16x16x128_f8f6f4 v[126:129], v[2:9], v[188:195], v[126:129]
	v_mfma_f32_16x16x128_f8f6f4 v[118:121], v[10:17], v[188:195], v[118:121]
	v_mfma_f32_16x16x128_f8f6f4 v[110:113], v[2:9], v[196:203], v[110:113]
	v_mfma_f32_16x16x128_f8f6f4 v[102:105], v[10:17], v[196:203], v[102:105]
	v_mfma_f32_16x16x128_f8f6f4 v[94:97], v[2:9], v[204:211], v[94:97]
	v_mfma_f32_16x16x128_f8f6f4 v[90:93], v[10:17], v[204:211], v[90:93]
	v_mfma_f32_16x16x128_f8f6f4 v[86:89], v[2:9], v[212:219], v[86:89]
	v_mfma_f32_16x16x128_f8f6f4 v[82:85], v[10:17], v[212:219], v[82:85]
	s_setprio 0
	s_barrier
	s_add_u32 s6, s42, 0x20180
	s_addc_u32 s7, s43, 0
	s_mov_b32 m0, s71
	v_lshl_add_u64 v[2:3], s[6:7], 0, v[0:1]
	global_load_lds_dwordx4 v[2:3], off
	v_lshl_add_u64 v[2:3], s[6:7], 0, v[150:151]
	s_mov_b32 m0, s72
	s_nop 0
	global_load_lds_dwordx4 v[2:3], off
	s_waitcnt vmcnt(6)
	s_barrier
	s_setprio 1
	v_mfma_f32_16x16x128_f8f6f4 v[54:57], v[232:239], v[188:195], v[54:57]
	v_mfma_f32_16x16x128_f8f6f4 v[50:53], v[240:247], v[188:195], v[50:53]
	v_mfma_f32_16x16x128_f8f6f4 v[38:41], v[232:239], v[196:203], v[38:41]
	v_mfma_f32_16x16x128_f8f6f4 v[34:37], v[240:247], v[196:203], v[34:37]
	v_mfma_f32_16x16x128_f8f6f4 v[30:33], v[232:239], v[204:211], v[30:33]
	v_mfma_f32_16x16x128_f8f6f4 v[26:29], v[240:247], v[204:211], v[26:29]
	v_mfma_f32_16x16x128_f8f6f4 v[22:25], v[232:239], v[212:219], v[22:25]
	v_mfma_f32_16x16x128_f8f6f4 v[18:21], v[240:247], v[212:219], v[18:21]
	s_setprio 0
	s_lshl_b64 s[6:7], s[40:41], 2
	s_add_u32 s41, s28, s6
	s_addc_u32 s75, s65, s7
	s_add_u32 s44, s44, 0x20180
	s_addc_u32 s45, s45, 0
	s_add_u32 s76, s42, 0x200
	s_addc_u32 s77, s43, 0
	s_mov_b32 s78, 0
	s_barrier
	s_branch .LBB0_1793
.LBB0_1792:
	ds_read_b128 v[10:13], v165
	ds_read_b128 v[14:17], v166
	ds_read_b128 v[156:159], v167
	ds_read_b128 v[160:163], v168
	s_add_u32 s79, s44, 0xfffe0080
	s_addc_u32 s80, s45, -1
	s_and_b64 s[6:7], s[42:43], exec
	s_cselect_b32 s43, s15, s80
	s_cselect_b32 s42, s21, s79
	s_cselect_b32 s7, s9, s77
	s_cselect_b32 s6, s8, s76
	s_mov_b32 m0, s39
	v_lshl_add_u64 v[2:3], s[44:45], 0, v[152:153]
	ds_read_b128 v[188:191], v181
	ds_read_b128 v[192:195], v181 offset:1024
	ds_read_b128 v[196:199], v181 offset:2048
	ds_read_b128 v[200:203], v181 offset:3072
	ds_read_b128 v[204:207], v181 offset:4096
	ds_read_b128 v[208:211], v181 offset:5120
	ds_read_b128 v[212:215], v181 offset:6144
	ds_read_b128 v[216:219], v181 offset:7168
	global_load_lds_dwordx4 v[2:3], off
	v_lshl_add_u64 v[2:3], s[44:45], 0, v[154:155]
	s_mov_b32 m0, s74
	s_nop 0
	global_load_lds_dwordx4 v[2:3], off
	s_waitcnt lgkmcnt(8)
	s_barrier
	s_waitcnt lgkmcnt(0)
	s_setprio 1
	s_waitcnt lgkmcnt(0)
	v_mfma_f32_16x16x128_f8f6f4 v[142:145], v[10:17], v[188:195], v[142:145]
	v_mfma_f32_16x16x128_f8f6f4 v[138:141], v[156:163], v[188:195], v[138:141]
	v_mfma_f32_16x16x128_f8f6f4 v[134:137], v[10:17], v[196:203], v[134:137]
	v_mfma_f32_16x16x128_f8f6f4 v[130:133], v[156:163], v[196:203], v[130:133]
	v_mfma_f32_16x16x128_f8f6f4 v[122:125], v[10:17], v[204:211], v[122:125]
	v_mfma_f32_16x16x128_f8f6f4 v[114:117], v[156:163], v[204:211], v[114:117]
	v_mfma_f32_16x16x128_f8f6f4 v[106:109], v[10:17], v[212:219], v[106:109]
	v_mfma_f32_16x16x128_f8f6f4 v[98:101], v[156:163], v[212:219], v[98:101]
	s_setprio 0
	s_barrier
	s_mov_b32 m0, s56
	v_lshl_add_u64 v[6:7], s[6:7], 0, v[0:1]
	ds_read_b128 v[232:235], v169
	ds_read_b128 v[236:239], v170
	ds_read_b128 v[240:243], v171
	ds_read_b128 v[244:247], v172
	global_load_lds_dwordx4 v[6:7], off
	v_lshl_add_u64 v[8:9], s[6:7], 0, v[150:151]
	s_mov_b32 m0, s57
	s_nop 0
	global_load_lds_dwordx4 v[8:9], off
	s_barrier
	s_waitcnt lgkmcnt(0)
	s_setprio 1
	s_waitcnt lgkmcnt(0)
	v_mfma_f32_16x16x128_f8f6f4 v[78:81], v[232:239], v[188:195], v[78:81]
	v_mfma_f32_16x16x128_f8f6f4 v[74:77], v[240:247], v[188:195], v[74:77]
	v_mfma_f32_16x16x128_f8f6f4 v[70:73], v[232:239], v[196:203], v[70:73]
	v_mfma_f32_16x16x128_f8f6f4 v[66:69], v[240:247], v[196:203], v[66:69]
	v_mfma_f32_16x16x128_f8f6f4 v[62:65], v[232:239], v[204:211], v[62:65]
	v_mfma_f32_16x16x128_f8f6f4 v[58:61], v[240:247], v[204:211], v[58:61]
	v_mfma_f32_16x16x128_f8f6f4 v[46:49], v[232:239], v[212:219], v[46:49]
	v_mfma_f32_16x16x128_f8f6f4 v[42:45], v[240:247], v[212:219], v[42:45]
	s_setprio 0
	s_mov_b32 m0, s55
	v_lshl_add_u64 v[2:3], s[42:43], 0, v[146:147]
	s_barrier
	ds_read_b128 v[188:191], v181 offset:16384
	ds_read_b128 v[192:195], v181 offset:17408
	ds_read_b128 v[196:199], v181 offset:18432
	ds_read_b128 v[200:203], v181 offset:19456
	ds_read_b128 v[204:207], v181 offset:20480
	ds_read_b128 v[208:211], v181 offset:21504
	ds_read_b128 v[212:215], v181 offset:22528
	ds_read_b128 v[216:219], v181 offset:23552
	global_load_lds_dwordx4 v[2:3], off
	v_lshl_add_u64 v[4:5], s[42:43], 0, v[148:149]
	s_mov_b32 m0, s58
	s_nop 0
	global_load_lds_dwordx4 v[4:5], off
	s_barrier
	s_waitcnt lgkmcnt(0)
	s_setprio 1
	s_waitcnt lgkmcnt(0)
	v_mfma_f32_16x16x128_f8f6f4 v[126:129], v[10:17], v[188:195], v[126:129]
	v_mfma_f32_16x16x128_f8f6f4 v[118:121], v[156:163], v[188:195], v[118:121]
	v_mfma_f32_16x16x128_f8f6f4 v[110:113], v[10:17], v[196:203], v[110:113]
	v_mfma_f32_16x16x128_f8f6f4 v[102:105], v[156:163], v[196:203], v[102:105]
	v_mfma_f32_16x16x128_f8f6f4 v[94:97], v[10:17], v[204:211], v[94:97]
	v_mfma_f32_16x16x128_f8f6f4 v[90:93], v[156:163], v[204:211], v[90:93]
	v_mfma_f32_16x16x128_f8f6f4 v[86:89], v[10:17], v[212:219], v[86:89]
	v_mfma_f32_16x16x128_f8f6f4 v[82:85], v[156:163], v[212:219], v[82:85]
	s_setprio 0
	s_barrier
	s_add_u32 s80, s6, 0x20000
	s_addc_u32 s81, s7, 0
	s_mov_b32 m0, s59
	v_lshl_add_u64 v[10:11], s[80:81], 0, v[0:1]
	global_load_lds_dwordx4 v[10:11], off
	v_lshl_add_u64 v[10:11], s[80:81], 0, v[150:151]
	s_mov_b32 m0, s60
	s_nop 0
	global_load_lds_dwordx4 v[10:11], off
	s_waitcnt vmcnt(6)
	s_barrier
	s_setprio 1
	v_mfma_f32_16x16x128_f8f6f4 v[54:57], v[232:239], v[188:195], v[54:57]
	v_mfma_f32_16x16x128_f8f6f4 v[50:53], v[240:247], v[188:195], v[50:53]
	v_mfma_f32_16x16x128_f8f6f4 v[38:41], v[232:239], v[196:203], v[38:41]
	v_mfma_f32_16x16x128_f8f6f4 v[34:37], v[240:247], v[196:203], v[34:37]
	v_mfma_f32_16x16x128_f8f6f4 v[30:33], v[232:239], v[204:211], v[30:33]
	v_mfma_f32_16x16x128_f8f6f4 v[26:29], v[240:247], v[204:211], v[26:29]
	v_mfma_f32_16x16x128_f8f6f4 v[22:25], v[232:239], v[212:219], v[22:25]
	v_mfma_f32_16x16x128_f8f6f4 v[18:21], v[240:247], v[212:219], v[18:21]
	s_setprio 0
	s_barrier
	ds_read_b128 v[10:13], v173
	ds_read_b128 v[14:17], v174
	ds_read_b128 v[156:159], v175
	ds_read_b128 v[160:163], v176
	s_add_u32 s42, s42, 0x20000
	s_addc_u32 s43, s43, 0
	s_mov_b32 m0, s61
	v_lshl_add_u64 v[182:183], s[42:43], 0, v[146:147]
	ds_read_b128 v[188:191], v181 offset:32768
	ds_read_b128 v[192:195], v181 offset:33792
	ds_read_b128 v[196:199], v181 offset:34816
	ds_read_b128 v[200:203], v181 offset:35840
	ds_read_b128 v[204:207], v181 offset:36864
	ds_read_b128 v[208:211], v181 offset:37888
	ds_read_b128 v[212:215], v181 offset:38912
	ds_read_b128 v[216:219], v181 offset:39936
	global_load_lds_dwordx4 v[182:183], off
	v_lshl_add_u64 v[182:183], s[42:43], 0, v[148:149]
	s_mov_b32 m0, s62
	s_nop 0
	global_load_lds_dwordx4 v[182:183], off
	s_waitcnt lgkmcnt(8)
	s_barrier
	s_waitcnt lgkmcnt(0)
	s_setprio 1
	s_waitcnt lgkmcnt(0)
	v_mfma_f32_16x16x128_f8f6f4 v[142:145], v[10:17], v[188:195], v[142:145]
	v_mfma_f32_16x16x128_f8f6f4 v[138:141], v[156:163], v[188:195], v[138:141]
	v_mfma_f32_16x16x128_f8f6f4 v[134:137], v[10:17], v[196:203], v[134:137]
	v_mfma_f32_16x16x128_f8f6f4 v[130:133], v[156:163], v[196:203], v[130:133]
	v_mfma_f32_16x16x128_f8f6f4 v[122:125], v[10:17], v[204:211], v[122:125]
	v_mfma_f32_16x16x128_f8f6f4 v[114:117], v[156:163], v[204:211], v[114:117]
	v_mfma_f32_16x16x128_f8f6f4 v[106:109], v[10:17], v[212:219], v[106:109]
	v_mfma_f32_16x16x128_f8f6f4 v[98:101], v[156:163], v[212:219], v[98:101]
	s_setprio 0
	s_barrier
	s_mov_b32 m0, s67
	v_lshl_add_u64 v[6:7], v[6:7], 0, s[24:25]
	ds_read_b128 v[232:235], v177
	ds_read_b128 v[236:239], v178
	ds_read_b128 v[240:243], v179
	ds_read_b128 v[244:247], v180
	global_load_lds_dwordx4 v[6:7], off
	v_lshl_add_u64 v[6:7], v[8:9], 0, s[24:25]
	s_mov_b32 m0, s68
	s_nop 0
	global_load_lds_dwordx4 v[6:7], off
	s_barrier
	s_waitcnt lgkmcnt(0)
	s_setprio 1
	s_waitcnt lgkmcnt(0)
	v_mfma_f32_16x16x128_f8f6f4 v[78:81], v[232:239], v[188:195], v[78:81]
	v_mfma_f32_16x16x128_f8f6f4 v[74:77], v[240:247], v[188:195], v[74:77]
	v_mfma_f32_16x16x128_f8f6f4 v[70:73], v[232:239], v[196:203], v[70:73]
	v_mfma_f32_16x16x128_f8f6f4 v[66:69], v[240:247], v[196:203], v[66:69]
	v_mfma_f32_16x16x128_f8f6f4 v[62:65], v[232:239], v[204:211], v[62:65]
	v_mfma_f32_16x16x128_f8f6f4 v[58:61], v[240:247], v[204:211], v[58:61]
	v_mfma_f32_16x16x128_f8f6f4 v[46:49], v[232:239], v[212:219], v[46:49]
	v_mfma_f32_16x16x128_f8f6f4 v[42:45], v[240:247], v[212:219], v[42:45]
	s_setprio 0
	s_mov_b32 m0, s69
	v_lshl_add_u64 v[2:3], v[2:3], 0, s[24:25]
	s_barrier
	ds_read_b128 v[188:191], v181 offset:49152
	ds_read_b128 v[192:195], v181 offset:50176
	ds_read_b128 v[196:199], v181 offset:51200
	ds_read_b128 v[200:203], v181 offset:52224
	ds_read_b128 v[204:207], v181 offset:53248
	ds_read_b128 v[208:211], v181 offset:54272
	ds_read_b128 v[212:215], v181 offset:55296
	ds_read_b128 v[216:219], v181 offset:56320
	global_load_lds_dwordx4 v[2:3], off
	v_lshl_add_u64 v[2:3], v[4:5], 0, s[24:25]
	s_mov_b32 m0, s70
	s_nop 0
	global_load_lds_dwordx4 v[2:3], off
	s_barrier
	s_waitcnt lgkmcnt(0)
	s_setprio 1
	s_waitcnt lgkmcnt(0)
	v_mfma_f32_16x16x128_f8f6f4 v[126:129], v[10:17], v[188:195], v[126:129]
	v_mfma_f32_16x16x128_f8f6f4 v[118:121], v[156:163], v[188:195], v[118:121]
	v_mfma_f32_16x16x128_f8f6f4 v[110:113], v[10:17], v[196:203], v[110:113]
	v_mfma_f32_16x16x128_f8f6f4 v[102:105], v[156:163], v[196:203], v[102:105]
	v_mfma_f32_16x16x128_f8f6f4 v[94:97], v[10:17], v[204:211], v[94:97]
	v_mfma_f32_16x16x128_f8f6f4 v[90:93], v[156:163], v[204:211], v[90:93]
	v_mfma_f32_16x16x128_f8f6f4 v[86:89], v[10:17], v[212:219], v[86:89]
	v_mfma_f32_16x16x128_f8f6f4 v[82:85], v[156:163], v[212:219], v[82:85]
	s_setprio 0
	s_barrier
	s_add_u32 s6, s6, 0x20080
	s_addc_u32 s7, s7, 0
	s_mov_b32 m0, s71
	v_lshl_add_u64 v[2:3], s[6:7], 0, v[0:1]
	global_load_lds_dwordx4 v[2:3], off
	v_lshl_add_u64 v[2:3], s[6:7], 0, v[150:151]
	s_mov_b32 m0, s72
	s_nop 0
	global_load_lds_dwordx4 v[2:3], off
	s_waitcnt vmcnt(6)
	s_barrier
	s_setprio 1
	v_mfma_f32_16x16x128_f8f6f4 v[54:57], v[232:239], v[188:195], v[54:57]
	v_mfma_f32_16x16x128_f8f6f4 v[50:53], v[240:247], v[188:195], v[50:53]
	v_mfma_f32_16x16x128_f8f6f4 v[38:41], v[232:239], v[196:203], v[38:41]
	v_mfma_f32_16x16x128_f8f6f4 v[34:37], v[240:247], v[196:203], v[34:37]
	v_mfma_f32_16x16x128_f8f6f4 v[30:33], v[232:239], v[204:211], v[30:33]
	v_mfma_f32_16x16x128_f8f6f4 v[26:29], v[240:247], v[204:211], v[26:29]
	v_mfma_f32_16x16x128_f8f6f4 v[22:25], v[232:239], v[212:219], v[22:25]
	v_mfma_f32_16x16x128_f8f6f4 v[18:21], v[240:247], v[212:219], v[18:21]
	s_setprio 0
	s_add_i32 s78, s78, 2
	s_add_u32 s44, s44, 0x100
	s_addc_u32 s45, s45, 0
	s_add_u32 s76, s76, 0x100
	s_addc_u32 s77, s77, 0
	s_cmp_gt_u32 s78, 5
	s_barrier
	s_cbranch_scc1 .LBB0_1782

.LBB0_1925:
	ds_read_b128 v[2:5], v233
	ds_read_b128 v[6:9], v234
	ds_read_b128 v[10:13], v235
	ds_read_b128 v[14:17], v236
	s_add_u32 s40, s6, 0xfffe0080
	s_addc_u32 s41, s7, -1
	s_cmp_eq_u32 s71, 4
	s_cselect_b32 s43, s21, s41
	s_cselect_b32 s42, s67, s40
	s_cselect_b32 s41, s15, s70
	s_cselect_b32 s40, s68, s69
	v_add_u32_e32 v0, s55, v232
	v_lshl_add_u64 v[146:147], s[6:7], 0, v[204:205]
	s_add_i32 m0, s47, 0xc000
	ds_read_b128 v[150:153], v0
	ds_read_b128 v[154:157], v0 offset:1024
	ds_read_b128 v[158:161], v0 offset:2048
	ds_read_b128 v[162:165], v0 offset:3072
	ds_read_b128 v[166:169], v0 offset:4096
	ds_read_b128 v[170:173], v0 offset:5120
	ds_read_b128 v[174:177], v0 offset:6144
	ds_read_b128 v[178:181], v0 offset:7168
	global_load_lds_dwordx4 v[146:147], off
	v_lshl_add_u64 v[146:147], s[6:7], 0, v[206:207]
	s_add_i32 m0, s47, 0xe000
	s_nop 0
	global_load_lds_dwordx4 v[146:147], off
	s_waitcnt lgkmcnt(8)
	s_barrier
	s_waitcnt lgkmcnt(0)
	s_setprio 1
	s_waitcnt lgkmcnt(0)
	v_mfma_f32_16x16x128_f8f6f4 v[142:145], v[2:9], v[150:157], v[142:145]
	v_mfma_f32_16x16x128_f8f6f4 v[138:141], v[10:17], v[150:157], v[138:141]
	v_mfma_f32_16x16x128_f8f6f4 v[126:129], v[2:9], v[158:165], v[126:129]
	v_mfma_f32_16x16x128_f8f6f4 v[122:125], v[10:17], v[158:165], v[122:125]
	v_mfma_f32_16x16x128_f8f6f4 v[110:113], v[2:9], v[166:173], v[110:113]
	v_mfma_f32_16x16x128_f8f6f4 v[106:109], v[10:17], v[166:173], v[106:109]
	v_mfma_f32_16x16x128_f8f6f4 v[94:97], v[2:9], v[174:181], v[94:97]
	v_mfma_f32_16x16x128_f8f6f4 v[90:93], v[10:17], v[174:181], v[90:93]
	s_setprio 0
	s_barrier
	s_mov_b32 m0, s48
	v_lshl_add_u64 v[146:147], s[40:41], 0, v[200:201]
	ds_read_b128 v[188:191], v237
	ds_read_b128 v[192:195], v238
	ds_read_b128 v[208:211], v239
	ds_read_b128 v[212:215], v240
	global_load_lds_dwordx4 v[146:147], off
	v_lshl_add_u64 v[148:149], s[40:41], 0, v[196:197]
	s_mov_b32 m0, s49
	s_nop 0
	global_load_lds_dwordx4 v[148:149], off
	s_barrier
	s_waitcnt lgkmcnt(0)
	s_setprio 1
	s_waitcnt lgkmcnt(0)
	v_mfma_f32_16x16x128_f8f6f4 v[134:137], v[188:195], v[150:157], v[134:137]
	v_mfma_f32_16x16x128_f8f6f4 v[130:133], v[208:215], v[150:157], v[130:133]
	v_mfma_f32_16x16x128_f8f6f4 v[118:121], v[188:195], v[158:165], v[118:121]
	v_mfma_f32_16x16x128_f8f6f4 v[114:117], v[208:215], v[158:165], v[114:117]
	v_mfma_f32_16x16x128_f8f6f4 v[102:105], v[188:195], v[166:173], v[102:105]
	v_mfma_f32_16x16x128_f8f6f4 v[98:101], v[208:215], v[166:173], v[98:101]
	v_mfma_f32_16x16x128_f8f6f4 v[86:89], v[188:195], v[174:181], v[86:89]
	v_mfma_f32_16x16x128_f8f6f4 v[82:85], v[208:215], v[174:181], v[82:85]
	s_setprio 0
	s_mov_b32 m0, s47
	v_lshl_add_u64 v[150:151], s[42:43], 0, v[202:203]
	s_barrier
	ds_read_b128 v[154:157], v0 offset:16384
	ds_read_b128 v[158:161], v0 offset:17408
	ds_read_b128 v[162:165], v0 offset:18432
	ds_read_b128 v[166:169], v0 offset:19456
	ds_read_b128 v[170:173], v0 offset:20480
	ds_read_b128 v[174:177], v0 offset:21504
	ds_read_b128 v[178:181], v0 offset:22528
	ds_read_b128 v[182:185], v0 offset:23552
	global_load_lds_dwordx4 v[150:151], off
	v_lshl_add_u64 v[152:153], s[42:43], 0, v[198:199]
	s_mov_b32 m0, s50
	s_nop 0
	global_load_lds_dwordx4 v[152:153], off
	s_barrier
	s_waitcnt lgkmcnt(0)
	s_setprio 1
	s_waitcnt lgkmcnt(0)
	v_mfma_f32_16x16x128_f8f6f4 v[78:81], v[2:9], v[154:161], v[78:81]
	v_mfma_f32_16x16x128_f8f6f4 v[74:77], v[10:17], v[154:161], v[74:77]
	v_mfma_f32_16x16x128_f8f6f4 v[62:65], v[2:9], v[162:169], v[62:65]
	v_mfma_f32_16x16x128_f8f6f4 v[58:61], v[10:17], v[162:169], v[58:61]
	v_mfma_f32_16x16x128_f8f6f4 v[46:49], v[2:9], v[170:177], v[46:49]
	v_mfma_f32_16x16x128_f8f6f4 v[42:45], v[10:17], v[170:177], v[42:45]
	v_mfma_f32_16x16x128_f8f6f4 v[30:33], v[2:9], v[178:185], v[30:33]
	v_mfma_f32_16x16x128_f8f6f4 v[26:29], v[10:17], v[178:185], v[26:29]
	s_setprio 0
	s_barrier
	s_add_u32 s72, s40, 0x20000
	s_addc_u32 s73, s41, 0
	s_mov_b32 m0, s51
	v_lshl_add_u64 v[2:3], s[72:73], 0, v[200:201]
	global_load_lds_dwordx4 v[2:3], off
	v_lshl_add_u64 v[2:3], s[72:73], 0, v[196:197]
	s_mov_b32 m0, s52
	s_nop 0
	global_load_lds_dwordx4 v[2:3], off
	s_waitcnt vmcnt(6)
	s_barrier
	s_setprio 1
	v_mfma_f32_16x16x128_f8f6f4 v[70:73], v[188:195], v[154:161], v[70:73]
	v_mfma_f32_16x16x128_f8f6f4 v[66:69], v[208:215], v[154:161], v[66:69]
	v_mfma_f32_16x16x128_f8f6f4 v[54:57], v[188:195], v[162:169], v[54:57]
	v_mfma_f32_16x16x128_f8f6f4 v[50:53], v[208:215], v[162:169], v[50:53]
	v_mfma_f32_16x16x128_f8f6f4 v[38:41], v[188:195], v[170:177], v[38:41]
	v_mfma_f32_16x16x128_f8f6f4 v[34:37], v[208:215], v[170:177], v[34:37]
	v_mfma_f32_16x16x128_f8f6f4 v[22:25], v[188:195], v[178:185], v[22:25]
	v_mfma_f32_16x16x128_f8f6f4 v[18:21], v[208:215], v[178:185], v[18:21]
	s_setprio 0
	s_barrier
	ds_read_b128 v[2:5], v241
	ds_read_b128 v[6:9], v242
	ds_read_b128 v[10:13], v243
	ds_read_b128 v[14:17], v244
	s_add_u32 s42, s42, 0x20000
	s_addc_u32 s43, s43, 0
	s_mov_b32 m0, s53
	v_lshl_add_u64 v[188:189], s[42:43], 0, v[202:203]
	ds_read_b128 v[154:157], v0 offset:32768
	ds_read_b128 v[158:161], v0 offset:33792
	ds_read_b128 v[162:165], v0 offset:34816
	ds_read_b128 v[166:169], v0 offset:35840
	ds_read_b128 v[170:173], v0 offset:36864
	ds_read_b128 v[174:177], v0 offset:37888
	ds_read_b128 v[178:181], v0 offset:38912
	ds_read_b128 v[182:185], v0 offset:39936
	global_load_lds_dwordx4 v[188:189], off
	v_lshl_add_u64 v[188:189], s[42:43], 0, v[198:199]
	s_mov_b32 m0, s54
	s_nop 0
	global_load_lds_dwordx4 v[188:189], off
	s_waitcnt lgkmcnt(8)
	s_barrier
	s_waitcnt lgkmcnt(0)
	s_setprio 1
	s_waitcnt lgkmcnt(0)
	v_mfma_f32_16x16x128_f8f6f4 v[142:145], v[2:9], v[154:161], v[142:145]
	v_mfma_f32_16x16x128_f8f6f4 v[138:141], v[10:17], v[154:161], v[138:141]
	v_mfma_f32_16x16x128_f8f6f4 v[126:129], v[2:9], v[162:169], v[126:129]
	v_mfma_f32_16x16x128_f8f6f4 v[122:125], v[10:17], v[162:169], v[122:125]
	v_mfma_f32_16x16x128_f8f6f4 v[110:113], v[2:9], v[170:177], v[110:113]
	v_mfma_f32_16x16x128_f8f6f4 v[106:109], v[10:17], v[170:177], v[106:109]
	v_mfma_f32_16x16x128_f8f6f4 v[94:97], v[2:9], v[178:185], v[94:97]
	v_mfma_f32_16x16x128_f8f6f4 v[90:93], v[10:17], v[178:185], v[90:93]
	s_setprio 0
	s_barrier
	s_mov_b32 m0, s58
	v_lshl_add_u64 v[146:147], v[146:147], 0, s[24:25]
	ds_read_b128 v[188:191], v245
	ds_read_b128 v[192:195], v246
	ds_read_b128 v[208:211], v247
	ds_read_b128 v[212:215], v248
	global_load_lds_dwordx4 v[146:147], off
	v_lshl_add_u64 v[146:147], v[148:149], 0, s[24:25]
	s_mov_b32 m0, s59
	s_nop 0
	global_load_lds_dwordx4 v[146:147], off
	s_barrier
	s_waitcnt lgkmcnt(0)
	s_setprio 1
	s_waitcnt lgkmcnt(0)
	v_mfma_f32_16x16x128_f8f6f4 v[134:137], v[188:195], v[154:161], v[134:137]
	v_mfma_f32_16x16x128_f8f6f4 v[130:133], v[208:215], v[154:161], v[130:133]
	v_mfma_f32_16x16x128_f8f6f4 v[118:121], v[188:195], v[162:169], v[118:121]
	v_mfma_f32_16x16x128_f8f6f4 v[114:117], v[208:215], v[162:169], v[114:117]
	v_mfma_f32_16x16x128_f8f6f4 v[102:105], v[188:195], v[170:177], v[102:105]
	v_mfma_f32_16x16x128_f8f6f4 v[98:101], v[208:215], v[170:177], v[98:101]
	v_mfma_f32_16x16x128_f8f6f4 v[86:89], v[188:195], v[178:185], v[86:89]
	v_mfma_f32_16x16x128_f8f6f4 v[82:85], v[208:215], v[178:185], v[82:85]
	s_setprio 0
	s_mov_b32 m0, s60
	v_lshl_add_u64 v[146:147], v[150:151], 0, s[24:25]
	s_barrier
	ds_read_b128 v[154:157], v0 offset:49152
	ds_read_b128 v[158:161], v0 offset:50176
	ds_read_b128 v[162:165], v0 offset:51200
	ds_read_b128 v[166:169], v0 offset:52224
	ds_read_b128 v[170:173], v0 offset:53248
	ds_read_b128 v[174:177], v0 offset:54272
	ds_read_b128 v[178:181], v0 offset:55296
	ds_read_b128 v[182:185], v0 offset:56320
	global_load_lds_dwordx4 v[146:147], off
	v_lshl_add_u64 v[146:147], v[152:153], 0, s[24:25]
	s_mov_b32 m0, s61
	s_nop 0
	global_load_lds_dwordx4 v[146:147], off
	s_barrier
	s_waitcnt lgkmcnt(0)
	s_setprio 1
	s_waitcnt lgkmcnt(0)
	v_mfma_f32_16x16x128_f8f6f4 v[78:81], v[2:9], v[154:161], v[78:81]
	v_mfma_f32_16x16x128_f8f6f4 v[74:77], v[10:17], v[154:161], v[74:77]
	v_mfma_f32_16x16x128_f8f6f4 v[62:65], v[2:9], v[162:169], v[62:65]
	v_mfma_f32_16x16x128_f8f6f4 v[58:61], v[10:17], v[162:169], v[58:61]
	v_mfma_f32_16x16x128_f8f6f4 v[46:49], v[2:9], v[170:177], v[46:49]
	v_mfma_f32_16x16x128_f8f6f4 v[42:45], v[10:17], v[170:177], v[42:45]
	v_mfma_f32_16x16x128_f8f6f4 v[30:33], v[2:9], v[178:185], v[30:33]
	v_mfma_f32_16x16x128_f8f6f4 v[26:29], v[10:17], v[178:185], v[26:29]
	s_setprio 0
	s_barrier
	s_add_u32 s40, s40, 0x20080
	s_addc_u32 s41, s41, 0
	s_mov_b32 m0, s62
	v_lshl_add_u64 v[2:3], s[40:41], 0, v[200:201]
	global_load_lds_dwordx4 v[2:3], off
	v_lshl_add_u64 v[2:3], s[40:41], 0, v[196:197]
	s_mov_b32 m0, s63
	s_nop 0
	global_load_lds_dwordx4 v[2:3], off
	s_waitcnt vmcnt(6)
	s_barrier
	s_setprio 1
	v_mfma_f32_16x16x128_f8f6f4 v[70:73], v[188:195], v[154:161], v[70:73]
	v_mfma_f32_16x16x128_f8f6f4 v[66:69], v[208:215], v[154:161], v[66:69]
	v_mfma_f32_16x16x128_f8f6f4 v[54:57], v[188:195], v[162:169], v[54:57]
	v_mfma_f32_16x16x128_f8f6f4 v[50:53], v[208:215], v[162:169], v[50:53]
	v_mfma_f32_16x16x128_f8f6f4 v[38:41], v[188:195], v[170:177], v[38:41]
	v_mfma_f32_16x16x128_f8f6f4 v[34:37], v[208:215], v[170:177], v[34:37]
	v_mfma_f32_16x16x128_f8f6f4 v[22:25], v[188:195], v[178:185], v[22:25]
	v_mfma_f32_16x16x128_f8f6f4 v[18:21], v[208:215], v[178:185], v[18:21]
	s_setprio 0
	s_add_i32 s71, s71, 2
	s_add_u32 s6, s6, 0x100
	s_addc_u32 s7, s7, 0
	s_add_u32 s69, s69, 0x100
	s_addc_u32 s70, s70, 0
	s_cmp_gt_u32 s71, 5
	s_barrier
	s_cbranch_scc0 .LBB0_1925
	v_readlane_b32 s21, v252, 52
	v_readlane_b32 s6, v252, 51
	s_nop 15
	s_nop 15
	v_mbcnt_lo_u32_b32 v0, -1, 0
	v_mbcnt_hi_u32_b32 v0, -1, v0
	s_lshl_b32 s42, s6, 6
	s_lshl_b32 s6, s65, 8
	s_ashr_i32 s7, s6, 31
	s_lshl_b32 s40, s21, 5
	s_lshl_b32 s15, s66, 8
	s_ashr_i32 s41, s40, 31
	s_lshl_b64 s[66:67], s[6:7], 1
	s_add_u32 s21, s10, s66
	s_addc_u32 s43, s11, s67
	s_lshl_b64 s[68:69], s[40:41], 1
	s_add_u32 s70, s21, s68
	s_addc_u32 s71, s43, s69
	s_add_u32 s21, s56, s66
	v_and_b32_e32 v249, 15, v0
	v_lshrrev_b32_e32 v0, 1, v0
	s_addc_u32 s43, s57, s67
	v_and_b32_e32 v217, 24, v0
	s_add_u32 s66, s21, s68
	v_lshlrev_b32_e32 v0, 1, v217
	s_addc_u32 s67, s43, s69
	v_or_b32_e32 v2, s15, v249
	v_lshl_add_u64 v[210:211], s[70:71], 0, v[0:1]
	v_lshl_add_u64 v[212:213], s[66:67], 0, v[0:1]
	v_or_b32_e32 v0, s42, v249
	v_add_u32_e32 v2, s42, v2
	v_add_u32_e32 v216, s15, v0
	v_ashrrev_i32_e32 v3, 31, v2
	v_or_b32_e32 v214, 32, v216
	v_lshlrev_b64 v[4:5], 11, v[2:3]
	v_ashrrev_i32_e32 v215, 31, v214
	v_lshl_add_u64 v[6:7], v[210:211], 0, v[4:5]
	v_lshl_add_u64 v[4:5], v[212:213], 0, v[4:5]
	v_lshlrev_b64 v[8:9], 11, v[214:215]
	global_load_dwordx4 v[188:191], v[6:7], off
	global_load_dwordx4 v[192:195], v[4:5], off
	v_lshl_add_u64 v[10:11], v[210:211], 0, v[8:9]
	v_lshl_add_u64 v[8:9], v[212:213], 0, v[8:9]
	global_load_dwordx4 v[182:185], v[6:7], off offset:256
	global_load_dwordx4 v[178:181], v[4:5], off offset:256
	global_load_dwordx4 v[166:169], v[10:11], off
	global_load_dwordx4 v[158:161], v[10:11], off offset:256
	global_load_dwordx4 v[162:165], v[8:9], off
	global_load_dwordx4 v[154:157], v[8:9], off offset:256
	v_or_b32_e32 v2, 16, v2
	v_or_b32_e32 v6, 48, v216
	v_ashrrev_i32_e32 v3, 31, v2
	v_ashrrev_i32_e32 v7, 31, v6
	v_lshlrev_b64 v[2:3], 11, v[2:3]
	v_lshlrev_b64 v[6:7], 11, v[6:7]
	v_lshl_add_u64 v[4:5], v[210:211], 0, v[2:3]
	v_lshl_add_u64 v[2:3], v[212:213], 0, v[2:3]
	v_lshl_add_u64 v[8:9], v[210:211], 0, v[6:7]
	v_lshl_add_u64 v[208:209], v[212:213], 0, v[6:7]
	global_load_dwordx4 v[174:177], v[4:5], off
	global_load_dwordx4 v[14:17], v[4:5], off offset:256
	global_load_dwordx4 v[170:173], v[2:3], off
	global_load_dwordx4 v[10:13], v[2:3], off offset:256
	global_load_dwordx4 v[150:153], v[8:9], off
	s_nop 0
	global_load_dwordx4 v[6:9], v[8:9], off offset:256
	s_nop 0
	global_load_dwordx4 v[146:149], v[208:209], off
	global_load_dwordx4 v[2:5], v[208:209], off offset:256
	v_pk_mul_f32 v[144:145], v[144:145], s[18:19] op_sel_hi:[1,0]
	v_pk_mul_f32 v[142:143], v[142:143], s[18:19] op_sel_hi:[1,0]
	v_pk_mul_f32 v[140:141], v[140:141], s[18:19] op_sel_hi:[1,0]
	v_pk_mul_f32 v[138:139], v[138:139], s[18:19] op_sel_hi:[1,0]
	v_exp_f32_e32 v142, v142
	v_exp_f32_e32 v138, v138
	v_exp_f32_e32 v143, v143
	v_exp_f32_e32 v139, v139
	v_exp_f32_e32 v144, v144
	v_exp_f32_e32 v145, v145
	v_exp_f32_e32 v140, v140
	v_exp_f32_e32 v141, v141
	v_pk_add_f32 v[142:143], v[142:143], 1.0 op_sel_hi:[1,0]
	v_pk_add_f32 v[144:145], v[144:145], 1.0 op_sel_hi:[1,0]
	v_pk_add_f32 v[138:139], v[138:139], 1.0 op_sel_hi:[1,0]
	v_pk_add_f32 v[140:141], v[140:141], 1.0 op_sel_hi:[1,0]
	v_rcp_f32_e32 v142, v142
	v_rcp_f32_e32 v230, v138
	v_rcp_f32_e32 v143, v143
	v_rcp_f32_e32 v231, v139
	v_rcp_f32_e32 v138, v144
	v_rcp_f32_e32 v139, v145
	v_rcp_f32_e32 v144, v140
	v_rcp_f32_e32 v145, v141
	v_or_b32_e32 v208, s40, v217
	v_mov_b32_e32 v209, s41
	v_ashrrev_i32_e32 v217, 31, v216
	v_lshl_add_u64 v[208:209], v[208:209], 0, s[6:7]
	v_lshlrev_b64 v[216:217], 10, v[216:217]
	v_lshl_add_u64 v[220:221], v[216:217], 0, v[208:209]
	s_and_b64 vcc, exec, s[12:13]
	s_waitcnt vmcnt(0)
	v_lshlrev_b32_e32 v218, 16, v188
	v_and_b32_e32 v219, 0xffff0000, v188
	v_lshlrev_b32_e32 v188, 16, v189
	v_and_b32_e32 v189, 0xffff0000, v189
	v_lshlrev_b32_e32 v226, 16, v190
	v_and_b32_e32 v227, 0xffff0000, v190
	v_lshlrev_b32_e32 v190, 16, v191
	v_and_b32_e32 v191, 0xffff0000, v191
	v_lshlrev_b32_e32 v250, 16, v192
	v_and_b32_e32 v251, 0xffff0000, v192
	v_lshlrev_b32_e32 v192, 16, v193
	v_and_b32_e32 v193, 0xffff0000, v193
	v_lshlrev_b32_e32 v224, 16, v194
	v_and_b32_e32 v225, 0xffff0000, v194
	v_lshlrev_b32_e32 v194, 16, v195
	v_and_b32_e32 v195, 0xffff0000, v195
	v_pk_fma_f32 v[140:141], v[138:139], v[192:193], v[188:189]
	v_pk_fma_f32 v[138:139], v[142:143], v[250:251], v[218:219]
	v_pk_fma_f32 v[144:145], v[144:145], v[194:195], v[190:191]
	v_pk_fma_f32 v[142:143], v[230:231], v[224:225], v[226:227]
	v_lshl_add_u64 v[218:219], v[220:221], 2, s[8:9]
	s_cbranch_vccz .LBB0_1973
	global_store_dwordx4 v[218:219], v[138:141], off
	global_store_dwordx4 v[218:219], v[142:145], off offset:16
	v_mov_b64_e32 v[250:251], v[186:187]
	s_cbranch_execnz .LBB0_1929
